# speedup vs baseline: 1.0175x; 1.0109x over previous
_Z5k_fftPKtPtPKDv2_f:
	s_load_dwordx2 s[6:7], s[0:1], 0x10
	s_load_dwordx2 s[8:9], s[0:1], 0x0
	v_and_b32_e32 v1, 0xf0, v0
	v_and_b32_e32 v18, 15, v0
	v_mul_u32_u24_e32 v1, v1, v18
	v_lshlrev_b32_e32 v1, 3, v1
	s_waitcnt lgkmcnt(0)
	global_load_dwordx2 v[86:87], v1, s[6:7]
	s_lshr_b32 s4, s2, 3
	s_and_b32 s3, s2, 7
	s_and_b32 s4, s4, 0x1ffffff8
	s_or_b32 s4, s4, s3
	s_bfe_u32 s16, s2, 0x30003
	s_lshl_b32 s3, s4, 3
	s_or_b32 s3, s3, s16
	s_lshl_b32 s22, s3, 14
	s_add_u32 s22, s8, s22
	s_addc_u32 s23, s9, 0
	s_mov_b32 s11, 0
	s_lshr_b32 s10, s3, 1
	s_lshl_b64 s[10:11], s[10:11], 14
	s_add_u32 s3, s8, s10
	s_addc_u32 s8, s9, s11
	s_lshr_b32 s2, s2, 2
	s_and_b32 s2, s2, 2
	s_add_u32 s2, s3, s2
	v_mov_b32_e32 v3, 0
	v_lshlrev_b32_e32 v2, 2, v0
	s_addc_u32 s3, s8, 0
	s_movk_i32 s5, 0x1000
	v_lshl_add_u64 v[6:7], s[2:3], 0, v[2:3]
	v_add_co_u32_e32 v8, vcc, s5, v6
	s_movk_i32 s12, 0x2000
	s_nop 0
	v_addc_co_u32_e32 v9, vcc, 0, v7, vcc
	v_add_co_u32_e32 v10, vcc, s12, v6
	s_movk_i32 s13, 0x3000
	s_add_u32 s8, s2, 0x1000000
	v_addc_co_u32_e32 v11, vcc, 0, v7, vcc
	s_addc_u32 s9, s3, 0
	s_add_u32 s20, s2, 0x2000000
	s_addc_u32 s21, s3, 0
	v_add_co_u32_e32 v6, vcc, s13, v6
	v_lshl_add_u64 v[12:13], s[8:9], 0, v[2:3]
	s_nop 0
	v_addc_co_u32_e32 v7, vcc, 0, v7, vcc
	v_add_co_u32_e32 v14, vcc, s5, v12
	v_lshlrev_b32_e32 v1, 3, v0
	s_nop 0
	v_addc_co_u32_e32 v15, vcc, 0, v13, vcc
	v_add_co_u32_e32 v16, vcc, s12, v12
	v_or_b32_e32 v19, 0x1000, v2
	s_nop 0
	v_addc_co_u32_e32 v17, vcc, 0, v13, vcc
	v_add_co_u32_e32 v12, vcc, s13, v12
	v_or_b32_e32 v20, 0x2000, v2
	v_or_b32_e32 v21, 0x3000, v2
	v_addc_co_u32_e32 v13, vcc, 0, v13, vcc
	v_mul_u32_u24_e32 v3, 3, v0
	s_movk_i32 s5, 0x888
	v_lshlrev_b32_e32 v3, 3, v3
	s_mov_b32 s10, 0x3ec3ef15
	s_mov_b32 s11, 0xbf6c835e
	s_mov_b32 s14, s11
	s_mov_b32 s15, s10
	s_mov_b32 s12, 0xbf3504f3
	s_mov_b32 s13, s12
	v_mov_b32_e32 v88, v0
	global_load_dword v85, v2, s[22:23] nt
	global_load_dword v84, v2, s[22:23] offset:1024 nt
	global_load_dword v83, v2, s[22:23] offset:2048 nt
	global_load_dword v82, v2, s[22:23] offset:3072 nt
	global_load_dword v81, v19, s[22:23] nt
	global_load_dword v80, v19, s[22:23] offset:1024 nt
	global_load_dword v79, v19, s[22:23] offset:2048 nt
	global_load_dword v78, v19, s[22:23] offset:3072 nt
	global_load_dword v77, v20, s[22:23] nt
	global_load_dword v76, v20, s[22:23] offset:1024 nt
	global_load_dword v75, v20, s[22:23] offset:2048 nt
	global_load_dword v74, v20, s[22:23] offset:3072 nt
	global_load_dword v73, v21, s[22:23] nt
	global_load_dword v72, v21, s[22:23] offset:1024 nt
	global_load_dword v71, v21, s[22:23] offset:2048 nt
	global_load_dword v70, v21, s[22:23] offset:3072 nt
	v_mul_u32_u24_e32 v5, 5, v0
	v_mul_u32_u24_e32 v6, 6, v0
	v_mul_u32_u24_e32 v7, 7, v0
	v_mul_u32_u24_e32 v9, 9, v0
	v_mul_u32_u24_e32 v10, 10, v0
	v_lshrrev_b32_e32 v16, 1, v0
	v_lshlrev_b32_e32 v2, 4, v0
	v_lshlrev_b32_e32 v4, 5, v0
	v_lshlrev_b32_e32 v8, 6, v0
	v_mul_u32_u24_e32 v11, 11, v0
	v_mul_u32_u24_e32 v12, 12, v0
	v_mul_u32_u24_e32 v13, 13, v0
	v_mul_u32_u24_e32 v14, 14, v0
	v_mul_u32_u24_e32 v15, 15, v0
	v_lshlrev_b32_e32 v5, 3, v5
	v_lshlrev_b32_e32 v6, 3, v6
	v_lshlrev_b32_e32 v7, 3, v7
	v_lshlrev_b32_e32 v9, 3, v9
	v_lshlrev_b32_e32 v64, 3, v10
	v_and_b32_e32 v10, 0x78, v16
	v_lshlrev_b32_e32 v65, 3, v11
	v_lshlrev_b32_e32 v66, 3, v12
	v_lshlrev_b32_e32 v67, 3, v13
	v_lshlrev_b32_e32 v68, 3, v14
	v_lshlrev_b32_e32 v69, 3, v15
	v_mad_u32_u24 v96, v18, s5, v10
	global_load_dwordx2 v[30:31], v1, s[6:7]
	s_nop 0
	s_mov_b32 s6, 0x3f6c835e
	s_mov_b32 s7, 0xbec3ef15
	s_mov_b32 s8, 0x3f3504f3
	s_mov_b32 s9, s8
	s_waitcnt vmcnt(16)
	v_cvt_f32_fp8_e32 v32, v85
	s_waitcnt vmcnt(15)
	v_cvt_f32_fp8_sdwa v33, v85 src0_sel:BYTE_2
	s_waitcnt vmcnt(14)
	v_cvt_f32_fp8_e32 v34, v84
	v_cvt_f32_fp8_sdwa v35, v84 src0_sel:BYTE_2
	s_waitcnt vmcnt(13)
	s_waitcnt vmcnt(12)
	v_cvt_f32_fp8_e32 v40, v81
	s_waitcnt vmcnt(11)
	v_cvt_f32_fp8_sdwa v41, v81 src0_sel:BYTE_2
	s_waitcnt vmcnt(10)
	v_cvt_f32_fp8_e32 v42, v80
	v_cvt_f32_fp8_sdwa v43, v80 src0_sel:BYTE_2
	v_cvt_f32_fp8_e32 v36, v83
	v_cvt_f32_fp8_sdwa v37, v83 src0_sel:BYTE_2
	s_waitcnt vmcnt(9)
	v_cvt_f32_fp8_e32 v44, v79
	s_waitcnt vmcnt(8)
	v_cvt_f32_fp8_e32 v48, v77
	s_waitcnt vmcnt(7)
	v_cvt_f32_fp8_sdwa v49, v77 src0_sel:BYTE_2
	s_waitcnt vmcnt(6)
	v_cvt_f32_fp8_e32 v50, v76
	v_cvt_f32_fp8_sdwa v51, v76 src0_sel:BYTE_2
	s_waitcnt vmcnt(5)
	s_waitcnt vmcnt(4)
	v_cvt_f32_fp8_e32 v56, v73
	s_waitcnt vmcnt(3)
	v_cvt_f32_fp8_sdwa v57, v73 src0_sel:BYTE_2
	s_waitcnt vmcnt(2)
	v_cvt_f32_fp8_e32 v58, v72
	v_cvt_f32_fp8_sdwa v59, v72 src0_sel:BYTE_2
	v_cvt_f32_fp8_sdwa v45, v79 src0_sel:BYTE_2
	v_cvt_f32_fp8_e32 v52, v75
	v_cvt_f32_fp8_sdwa v53, v75 src0_sel:BYTE_2
	v_cvt_f32_fp8_e32 v60, v71
	v_cvt_f32_fp8_sdwa v61, v71 src0_sel:BYTE_2
	s_waitcnt vmcnt(1)
	v_cvt_f32_fp8_e32 v38, v82
	v_cvt_f32_fp8_sdwa v39, v82 src0_sel:BYTE_2
	v_cvt_f32_fp8_e32 v46, v78
	v_cvt_f32_fp8_sdwa v47, v78 src0_sel:BYTE_2
	v_cvt_f32_fp8_e32 v54, v74
	v_cvt_f32_fp8_sdwa v55, v74 src0_sel:BYTE_2
	v_cvt_f32_fp8_e32 v62, v70
	v_cvt_f32_fp8_sdwa v63, v70 src0_sel:BYTE_2
	v_pk_add_f32 v[64:65], v[32:33], v[48:49]
	v_pk_add_f32 v[32:33], v[32:33], v[48:49] neg_lo:[0,1] neg_hi:[0,1]
	v_pk_add_f32 v[48:49], v[40:41], v[56:57]
	v_pk_add_f32 v[40:41], v[40:41], v[56:57] neg_lo:[0,1] neg_hi:[0,1]
	v_pk_add_f32 v[56:57], v[64:65], v[48:49]
	v_pk_add_f32 v[48:49], v[64:65], v[48:49] neg_lo:[0,1] neg_hi:[0,1]
	v_pk_add_f32 v[64:65], v[32:33], v[40:41] op_sel:[0,1] op_sel_hi:[1,0] neg_hi:[0,1]
	v_pk_add_f32 v[32:33], v[32:33], v[40:41] op_sel:[0,1] op_sel_hi:[1,0] neg_lo:[0,1]
	v_pk_add_f32 v[40:41], v[34:35], v[50:51]
	v_pk_add_f32 v[34:35], v[34:35], v[50:51] neg_lo:[0,1] neg_hi:[0,1]
	v_pk_add_f32 v[50:51], v[42:43], v[58:59]
	v_pk_add_f32 v[42:43], v[42:43], v[58:59] neg_lo:[0,1] neg_hi:[0,1]
	v_pk_add_f32 v[58:59], v[40:41], v[50:51]
	v_pk_add_f32 v[40:41], v[40:41], v[50:51] neg_lo:[0,1] neg_hi:[0,1]
	v_pk_add_f32 v[50:51], v[34:35], v[42:43] op_sel:[0,1] op_sel_hi:[1,0] neg_hi:[0,1]
	v_pk_add_f32 v[34:35], v[34:35], v[42:43] op_sel:[0,1] op_sel_hi:[1,0] neg_lo:[0,1]
	v_pk_add_f32 v[42:43], v[36:37], v[52:53]
	v_pk_add_f32 v[36:37], v[36:37], v[52:53] neg_lo:[0,1] neg_hi:[0,1]
	v_pk_add_f32 v[52:53], v[44:45], v[60:61]
	v_pk_add_f32 v[44:45], v[44:45], v[60:61] neg_lo:[0,1] neg_hi:[0,1]
	v_pk_add_f32 v[60:61], v[42:43], v[52:53]
	v_pk_add_f32 v[42:43], v[42:43], v[52:53] neg_lo:[0,1] neg_hi:[0,1]
	v_pk_add_f32 v[52:53], v[36:37], v[44:45] op_sel:[0,1] op_sel_hi:[1,0] neg_hi:[0,1]
	v_pk_add_f32 v[36:37], v[36:37], v[44:45] op_sel:[0,1] op_sel_hi:[1,0] neg_lo:[0,1]
	v_pk_add_f32 v[44:45], v[38:39], v[54:55]
	v_pk_add_f32 v[38:39], v[38:39], v[54:55] neg_lo:[0,1] neg_hi:[0,1]
	v_pk_add_f32 v[54:55], v[46:47], v[62:63]
	v_pk_add_f32 v[46:47], v[46:47], v[62:63] neg_lo:[0,1] neg_hi:[0,1]
	v_pk_add_f32 v[62:63], v[44:45], v[54:55]
	v_pk_add_f32 v[44:45], v[44:45], v[54:55] neg_lo:[0,1] neg_hi:[0,1]
	v_pk_add_f32 v[54:55], v[38:39], v[46:47] op_sel:[0,1] op_sel_hi:[1,0] neg_hi:[0,1]
	v_pk_add_f32 v[38:39], v[38:39], v[46:47] op_sel:[0,1] op_sel_hi:[1,0] neg_lo:[0,1]
	v_pk_mul_f32 v[46:47], v[50:51], s[6:7] op_sel:[0,0] op_sel_hi:[0,1]
	v_pk_fma_f32 v[46:47], v[50:51], s[6:7], v[46:47] op_sel:[1,1,0] op_sel_hi:[1,0,1] neg_lo:[0,1,0]
	v_pk_mul_f32 v[50:51], v[34:35], s[10:11] op_sel:[0,0] op_sel_hi:[0,1]
	v_pk_fma_f32 v[50:51], v[34:35], s[10:11], v[50:51] op_sel:[1,1,0] op_sel_hi:[1,0,1] neg_lo:[0,1,0]
	v_pk_add_f32 v[34:35], v[52:53], v[52:53] op_sel:[0,1] op_sel_hi:[1,0] neg_hi:[0,1]
	v_pk_add_f32 v[40:41], v[40:41], v[40:41] op_sel:[0,1] op_sel_hi:[1,0] neg_hi:[0,1]
	s_nop 0
	v_pk_mul_f32 v[52:53], v[54:55], s[10:11] op_sel:[0,0] op_sel_hi:[0,1]
	v_pk_fma_f32 v[52:53], v[54:55], s[10:11], v[52:53] op_sel:[1,1,0] op_sel_hi:[1,0,1] neg_lo:[0,1,0]
	v_pk_mul_f32 v[54:55], v[38:39], s[14:15] op_sel:[0,0] op_sel_hi:[0,1]
	v_pk_fma_f32 v[54:55], v[38:39], s[14:15], v[54:55] op_sel:[1,1,0] op_sel_hi:[1,0,1] neg_lo:[0,1,0]
	v_pk_add_f32 v[38:39], v[56:57], v[60:61]
	v_pk_mul_f32 v[34:35], v[34:35], s[8:9]
	v_pk_add_f32 v[56:57], v[56:57], v[60:61] neg_lo:[0,1] neg_hi:[0,1]
	v_pk_add_f32 v[60:61], v[58:59], v[62:63]
	v_pk_add_f32 v[58:59], v[58:59], v[62:63] neg_lo:[0,1] neg_hi:[0,1]
	v_pk_mul_f32 v[40:41], v[40:41], s[8:9]
	v_pk_add_f32 v[36:37], v[36:37], v[36:37] op_sel:[0,1] op_sel_hi:[1,0] neg_lo:[0,1]
	v_pk_add_f32 v[44:45], v[44:45], v[44:45] op_sel:[0,1] op_sel_hi:[1,0] neg_lo:[0,1]
	v_pk_add_f32 v[62:63], v[38:39], v[60:61]
	v_pk_add_f32 v[38:39], v[38:39], v[60:61] neg_lo:[0,1] neg_hi:[0,1]
	v_pk_add_f32 v[60:61], v[56:57], v[58:59] op_sel:[0,1] op_sel_hi:[1,0] neg_hi:[0,1]
	v_pk_add_f32 v[56:57], v[56:57], v[58:59] op_sel:[0,1] op_sel_hi:[1,0] neg_lo:[0,1]
	v_pk_add_f32 v[58:59], v[64:65], v[34:35]
	v_pk_add_f32 v[34:35], v[64:65], v[34:35] neg_lo:[0,1] neg_hi:[0,1]
	v_pk_add_f32 v[64:65], v[46:47], v[52:53]
	v_pk_add_f32 v[46:47], v[46:47], v[52:53] neg_lo:[0,1] neg_hi:[0,1]
	v_pk_mul_f32 v[36:37], v[36:37], s[12:13]
	v_pk_mul_f32 v[44:45], v[44:45], s[12:13]
	v_pk_add_f32 v[52:53], v[58:59], v[64:65]
	v_pk_add_f32 v[58:59], v[58:59], v[64:65] neg_lo:[0,1] neg_hi:[0,1]
	v_pk_add_f32 v[64:65], v[34:35], v[46:47] op_sel:[0,1] op_sel_hi:[1,0] neg_hi:[0,1]
	v_pk_add_f32 v[34:35], v[34:35], v[46:47] op_sel:[0,1] op_sel_hi:[1,0] neg_lo:[0,1]
	v_pk_add_f32 v[46:47], v[48:49], v[42:43] op_sel:[0,1] op_sel_hi:[1,0] neg_hi:[0,1]
	v_pk_add_f32 v[42:43], v[48:49], v[42:43] op_sel:[0,1] op_sel_hi:[1,0] neg_lo:[0,1]
	v_pk_add_f32 v[48:49], v[40:41], v[44:45]
	v_pk_add_f32 v[40:41], v[40:41], v[44:45] neg_lo:[0,1] neg_hi:[0,1]
	v_pk_add_f32 v[44:45], v[48:49], v[46:47]
	v_pk_add_f32 v[46:47], v[46:47], v[48:49] neg_lo:[0,1] neg_hi:[0,1]
	v_pk_add_f32 v[48:49], v[42:43], v[40:41] op_sel:[0,1] op_sel_hi:[1,0] neg_hi:[0,1]
	v_pk_add_f32 v[40:41], v[42:43], v[40:41] op_sel:[0,1] op_sel_hi:[1,0] neg_lo:[0,1]
	v_pk_add_f32 v[42:43], v[32:33], v[36:37]
	v_pk_add_f32 v[32:33], v[32:33], v[36:37] neg_lo:[0,1] neg_hi:[0,1]
	v_pk_add_f32 v[36:37], v[50:51], v[54:55]
	v_pk_add_f32 v[50:51], v[50:51], v[54:55] neg_lo:[0,1] neg_hi:[0,1]
	v_pk_add_f32 v[54:55], v[42:43], v[36:37]
	v_pk_add_f32 v[36:37], v[42:43], v[36:37] neg_lo:[0,1] neg_hi:[0,1]
	v_pk_add_f32 v[42:43], v[32:33], v[50:51] op_sel:[0,1] op_sel_hi:[1,0] neg_hi:[0,1]
	v_pk_add_f32 v[32:33], v[32:33], v[50:51] op_sel:[0,1] op_sel_hi:[1,0] neg_lo:[0,1]
	s_waitcnt vmcnt(0)
	v_pk_mul_f32 v[28:29], v[30:31], v[30:31] op_sel:[0,0] op_sel_hi:[0,1]
	v_pk_fma_f32 v[28:29], v[30:31], v[30:31], v[28:29] op_sel:[1,1,0] op_sel_hi:[1,0,1] neg_lo:[0,1,0]
	v_pk_mul_f32 v[24:25], v[28:29], v[28:29] op_sel:[0,0] op_sel_hi:[0,1]
	v_pk_fma_f32 v[24:25], v[28:29], v[28:29], v[24:25] op_sel:[1,1,0] op_sel_hi:[1,0,1] neg_lo:[0,1,0]
	v_pk_mul_f32 v[22:23], v[24:25], v[24:25] op_sel:[0,0] op_sel_hi:[0,1]
	v_pk_fma_f32 v[22:23], v[24:25], v[24:25], v[22:23] op_sel:[1,1,0] op_sel_hi:[1,0,1] neg_lo:[0,1,0]
	v_pk_mul_f32 v[26:27], v[30:31], v[28:29] op_sel:[0,0] op_sel_hi:[0,1]
	v_pk_fma_f32 v[26:27], v[30:31], v[28:29], v[26:27] op_sel:[1,1,0] op_sel_hi:[1,0,1] neg_lo:[0,1,0]
	v_pk_mul_f32 v[20:21], v[30:31], v[24:25] op_sel:[0,0] op_sel_hi:[0,1]
	v_pk_fma_f32 v[20:21], v[30:31], v[24:25], v[20:21] op_sel:[1,1,0] op_sel_hi:[1,0,1] neg_lo:[0,1,0]
	v_pk_mul_f32 v[16:17], v[28:29], v[24:25] op_sel:[0,0] op_sel_hi:[0,1]
	v_pk_fma_f32 v[16:17], v[28:29], v[24:25], v[16:17] op_sel:[1,1,0] op_sel_hi:[1,0,1] neg_lo:[0,1,0]
	v_pk_mul_f32 v[18:19], v[30:31], v[22:23] op_sel:[0,0] op_sel_hi:[0,1]
	v_pk_fma_f32 v[18:19], v[30:31], v[22:23], v[18:19] op_sel:[1,1,0] op_sel_hi:[1,0,1] neg_lo:[0,1,0]
	v_pk_mul_f32 v[12:13], v[28:29], v[22:23] op_sel:[0,0] op_sel_hi:[0,1]
	v_pk_fma_f32 v[12:13], v[28:29], v[22:23], v[12:13] op_sel:[1,1,0] op_sel_hi:[1,0,1] neg_lo:[0,1,0]
	v_pk_mul_f32 v[6:7], v[24:25], v[22:23] op_sel:[0,0] op_sel_hi:[0,1]
	v_pk_fma_f32 v[6:7], v[24:25], v[22:23], v[6:7] op_sel:[1,1,0] op_sel_hi:[1,0,1] neg_lo:[0,1,0]
	v_pk_mul_f32 v[10:11], v[26:27], v[24:25] op_sel:[0,0] op_sel_hi:[0,1]
	v_pk_fma_f32 v[10:11], v[26:27], v[24:25], v[10:11] op_sel:[1,1,0] op_sel_hi:[1,0,1] neg_lo:[0,1,0]
	v_pk_mul_f32 v[14:15], v[26:27], v[22:23] op_sel:[0,0] op_sel_hi:[0,1]
	v_pk_fma_f32 v[14:15], v[26:27], v[22:23], v[14:15] op_sel:[1,1,0] op_sel_hi:[1,0,1] neg_lo:[0,1,0]
	v_pk_mul_f32 v[8:9], v[20:21], v[22:23] op_sel:[0,0] op_sel_hi:[0,1]
	v_pk_fma_f32 v[8:9], v[20:21], v[22:23], v[8:9] op_sel:[1,1,0] op_sel_hi:[1,0,1] neg_lo:[0,1,0]
	v_pk_mul_f32 v[4:5], v[16:17], v[22:23] op_sel:[0,0] op_sel_hi:[0,1]
	v_pk_fma_f32 v[4:5], v[16:17], v[22:23], v[4:5] op_sel:[1,1,0] op_sel_hi:[1,0,1] neg_lo:[0,1,0]
	v_pk_mul_f32 v[2:3], v[10:11], v[22:23] op_sel:[0,0] op_sel_hi:[0,1]
	v_pk_fma_f32 v[2:3], v[10:11], v[22:23], v[2:3] op_sel:[1,1,0] op_sel_hi:[1,0,1] neg_lo:[0,1,0]
	v_pk_mul_f32 v[50:51], v[52:53], v[30:31] op_sel:[0,0] op_sel_hi:[0,1]
	v_pk_fma_f32 v[50:51], v[52:53], v[30:31], v[50:51] op_sel:[1,1,0] op_sel_hi:[1,0,1] neg_lo:[0,1,0]
	ds_write_b64 v1, v[50:51] offset:2184
	v_pk_mul_f32 v[50:51], v[44:45], v[28:29] op_sel:[0,0] op_sel_hi:[0,1]
	v_pk_fma_f32 v[50:51], v[44:45], v[28:29], v[50:51] op_sel:[1,1,0] op_sel_hi:[1,0,1] neg_lo:[0,1,0]
	v_pk_mul_f32 v[44:45], v[54:55], v[26:27] op_sel:[0,0] op_sel_hi:[0,1]
	v_pk_fma_f32 v[44:45], v[54:55], v[26:27], v[44:45] op_sel:[1,1,0] op_sel_hi:[1,0,1] neg_lo:[0,1,0]
	ds_write_b64 v1, v[44:45] offset:6552
	v_pk_mul_f32 v[44:45], v[60:61], v[24:25] op_sel:[0,0] op_sel_hi:[0,1]
	v_pk_fma_f32 v[44:45], v[60:61], v[24:25], v[44:45] op_sel:[1,1,0] op_sel_hi:[1,0,1] neg_lo:[0,1,0]
	ds_write_b64 v1, v[44:45] offset:8736
	v_pk_mul_f32 v[44:45], v[64:65], v[20:21] op_sel:[0,0] op_sel_hi:[0,1]
	v_pk_fma_f32 v[44:45], v[64:65], v[20:21], v[44:45] op_sel:[1,1,0] op_sel_hi:[1,0,1] neg_lo:[0,1,0]
	ds_write_b64 v1, v[44:45] offset:10920
	v_pk_mul_f32 v[44:45], v[48:49], v[16:17] op_sel:[0,0] op_sel_hi:[0,1]
	v_pk_fma_f32 v[44:45], v[48:49], v[16:17], v[44:45] op_sel:[1,1,0] op_sel_hi:[1,0,1] neg_lo:[0,1,0]
	ds_write_b64 v1, v[44:45] offset:13104
	v_pk_mul_f32 v[44:45], v[42:43], v[10:11] op_sel:[0,0] op_sel_hi:[0,1]
	v_pk_fma_f32 v[44:45], v[42:43], v[10:11], v[44:45] op_sel:[1,1,0] op_sel_hi:[1,0,1] neg_lo:[0,1,0]
	v_pk_mul_f32 v[42:43], v[38:39], v[22:23] op_sel:[0,0] op_sel_hi:[0,1]
	v_pk_fma_f32 v[42:43], v[38:39], v[22:23], v[42:43] op_sel:[1,1,0] op_sel_hi:[1,0,1] neg_lo:[0,1,0]
	v_pk_mul_f32 v[38:39], v[58:59], v[18:19] op_sel:[0,0] op_sel_hi:[0,1]
	v_pk_fma_f32 v[38:39], v[58:59], v[18:19], v[38:39] op_sel:[1,1,0] op_sel_hi:[1,0,1] neg_lo:[0,1,0]
	ds_write_b64 v1, v[38:39] offset:19656
	v_pk_mul_f32 v[38:39], v[46:47], v[12:13] op_sel:[0,0] op_sel_hi:[0,1]
	v_pk_fma_f32 v[38:39], v[46:47], v[12:13], v[38:39] op_sel:[1,1,0] op_sel_hi:[1,0,1] neg_lo:[0,1,0]
	ds_write_b64 v1, v[38:39] offset:21840
	v_pk_mul_f32 v[38:39], v[36:37], v[14:15] op_sel:[0,0] op_sel_hi:[0,1]
	v_pk_fma_f32 v[38:39], v[36:37], v[14:15], v[38:39] op_sel:[1,1,0] op_sel_hi:[1,0,1] neg_lo:[0,1,0]
	v_pk_mul_f32 v[36:37], v[56:57], v[6:7] op_sel:[0,0] op_sel_hi:[0,1]
	v_pk_fma_f32 v[36:37], v[56:57], v[6:7], v[36:37] op_sel:[1,1,0] op_sel_hi:[1,0,1] neg_lo:[0,1,0]
	ds_write_b64 v1, v[36:37] offset:26208
	v_pk_mul_f32 v[36:37], v[34:35], v[8:9] op_sel:[0,0] op_sel_hi:[0,1]
	v_pk_fma_f32 v[36:37], v[34:35], v[8:9], v[36:37] op_sel:[1,1,0] op_sel_hi:[1,0,1] neg_lo:[0,1,0]
	v_pk_mul_f32 v[34:35], v[40:41], v[4:5] op_sel:[0,0] op_sel_hi:[0,1]
	v_pk_fma_f32 v[34:35], v[40:41], v[4:5], v[34:35] op_sel:[1,1,0] op_sel_hi:[1,0,1] neg_lo:[0,1,0]
	ds_write_b64 v1, v[34:35] offset:30576
	v_pk_mul_f32 v[34:35], v[32:33], v[2:3] op_sel:[0,0] op_sel_hi:[0,1]
	v_pk_fma_f32 v[34:35], v[32:33], v[2:3], v[34:35] op_sel:[1,1,0] op_sel_hi:[1,0,1] neg_lo:[0,1,0]
	ds_write_b64 v1, v[62:63]
	ds_write_b64 v1, v[50:51] offset:4368
	ds_write_b64 v1, v[44:45] offset:15288
	ds_write_b64 v1, v[42:43] offset:17472
	ds_write_b64 v1, v[38:39] offset:24024
	ds_write_b64 v1, v[36:37] offset:28392
	ds_write_b64 v1, v[34:35] offset:32760
	ds_write_b64 v1, v[86:87] offset:34816
	s_waitcnt lgkmcnt(0)
	s_barrier
	ds_read2_b64 v[32:35], v96 offset1:16
	ds_read2_b64 v[36:39], v96 offset0:32 offset1:48
	ds_read2_b64 v[40:43], v96 offset0:64 offset1:80
	ds_read2_b64 v[44:47], v96 offset0:128 offset1:144
	ds_read2_b64 v[48:51], v96 offset0:96 offset1:112
	ds_read2_b64 v[52:55], v96 offset0:192 offset1:208
	ds_read2_b64 v[56:59], v96 offset0:160 offset1:176
	ds_read2_b64 v[60:63], v96 offset0:224 offset1:240
	v_lshlrev_b32_e32 v115, 2, v0
	v_lshlrev_b32_e32 v119, 2, v0
	v_lshlrev_b32_e32 v123, 2, v0
	v_lshlrev_b32_e32 v127, 2, v0
	v_or_b32_e32 v119, 0x1000, v119
	v_or_b32_e32 v123, 0x2000, v123
	v_or_b32_e32 v127, 0x3000, v127
	global_load_ushort v112, v115, s[20:21]
	global_load_ushort v113, v115, s[20:21] offset:1024
	global_load_ushort v114, v115, s[20:21] offset:2048
	global_load_ushort v115, v115, s[20:21] offset:3072
	global_load_ushort v116, v119, s[20:21]
	global_load_ushort v117, v119, s[20:21] offset:1024
	global_load_ushort v118, v119, s[20:21] offset:2048
	global_load_ushort v119, v119, s[20:21] offset:3072
	global_load_ushort v120, v123, s[20:21]
	global_load_ushort v121, v123, s[20:21] offset:1024
	global_load_ushort v122, v123, s[20:21] offset:2048
	global_load_ushort v123, v123, s[20:21] offset:3072
	global_load_ushort v124, v127, s[20:21]
	global_load_ushort v125, v127, s[20:21] offset:1024
	global_load_ushort v126, v127, s[20:21] offset:2048
	global_load_ushort v127, v127, s[20:21] offset:3072
	s_waitcnt lgkmcnt(4)
	v_pk_add_f32 v[64:65], v[32:33], v[44:45]
	v_pk_add_f32 v[32:33], v[32:33], v[44:45] neg_lo:[0,1] neg_hi:[0,1]
	s_waitcnt lgkmcnt(2)
	v_pk_add_f32 v[44:45], v[40:41], v[52:53]
	v_pk_add_f32 v[40:41], v[40:41], v[52:53] neg_lo:[0,1] neg_hi:[0,1]
	v_pk_add_f32 v[52:53], v[64:65], v[44:45]
	v_pk_add_f32 v[44:45], v[64:65], v[44:45] neg_lo:[0,1] neg_hi:[0,1]
	v_pk_add_f32 v[64:65], v[32:33], v[40:41] op_sel:[0,1] op_sel_hi:[1,0] neg_hi:[0,1]
	v_pk_add_f32 v[32:33], v[32:33], v[40:41] op_sel:[0,1] op_sel_hi:[1,0] neg_lo:[0,1]
	v_pk_add_f32 v[40:41], v[34:35], v[46:47]
	v_pk_add_f32 v[34:35], v[34:35], v[46:47] neg_lo:[0,1] neg_hi:[0,1]
	v_pk_add_f32 v[46:47], v[42:43], v[54:55]
	v_pk_add_f32 v[42:43], v[42:43], v[54:55] neg_lo:[0,1] neg_hi:[0,1]
	v_pk_add_f32 v[54:55], v[40:41], v[46:47]
	v_pk_add_f32 v[40:41], v[40:41], v[46:47] neg_lo:[0,1] neg_hi:[0,1]
	v_pk_add_f32 v[46:47], v[34:35], v[42:43] op_sel:[0,1] op_sel_hi:[1,0] neg_hi:[0,1]
	v_pk_add_f32 v[34:35], v[34:35], v[42:43] op_sel:[0,1] op_sel_hi:[1,0] neg_lo:[0,1]
	s_waitcnt lgkmcnt(1)
	v_pk_add_f32 v[42:43], v[36:37], v[56:57]
	v_pk_add_f32 v[36:37], v[36:37], v[56:57] neg_lo:[0,1] neg_hi:[0,1]
	s_waitcnt lgkmcnt(0)
	v_pk_add_f32 v[56:57], v[48:49], v[60:61]
	v_pk_add_f32 v[48:49], v[48:49], v[60:61] neg_lo:[0,1] neg_hi:[0,1]
	v_pk_add_f32 v[60:61], v[42:43], v[56:57]
	v_pk_add_f32 v[42:43], v[42:43], v[56:57] neg_lo:[0,1] neg_hi:[0,1]
	v_pk_add_f32 v[56:57], v[36:37], v[48:49] op_sel:[0,1] op_sel_hi:[1,0] neg_hi:[0,1]
	v_pk_add_f32 v[36:37], v[36:37], v[48:49] op_sel:[0,1] op_sel_hi:[1,0] neg_lo:[0,1]
	v_pk_add_f32 v[48:49], v[38:39], v[58:59]
	v_pk_add_f32 v[38:39], v[38:39], v[58:59] neg_lo:[0,1] neg_hi:[0,1]
	v_pk_add_f32 v[58:59], v[50:51], v[62:63]
	v_pk_add_f32 v[50:51], v[50:51], v[62:63] neg_lo:[0,1] neg_hi:[0,1]
	v_pk_add_f32 v[62:63], v[48:49], v[58:59]
	v_pk_add_f32 v[48:49], v[48:49], v[58:59] neg_lo:[0,1] neg_hi:[0,1]
	v_pk_add_f32 v[58:59], v[38:39], v[50:51] op_sel:[0,1] op_sel_hi:[1,0] neg_hi:[0,1]
	v_pk_add_f32 v[38:39], v[38:39], v[50:51] op_sel:[0,1] op_sel_hi:[1,0] neg_lo:[0,1]
	v_pk_mul_f32 v[50:51], v[46:47], s[6:7] op_sel:[0,0] op_sel_hi:[0,1]
	v_pk_fma_f32 v[50:51], v[46:47], s[6:7], v[50:51] op_sel:[1,1,0] op_sel_hi:[1,0,1] neg_lo:[0,1,0]
	v_pk_mul_f32 v[46:47], v[34:35], s[10:11] op_sel:[0,0] op_sel_hi:[0,1]
	v_pk_fma_f32 v[46:47], v[34:35], s[10:11], v[46:47] op_sel:[1,1,0] op_sel_hi:[1,0,1] neg_lo:[0,1,0]
	v_pk_add_f32 v[34:35], v[56:57], v[56:57] op_sel:[0,1] op_sel_hi:[1,0] neg_hi:[0,1]
	v_pk_add_f32 v[40:41], v[40:41], v[40:41] op_sel:[0,1] op_sel_hi:[1,0] neg_hi:[0,1]
	s_nop 0
	v_pk_mul_f32 v[56:57], v[58:59], s[10:11] op_sel:[0,0] op_sel_hi:[0,1]
	v_pk_fma_f32 v[56:57], v[58:59], s[10:11], v[56:57] op_sel:[1,1,0] op_sel_hi:[1,0,1] neg_lo:[0,1,0]
	v_pk_mul_f32 v[58:59], v[38:39], s[14:15] op_sel:[0,0] op_sel_hi:[0,1]
	v_pk_fma_f32 v[58:59], v[38:39], s[14:15], v[58:59] op_sel:[1,1,0] op_sel_hi:[1,0,1] neg_lo:[0,1,0]
	v_pk_add_f32 v[38:39], v[52:53], v[60:61]
	v_pk_mul_f32 v[34:35], v[34:35], s[8:9]
	v_pk_add_f32 v[52:53], v[52:53], v[60:61] neg_lo:[0,1] neg_hi:[0,1]
	v_pk_add_f32 v[60:61], v[54:55], v[62:63]
	v_pk_add_f32 v[54:55], v[54:55], v[62:63] neg_lo:[0,1] neg_hi:[0,1]
	v_pk_add_f32 v[36:37], v[36:37], v[36:37] op_sel:[0,1] op_sel_hi:[1,0] neg_lo:[0,1]
	v_pk_add_f32 v[48:49], v[48:49], v[48:49] op_sel:[0,1] op_sel_hi:[1,0] neg_lo:[0,1]
	v_pk_add_f32 v[62:63], v[38:39], v[60:61]
	v_pk_add_f32 v[60:61], v[38:39], v[60:61] neg_lo:[0,1] neg_hi:[0,1]
	v_pk_add_f32 v[66:67], v[52:53], v[54:55] op_sel:[0,1] op_sel_hi:[1,0] neg_hi:[0,1]
	v_pk_add_f32 v[52:53], v[52:53], v[54:55] op_sel:[0,1] op_sel_hi:[1,0] neg_lo:[0,1]
	v_pk_add_f32 v[38:39], v[64:65], v[34:35]
	v_pk_add_f32 v[34:35], v[64:65], v[34:35] neg_lo:[0,1] neg_hi:[0,1]
	v_pk_add_f32 v[54:55], v[50:51], v[56:57]
	v_pk_add_f32 v[50:51], v[50:51], v[56:57] neg_lo:[0,1] neg_hi:[0,1]
	v_pk_mul_f32 v[40:41], v[40:41], s[8:9]
	v_pk_mul_f32 v[36:37], v[36:37], s[12:13]
	v_pk_mul_f32 v[48:49], v[48:49], s[12:13]
	v_pk_add_f32 v[56:57], v[38:39], v[54:55]
	v_pk_add_f32 v[54:55], v[38:39], v[54:55] neg_lo:[0,1] neg_hi:[0,1]
	v_pk_add_f32 v[64:65], v[34:35], v[50:51] op_sel:[0,1] op_sel_hi:[1,0] neg_hi:[0,1]
	v_pk_add_f32 v[50:51], v[34:35], v[50:51] op_sel:[0,1] op_sel_hi:[1,0] neg_lo:[0,1]
	v_pk_add_f32 v[34:35], v[44:45], v[42:43] op_sel:[0,1] op_sel_hi:[1,0] neg_hi:[0,1]
	v_pk_add_f32 v[38:39], v[44:45], v[42:43] op_sel:[0,1] op_sel_hi:[1,0] neg_lo:[0,1]
	v_pk_add_f32 v[42:43], v[40:41], v[48:49]
	v_pk_add_f32 v[40:41], v[40:41], v[48:49] neg_lo:[0,1] neg_hi:[0,1]
	v_pk_add_f32 v[44:45], v[42:43], v[34:35]
	v_pk_add_f32 v[42:43], v[34:35], v[42:43] neg_lo:[0,1] neg_hi:[0,1]
	v_pk_add_f32 v[34:35], v[32:33], v[36:37]
	v_pk_add_f32 v[36:37], v[32:33], v[36:37] neg_lo:[0,1] neg_hi:[0,1]
	v_pk_add_f32 v[32:33], v[46:47], v[58:59]
	v_pk_add_f32 v[48:49], v[38:39], v[40:41] op_sel:[0,1] op_sel_hi:[1,0] neg_hi:[0,1]
	v_pk_add_f32 v[40:41], v[38:39], v[40:41] op_sel:[0,1] op_sel_hi:[1,0] neg_lo:[0,1]
	v_pk_add_f32 v[38:39], v[46:47], v[58:59] neg_lo:[0,1] neg_hi:[0,1]
	v_pk_add_f32 v[46:47], v[34:35], v[32:33]
	v_pk_add_f32 v[58:59], v[34:35], v[32:33] neg_lo:[0,1] neg_hi:[0,1]
	v_pk_add_f32 v[68:69], v[36:37], v[38:39] op_sel:[0,1] op_sel_hi:[1,0] neg_hi:[0,1]
	v_pk_add_f32 v[86:87], v[36:37], v[38:39] op_sel:[0,1] op_sel_hi:[1,0] neg_lo:[0,1]
	s_nop 0
	v_ashrrev_i32_e32 v32, 4, v88
	v_lshlrev_b32_e32 v90, 3, v32
	v_add_u32_e32 v91, 0x8800, v90
	v_and_b32_e32 v36, 15, v88
	v_mad_u32_u24 v92, v36, s5, v90
	ds_read_b64 v[36:37], v91 offset:128
	s_waitcnt lgkmcnt(0)
	v_pk_mul_f32 v[88:89], v[56:57], v[36:37] op_sel:[0,0] op_sel_hi:[0,1]
	v_pk_fma_f32 v[88:89], v[56:57], v[36:37], v[88:89] op_sel:[1,1,0] op_sel_hi:[1,0,1] neg_lo:[0,1,0]
	v_pk_mul_f32 v[32:33], v[36:37], v[36:37] op_sel:[0,0] op_sel_hi:[0,1]
	v_pk_fma_f32 v[32:33], v[36:37], v[36:37], v[32:33] op_sel:[1,1,0] op_sel_hi:[1,0,1] neg_lo:[0,1,0]
	v_pk_mul_f32 v[56:57], v[44:45], v[32:33] op_sel:[0,0] op_sel_hi:[0,1]
	v_pk_fma_f32 v[56:57], v[44:45], v[32:33], v[56:57] op_sel:[1,1,0] op_sel_hi:[1,0,1] neg_lo:[0,1,0]
	v_pk_mul_f32 v[34:35], v[32:33], v[36:37] op_sel:[0,0] op_sel_hi:[0,1]
	v_pk_fma_f32 v[34:35], v[32:33], v[36:37], v[34:35] op_sel:[1,1,0] op_sel_hi:[1,0,1] neg_lo:[0,1,0]
	v_pk_mul_f32 v[44:45], v[46:47], v[34:35] op_sel:[0,0] op_sel_hi:[0,1]
	v_pk_fma_f32 v[44:45], v[46:47], v[34:35], v[44:45] op_sel:[1,1,0] op_sel_hi:[1,0,1] neg_lo:[0,1,0]
	ds_write2_b64 v92, v[56:57], v[44:45] offset0:32 offset1:48
	v_pk_mul_f32 v[32:33], v[34:35], v[36:37] op_sel:[0,0] op_sel_hi:[0,1]
	v_pk_fma_f32 v[32:33], v[34:35], v[36:37], v[32:33] op_sel:[1,1,0] op_sel_hi:[1,0,1] neg_lo:[0,1,0]
	v_pk_mul_f32 v[44:45], v[66:67], v[32:33] op_sel:[0,0] op_sel_hi:[0,1]
	v_pk_fma_f32 v[44:45], v[66:67], v[32:33], v[44:45] op_sel:[1,1,0] op_sel_hi:[1,0,1] neg_lo:[0,1,0]
	v_pk_mul_f32 v[34:35], v[32:33], v[36:37] op_sel:[0,0] op_sel_hi:[0,1]
	v_pk_fma_f32 v[34:35], v[32:33], v[36:37], v[34:35] op_sel:[1,1,0] op_sel_hi:[1,0,1] neg_lo:[0,1,0]
	v_pk_mul_f32 v[46:47], v[64:65], v[34:35] op_sel:[0,0] op_sel_hi:[0,1]
	v_pk_fma_f32 v[46:47], v[64:65], v[34:35], v[46:47] op_sel:[1,1,0] op_sel_hi:[1,0,1] neg_lo:[0,1,0]
	ds_write2_b64 v92, v[44:45], v[46:47] offset0:64 offset1:80
	v_pk_mul_f32 v[32:33], v[34:35], v[36:37] op_sel:[0,0] op_sel_hi:[0,1]
	v_pk_fma_f32 v[32:33], v[34:35], v[36:37], v[32:33] op_sel:[1,1,0] op_sel_hi:[1,0,1] neg_lo:[0,1,0]
	v_pk_mul_f32 v[44:45], v[48:49], v[32:33] op_sel:[0,0] op_sel_hi:[0,1]
	v_pk_fma_f32 v[44:45], v[48:49], v[32:33], v[44:45] op_sel:[1,1,0] op_sel_hi:[1,0,1] neg_lo:[0,1,0]
	v_pk_mul_f32 v[34:35], v[32:33], v[36:37] op_sel:[0,0] op_sel_hi:[0,1]
	v_pk_fma_f32 v[34:35], v[32:33], v[36:37], v[34:35] op_sel:[1,1,0] op_sel_hi:[1,0,1] neg_lo:[0,1,0]
	v_pk_mul_f32 v[46:47], v[68:69], v[34:35] op_sel:[0,0] op_sel_hi:[0,1]
	v_pk_fma_f32 v[46:47], v[68:69], v[34:35], v[46:47] op_sel:[1,1,0] op_sel_hi:[1,0,1] neg_lo:[0,1,0]
	ds_write2_b64 v92, v[44:45], v[46:47] offset0:96 offset1:112
	v_pk_mul_f32 v[32:33], v[34:35], v[36:37] op_sel:[0,0] op_sel_hi:[0,1]
	v_pk_fma_f32 v[32:33], v[34:35], v[36:37], v[32:33] op_sel:[1,1,0] op_sel_hi:[1,0,1] neg_lo:[0,1,0]
	v_pk_mul_f32 v[44:45], v[60:61], v[32:33] op_sel:[0,0] op_sel_hi:[0,1]
	v_pk_fma_f32 v[44:45], v[60:61], v[32:33], v[44:45] op_sel:[1,1,0] op_sel_hi:[1,0,1] neg_lo:[0,1,0]
	v_pk_mul_f32 v[34:35], v[32:33], v[36:37] op_sel:[0,0] op_sel_hi:[0,1]
	v_pk_fma_f32 v[34:35], v[32:33], v[36:37], v[34:35] op_sel:[1,1,0] op_sel_hi:[1,0,1] neg_lo:[0,1,0]
	v_pk_mul_f32 v[46:47], v[54:55], v[34:35] op_sel:[0,0] op_sel_hi:[0,1]
	v_pk_fma_f32 v[46:47], v[54:55], v[34:35], v[46:47] op_sel:[1,1,0] op_sel_hi:[1,0,1] neg_lo:[0,1,0]
	ds_write2_b64 v92, v[44:45], v[46:47] offset0:128 offset1:144
	v_pk_mul_f32 v[32:33], v[34:35], v[36:37] op_sel:[0,0] op_sel_hi:[0,1]
	v_pk_fma_f32 v[32:33], v[34:35], v[36:37], v[32:33] op_sel:[1,1,0] op_sel_hi:[1,0,1] neg_lo:[0,1,0]
	v_pk_mul_f32 v[44:45], v[42:43], v[32:33] op_sel:[0,0] op_sel_hi:[0,1]
	v_pk_fma_f32 v[44:45], v[42:43], v[32:33], v[44:45] op_sel:[1,1,0] op_sel_hi:[1,0,1] neg_lo:[0,1,0]
	v_pk_mul_f32 v[34:35], v[32:33], v[36:37] op_sel:[0,0] op_sel_hi:[0,1]
	v_pk_fma_f32 v[34:35], v[32:33], v[36:37], v[34:35] op_sel:[1,1,0] op_sel_hi:[1,0,1] neg_lo:[0,1,0]
	v_pk_mul_f32 v[42:43], v[58:59], v[34:35] op_sel:[0,0] op_sel_hi:[0,1]
	v_pk_fma_f32 v[42:43], v[58:59], v[34:35], v[42:43] op_sel:[1,1,0] op_sel_hi:[1,0,1] neg_lo:[0,1,0]
	ds_write2_b64 v92, v[44:45], v[42:43] offset0:160 offset1:176
	v_pk_mul_f32 v[32:33], v[34:35], v[36:37] op_sel:[0,0] op_sel_hi:[0,1]
	v_pk_fma_f32 v[32:33], v[34:35], v[36:37], v[32:33] op_sel:[1,1,0] op_sel_hi:[1,0,1] neg_lo:[0,1,0]
	v_pk_mul_f32 v[42:43], v[52:53], v[32:33] op_sel:[0,0] op_sel_hi:[0,1]
	v_pk_fma_f32 v[42:43], v[52:53], v[32:33], v[42:43] op_sel:[1,1,0] op_sel_hi:[1,0,1] neg_lo:[0,1,0]
	v_pk_mul_f32 v[34:35], v[32:33], v[36:37] op_sel:[0,0] op_sel_hi:[0,1]
	v_pk_fma_f32 v[34:35], v[32:33], v[36:37], v[34:35] op_sel:[1,1,0] op_sel_hi:[1,0,1] neg_lo:[0,1,0]
	v_pk_mul_f32 v[38:39], v[50:51], v[34:35] op_sel:[0,0] op_sel_hi:[0,1]
	v_pk_fma_f32 v[38:39], v[50:51], v[34:35], v[38:39] op_sel:[1,1,0] op_sel_hi:[1,0,1] neg_lo:[0,1,0]
	v_pk_mul_f32 v[32:33], v[34:35], v[36:37] op_sel:[0,0] op_sel_hi:[0,1]
	v_pk_fma_f32 v[32:33], v[34:35], v[36:37], v[32:33] op_sel:[1,1,0] op_sel_hi:[1,0,1] neg_lo:[0,1,0]
	v_pk_mul_f32 v[46:47], v[40:41], v[32:33] op_sel:[0,0] op_sel_hi:[0,1]
	v_pk_fma_f32 v[46:47], v[40:41], v[32:33], v[46:47] op_sel:[1,1,0] op_sel_hi:[1,0,1] neg_lo:[0,1,0]
	v_pk_mul_f32 v[34:35], v[32:33], v[36:37] op_sel:[0,0] op_sel_hi:[0,1]
	v_pk_fma_f32 v[34:35], v[32:33], v[36:37], v[34:35] op_sel:[1,1,0] op_sel_hi:[1,0,1] neg_lo:[0,1,0]
	v_pk_mul_f32 v[44:45], v[86:87], v[34:35] op_sel:[0,0] op_sel_hi:[0,1]
	v_pk_fma_f32 v[44:45], v[86:87], v[34:35], v[44:45] op_sel:[1,1,0] op_sel_hi:[1,0,1] neg_lo:[0,1,0]
	ds_write2_b64 v92, v[46:47], v[44:45] offset0:224 offset1:240
	v_mov_b32_e32 v32, v0
	ds_write2_b64 v92, v[62:63], v[88:89] offset1:16
	ds_write2_b64 v92, v[42:43], v[38:39] offset0:192 offset1:208
	s_waitcnt lgkmcnt(0)
	s_barrier
	s_nop 0
	v_and_b32_e32 v33, 15, v32
	v_and_b32_e32 v32, 0x1ffffff0, v32
	v_lshlrev_b32_e32 v32, 3, v32
	v_mad_u32_u24 v60, v33, s5, v32
	ds_read2_b64 v[32:35], v60 offset1:1
	ds_read2_b64 v[36:39], v60 offset0:2 offset1:3
	ds_read2_b64 v[40:43], v60 offset0:8 offset1:9
	ds_read2_b64 v[44:47], v60 offset0:4 offset1:5
	ds_read2_b64 v[48:51], v60 offset0:6 offset1:7
	ds_read2_b64 v[52:55], v60 offset0:12 offset1:13
	ds_read2_b64 v[56:59], v60 offset0:10 offset1:11
	ds_read2_b64 v[60:63], v60 offset0:14 offset1:15
	s_waitcnt lgkmcnt(5)
	v_pk_add_f32 v[64:65], v[32:33], v[40:41]
	v_pk_add_f32 v[32:33], v[32:33], v[40:41] neg_lo:[0,1] neg_hi:[0,1]
	s_waitcnt lgkmcnt(2)
	v_pk_add_f32 v[40:41], v[44:45], v[52:53]
	v_pk_add_f32 v[44:45], v[44:45], v[52:53] neg_lo:[0,1] neg_hi:[0,1]
	v_pk_add_f32 v[52:53], v[64:65], v[40:41]
	v_pk_add_f32 v[40:41], v[64:65], v[40:41] neg_lo:[0,1] neg_hi:[0,1]
	v_pk_add_f32 v[64:65], v[32:33], v[44:45] op_sel:[0,1] op_sel_hi:[1,0] neg_hi:[0,1]
	v_pk_add_f32 v[66:67], v[32:33], v[44:45] op_sel:[0,1] op_sel_hi:[1,0] neg_lo:[0,1]
	v_pk_add_f32 v[32:33], v[34:35], v[42:43]
	v_pk_add_f32 v[34:35], v[34:35], v[42:43] neg_lo:[0,1] neg_hi:[0,1]
	v_pk_add_f32 v[42:43], v[46:47], v[54:55]
	v_pk_add_f32 v[44:45], v[46:47], v[54:55] neg_lo:[0,1] neg_hi:[0,1]
	v_pk_add_f32 v[46:47], v[32:33], v[42:43]
	v_pk_add_f32 v[32:33], v[32:33], v[42:43] neg_lo:[0,1] neg_hi:[0,1]
	v_pk_add_f32 v[42:43], v[34:35], v[44:45] op_sel:[0,1] op_sel_hi:[1,0] neg_hi:[0,1]
	v_pk_add_f32 v[34:35], v[34:35], v[44:45] op_sel:[0,1] op_sel_hi:[1,0] neg_lo:[0,1]
	s_waitcnt lgkmcnt(1)
	v_pk_add_f32 v[44:45], v[36:37], v[56:57]
	s_waitcnt lgkmcnt(0)
	v_pk_add_f32 v[54:55], v[48:49], v[60:61]
	v_pk_add_f32 v[32:33], v[32:33], v[32:33] op_sel:[0,1] op_sel_hi:[1,0] neg_hi:[0,1]
	v_pk_add_f32 v[36:37], v[36:37], v[56:57] neg_lo:[0,1] neg_hi:[0,1]
	v_pk_add_f32 v[48:49], v[48:49], v[60:61] neg_lo:[0,1] neg_hi:[0,1]
	v_pk_add_f32 v[56:57], v[44:45], v[54:55]
	v_pk_add_f32 v[54:55], v[44:45], v[54:55] neg_lo:[0,1] neg_hi:[0,1]
	v_pk_add_f32 v[44:45], v[36:37], v[48:49] op_sel:[0,1] op_sel_hi:[1,0] neg_hi:[0,1]
	v_pk_mul_f32 v[68:69], v[32:33], s[8:9]
	v_pk_add_f32 v[36:37], v[36:37], v[48:49] op_sel:[0,1] op_sel_hi:[1,0] neg_lo:[0,1]
	v_pk_add_f32 v[48:49], v[38:39], v[58:59]
	v_pk_add_f32 v[32:33], v[44:45], v[44:45] op_sel:[0,1] op_sel_hi:[1,0] neg_hi:[0,1]
	v_pk_add_f32 v[38:39], v[38:39], v[58:59] neg_lo:[0,1] neg_hi:[0,1]
	v_pk_add_f32 v[58:59], v[50:51], v[62:63]
	v_pk_mul_f32 v[86:87], v[34:35], s[10:11] op_sel:[0,0] op_sel_hi:[0,1]
	v_pk_fma_f32 v[86:87], v[34:35], s[10:11], v[86:87] op_sel:[1,1,0] op_sel_hi:[1,0,1] neg_lo:[0,1,0]
	v_pk_mul_f32 v[34:35], v[32:33], s[8:9]
	v_pk_add_f32 v[32:33], v[36:37], v[36:37] op_sel:[0,1] op_sel_hi:[1,0] neg_lo:[0,1]
	v_pk_add_f32 v[50:51], v[50:51], v[62:63] neg_lo:[0,1] neg_hi:[0,1]
	v_pk_add_f32 v[60:61], v[48:49], v[58:59]
	v_pk_add_f32 v[48:49], v[48:49], v[58:59] neg_lo:[0,1] neg_hi:[0,1]
	v_pk_add_f32 v[58:59], v[38:39], v[50:51] op_sel:[0,1] op_sel_hi:[1,0] neg_hi:[0,1]
	v_pk_add_f32 v[38:39], v[38:39], v[50:51] op_sel:[0,1] op_sel_hi:[1,0] neg_lo:[0,1]
	v_pk_mul_f32 v[88:89], v[32:33], s[12:13]
	v_pk_add_f32 v[36:37], v[46:47], v[60:61]
	v_pk_add_f32 v[32:33], v[48:49], v[48:49] op_sel:[0,1] op_sel_hi:[1,0] neg_lo:[0,1]
	v_pk_mul_f32 v[44:45], v[58:59], s[10:11] op_sel:[0,0] op_sel_hi:[0,1]
	v_pk_fma_f32 v[44:45], v[58:59], s[10:11], v[44:45] op_sel:[1,1,0] op_sel_hi:[1,0,1] neg_lo:[0,1,0]
	v_pk_mul_f32 v[58:59], v[38:39], s[14:15] op_sel:[0,0] op_sel_hi:[0,1]
	v_pk_fma_f32 v[58:59], v[38:39], s[14:15], v[58:59] op_sel:[1,1,0] op_sel_hi:[1,0,1] neg_lo:[0,1,0]
	v_pk_add_f32 v[38:39], v[52:53], v[56:57] neg_lo:[0,1] neg_hi:[0,1]
	v_pk_mul_f32 v[48:49], v[32:33], s[12:13]
	v_pk_add_f32 v[32:33], v[52:53], v[56:57]
	v_pk_add_f32 v[46:47], v[46:47], v[60:61] neg_lo:[0,1] neg_hi:[0,1]
	v_pk_mul_f32 v[62:63], v[42:43], s[6:7] op_sel:[0,0] op_sel_hi:[0,1]
	v_pk_fma_f32 v[62:63], v[42:43], s[6:7], v[62:63] op_sel:[1,1,0] op_sel_hi:[1,0,1] neg_lo:[0,1,0]
	v_pk_add_f32 v[50:51], v[32:33], v[36:37]
	v_pk_add_f32 v[36:37], v[32:33], v[36:37] neg_lo:[0,1] neg_hi:[0,1]
	v_pk_add_f32 v[42:43], v[38:39], v[46:47] op_sel:[0,1] op_sel_hi:[1,0] neg_hi:[0,1]
	v_pk_add_f32 v[32:33], v[38:39], v[46:47] op_sel:[0,1] op_sel_hi:[1,0] neg_lo:[0,1]
	v_pk_add_f32 v[38:39], v[64:65], v[34:35]
	v_pk_add_f32 v[34:35], v[64:65], v[34:35] neg_lo:[0,1] neg_hi:[0,1]
	v_pk_add_f32 v[46:47], v[62:63], v[44:45]
	v_pk_add_f32 v[56:57], v[62:63], v[44:45] neg_lo:[0,1] neg_hi:[0,1]
	v_pk_add_f32 v[52:53], v[38:39], v[46:47]
	v_pk_add_f32 v[38:39], v[38:39], v[46:47] neg_lo:[0,1] neg_hi:[0,1]
	v_pk_add_f32 v[44:45], v[34:35], v[56:57] op_sel:[0,1] op_sel_hi:[1,0] neg_hi:[0,1]
	v_pk_add_f32 v[34:35], v[34:35], v[56:57] op_sel:[0,1] op_sel_hi:[1,0] neg_lo:[0,1]
	v_pk_add_f32 v[46:47], v[40:41], v[54:55] op_sel:[0,1] op_sel_hi:[1,0] neg_hi:[0,1]
	v_pk_add_f32 v[56:57], v[40:41], v[54:55] op_sel:[0,1] op_sel_hi:[1,0] neg_lo:[0,1]
	v_pk_add_f32 v[40:41], v[68:69], v[48:49]
	v_pk_add_f32 v[60:61], v[68:69], v[48:49] neg_lo:[0,1] neg_hi:[0,1]
	v_pk_add_f32 v[54:55], v[40:41], v[46:47]
	v_pk_add_f32 v[40:41], v[46:47], v[40:41] neg_lo:[0,1] neg_hi:[0,1]
	v_pk_add_f32 v[46:47], v[66:67], v[88:89]
	v_pk_add_f32 v[62:63], v[86:87], v[58:59]
	v_pk_add_f32 v[58:59], v[86:87], v[58:59] neg_lo:[0,1] neg_hi:[0,1]
	v_pk_add_f32 v[48:49], v[56:57], v[60:61] op_sel:[0,1] op_sel_hi:[1,0] neg_hi:[0,1]
	v_pk_add_f32 v[64:65], v[56:57], v[60:61] op_sel:[0,1] op_sel_hi:[1,0] neg_lo:[0,1]
	v_pk_add_f32 v[60:61], v[66:67], v[88:89] neg_lo:[0,1] neg_hi:[0,1]
	v_pk_add_f32 v[56:57], v[46:47], v[62:63]
	v_pk_add_f32 v[68:69], v[46:47], v[62:63] neg_lo:[0,1] neg_hi:[0,1]
	v_pk_add_f32 v[46:47], v[60:61], v[58:59] op_sel:[0,1] op_sel_hi:[1,0] neg_hi:[0,1]
	v_pk_add_f32 v[66:67], v[60:61], v[58:59] op_sel:[0,1] op_sel_hi:[1,0] neg_lo:[0,1]
	v_mov_b32_e32 v58, v0
	s_nop 0
	v_and_b32_e32 v59, -16, v58
	v_and_b32_e32 v60, 15, v58
	v_lshlrev_b32_e32 v61, 3, v59
	v_mad_u32_u24 v61, v60, s5, v61
	v_cmp_ne_u32_e32 vcc, 0, v60
	ds_write2_b64 v61, v[50:51], v[52:53] offset1:1
	ds_write2_b64 v61, v[54:55], v[56:57] offset0:2 offset1:3
	ds_write2_b64 v61, v[42:43], v[44:45] offset0:4 offset1:5
	ds_write2_b64 v61, v[48:49], v[46:47] offset0:6 offset1:7
	ds_write2_b64 v61, v[36:37], v[38:39] offset0:8 offset1:9
	ds_write2_b64 v61, v[40:41], v[68:69] offset0:10 offset1:11
	ds_write2_b64 v61, v[32:33], v[34:35] offset0:12 offset1:13
	ds_write2_b64 v61, v[64:65], v[66:67] offset0:14 offset1:15
	s_waitcnt lgkmcnt(0)
	s_barrier
	s_and_saveexec_b64 s[6:7], vcc
	s_xor_b64 s[6:7], exec, s[6:7]
	v_sub_u32_e32 v60, 16, v60
	v_mul_u32_u24_e32 v60, 0x111, v60
	v_sub_u32_e32 v59, v60, v59
	v_add_u32_e32 v61, 0xf0, v59
	s_andn2_saveexec_b64 s[6:7], s[6:7]
	v_sub_u32_e32 v59, 0x100, v58
	v_cmp_lt_u32_e32 vcc, 15, v58
	s_nop 1
	v_cndmask_b32_e32 v61, 1, v59, vcc
	s_or_b64 exec, exec, s[6:7]
	v_mov_b32_e32 v59, 0
	v_lshlrev_b32_e32 v92, 3, v61
	ds_read_b64 v[90:91], v59
	ds_read2_b64 v[60:63], v92 offset0:14 offset1:15
	ds_read2_b64 v[86:89], v92 offset0:12 offset1:13
	v_cmp_eq_u32_e32 vcc, 0, v58
	v_cvt_f32_fp8_sdwa v93, v74 src0_sel:BYTE_3
	v_cvt_f32_fp8_sdwa v94, v72 src0_sel:BYTE_1
	s_waitcnt lgkmcnt(1)
	v_cndmask_b32_e32 v59, v63, v91, vcc
	v_cndmask_b32_e32 v58, v62, v90, vcc
	v_pk_add_f32 v[90:91], v[50:51], v[58:59] neg_hi:[0,1]
	v_pk_add_f32 v[50:51], v[50:51], v[58:59] neg_lo:[0,1]
	v_cvt_f32_fp8_sdwa v95, v72 src0_sel:BYTE_3
	v_pk_mul_f32 v[62:63], v[90:91], v[50:51] op_sel:[0,0] op_sel_hi:[0,1]
	v_pk_fma_f32 v[62:63], v[90:91], v[50:51], v[62:63] op_sel:[1,1,0] op_sel_hi:[1,0,1] neg_hi:[0,1,0]
	v_pk_add_f32 v[50:51], v[52:53], v[60:61] neg_hi:[0,1]
	v_pk_add_f32 v[52:53], v[52:53], v[60:61] neg_lo:[0,1]
	v_cvt_f32_fp8_sdwa v72, v71 src0_sel:BYTE_1
	v_pk_mul_f32 v[60:61], v[50:51], v[52:53] op_sel:[0,0] op_sel_hi:[0,1]
	v_pk_fma_f32 v[60:61], v[50:51], v[52:53], v[60:61] op_sel:[1,1,0] op_sel_hi:[1,0,1] neg_hi:[0,1,0]
	s_waitcnt lgkmcnt(0)
	v_pk_add_f32 v[50:51], v[54:55], v[88:89] neg_hi:[0,1]
	v_pk_add_f32 v[52:53], v[54:55], v[88:89] neg_lo:[0,1]
	v_pk_add_f32 v[54:55], v[56:57], v[86:87] neg_hi:[0,1]
	v_pk_add_f32 v[86:87], v[56:57], v[86:87] neg_lo:[0,1]
	v_cvt_f32_fp8_sdwa v98, v70 src0_sel:BYTE_1
	v_pk_mul_f32 v[58:59], v[50:51], v[52:53] op_sel:[0,0] op_sel_hi:[0,1]
	v_pk_fma_f32 v[58:59], v[50:51], v[52:53], v[58:59] op_sel:[1,1,0] op_sel_hi:[1,0,1] neg_hi:[0,1,0]
	ds_read2_b64 v[50:53], v92 offset0:10 offset1:11
	v_pk_mul_f32 v[56:57], v[54:55], v[86:87] op_sel:[0,0] op_sel_hi:[0,1]
	v_pk_fma_f32 v[56:57], v[54:55], v[86:87], v[56:57] op_sel:[1,1,0] op_sel_hi:[1,0,1] neg_hi:[0,1,0]
	ds_read2_b64 v[86:89], v92 offset0:8 offset1:9
	s_waitcnt lgkmcnt(1)
	v_pk_add_f32 v[90:91], v[42:43], v[52:53] neg_hi:[0,1]
	v_pk_add_f32 v[42:43], v[42:43], v[52:53] neg_lo:[0,1]
	v_cvt_f32_fp8_sdwa v99, v70 src0_sel:BYTE_3
	v_pk_mul_f32 v[54:55], v[90:91], v[42:43] op_sel:[0,0] op_sel_hi:[0,1]
	v_pk_fma_f32 v[54:55], v[90:91], v[42:43], v[54:55] op_sel:[1,1,0] op_sel_hi:[1,0,1] neg_hi:[0,1,0]
	v_pk_add_f32 v[42:43], v[44:45], v[50:51] neg_hi:[0,1]
	v_pk_add_f32 v[44:45], v[44:45], v[50:51] neg_lo:[0,1]
	s_mov_b32 s6, 0x3f6c835e
	v_pk_mul_f32 v[52:53], v[42:43], v[44:45] op_sel:[0,0] op_sel_hi:[0,1]
	v_pk_fma_f32 v[52:53], v[42:43], v[44:45], v[52:53] op_sel:[1,1,0] op_sel_hi:[1,0,1] neg_hi:[0,1,0]
	s_waitcnt lgkmcnt(0)
	v_pk_add_f32 v[42:43], v[48:49], v[88:89] neg_hi:[0,1]
	v_pk_add_f32 v[44:45], v[48:49], v[88:89] neg_lo:[0,1]
	v_pk_add_f32 v[88:89], v[46:47], v[86:87] neg_hi:[0,1]
	v_pk_add_f32 v[46:47], v[46:47], v[86:87] neg_lo:[0,1]
	s_mov_b32 s7, 0xbec3ef15
	v_pk_mul_f32 v[50:51], v[42:43], v[44:45] op_sel:[0,0] op_sel_hi:[0,1]
	v_pk_fma_f32 v[50:51], v[42:43], v[44:45], v[50:51] op_sel:[1,1,0] op_sel_hi:[1,0,1] neg_hi:[0,1,0]
	ds_read2_b64 v[42:45], v92 offset0:6 offset1:7
	v_pk_mul_f32 v[48:49], v[88:89], v[46:47] op_sel:[0,0] op_sel_hi:[0,1]
	v_pk_fma_f32 v[48:49], v[88:89], v[46:47], v[48:49] op_sel:[1,1,0] op_sel_hi:[1,0,1] neg_hi:[0,1,0]
	ds_read2_b64 v[86:89], v92 offset0:4 offset1:5
	s_waitcnt lgkmcnt(1)
	v_pk_add_f32 v[90:91], v[36:37], v[44:45] neg_hi:[0,1]
	v_pk_add_f32 v[36:37], v[36:37], v[44:45] neg_lo:[0,1]
	s_mov_b32 s9, s8
	v_pk_mul_f32 v[46:47], v[90:91], v[36:37] op_sel:[0,0] op_sel_hi:[0,1]
	v_pk_fma_f32 v[46:47], v[90:91], v[36:37], v[46:47] op_sel:[1,1,0] op_sel_hi:[1,0,1] neg_hi:[0,1,0]
	v_pk_add_f32 v[36:37], v[38:39], v[42:43] neg_hi:[0,1]
	v_pk_add_f32 v[38:39], v[38:39], v[42:43] neg_lo:[0,1]
	v_cvt_f32_fp8_sdwa v90, v76 src0_sel:BYTE_1
	v_pk_mul_f32 v[44:45], v[36:37], v[38:39] op_sel:[0,0] op_sel_hi:[0,1]
	v_pk_fma_f32 v[44:45], v[36:37], v[38:39], v[44:45] op_sel:[1,1,0] op_sel_hi:[1,0,1] neg_hi:[0,1,0]
	s_waitcnt lgkmcnt(0)
	v_pk_add_f32 v[36:37], v[40:41], v[88:89] neg_hi:[0,1]
	v_pk_add_f32 v[38:39], v[40:41], v[88:89] neg_lo:[0,1]
	v_pk_add_f32 v[88:89], v[68:69], v[86:87] neg_hi:[0,1]
	v_pk_add_f32 v[68:69], v[68:69], v[86:87] neg_lo:[0,1]
	v_cvt_f32_fp8_sdwa v91, v76 src0_sel:BYTE_3
	v_pk_mul_f32 v[42:43], v[36:37], v[38:39] op_sel:[0,0] op_sel_hi:[0,1]
	v_pk_fma_f32 v[42:43], v[36:37], v[38:39], v[42:43] op_sel:[1,1,0] op_sel_hi:[1,0,1] neg_hi:[0,1,0]
	ds_read2_b64 v[36:39], v92 offset0:2 offset1:3
	v_pk_mul_f32 v[40:41], v[88:89], v[68:69] op_sel:[0,0] op_sel_hi:[0,1]
	v_pk_fma_f32 v[40:41], v[88:89], v[68:69], v[40:41] op_sel:[1,1,0] op_sel_hi:[1,0,1] neg_hi:[0,1,0]
	ds_read2_b64 v[86:89], v92 offset1:1
	s_waitcnt lgkmcnt(1)
	v_pk_add_f32 v[68:69], v[32:33], v[38:39] neg_hi:[0,1]
	v_pk_add_f32 v[32:33], v[32:33], v[38:39] neg_lo:[0,1]
	v_cvt_f32_fp8_sdwa v76, v75 src0_sel:BYTE_1
	v_pk_mul_f32 v[38:39], v[68:69], v[32:33] op_sel:[0,0] op_sel_hi:[0,1]
	v_pk_fma_f32 v[38:39], v[68:69], v[32:33], v[38:39] op_sel:[1,1,0] op_sel_hi:[1,0,1] neg_hi:[0,1,0]
	v_pk_add_f32 v[32:33], v[34:35], v[36:37] neg_hi:[0,1]
	v_pk_add_f32 v[34:35], v[34:35], v[36:37] neg_lo:[0,1]
	v_cvt_f32_fp8_sdwa v68, v83 src0_sel:BYTE_1
	v_pk_mul_f32 v[36:37], v[32:33], v[34:35] op_sel:[0,0] op_sel_hi:[0,1]
	v_pk_fma_f32 v[36:37], v[32:33], v[34:35], v[36:37] op_sel:[1,1,0] op_sel_hi:[1,0,1] neg_hi:[0,1,0]
	s_waitcnt lgkmcnt(0)
	v_pk_add_f32 v[32:33], v[64:65], v[88:89] neg_hi:[0,1]
	v_pk_add_f32 v[64:65], v[64:65], v[88:89] neg_lo:[0,1]
	v_cvt_f32_fp8_sdwa v69, v83 src0_sel:BYTE_3
	v_pk_mul_f32 v[34:35], v[32:33], v[64:65] op_sel:[0,0] op_sel_hi:[0,1]
	v_pk_fma_f32 v[34:35], v[32:33], v[64:65], v[34:35] op_sel:[1,1,0] op_sel_hi:[1,0,1] neg_hi:[0,1,0]
	v_pk_add_f32 v[64:65], v[66:67], v[86:87] neg_hi:[0,1]
	v_pk_add_f32 v[66:67], v[66:67], v[86:87] neg_lo:[0,1]
	v_cvt_f32_fp8_sdwa v83, v81 src0_sel:BYTE_3
	v_pk_mul_f32 v[32:33], v[64:65], v[66:67] op_sel:[0,0] op_sel_hi:[0,1]
	v_pk_fma_f32 v[32:33], v[64:65], v[66:67], v[32:33] op_sel:[1,1,0] op_sel_hi:[1,0,1] neg_hi:[0,1,0]
	v_cvt_f32_fp8_sdwa v64, v85 src0_sel:BYTE_1
	v_cvt_f32_fp8_sdwa v65, v85 src0_sel:BYTE_3
	v_cvt_f32_fp8_sdwa v66, v84 src0_sel:BYTE_1
	v_cvt_f32_fp8_sdwa v67, v84 src0_sel:BYTE_3
	v_cvt_f32_fp8_sdwa v84, v82 src0_sel:BYTE_1
	v_cvt_f32_fp8_sdwa v85, v82 src0_sel:BYTE_3
	v_cvt_f32_fp8_sdwa v82, v81 src0_sel:BYTE_1
	v_cvt_f32_fp8_sdwa v86, v80 src0_sel:BYTE_1
	v_cvt_f32_fp8_sdwa v87, v80 src0_sel:BYTE_3
	v_cvt_f32_fp8_sdwa v80, v79 src0_sel:BYTE_1
	v_cvt_f32_fp8_sdwa v81, v79 src0_sel:BYTE_3
	v_cvt_f32_fp8_sdwa v88, v78 src0_sel:BYTE_1
	v_cvt_f32_fp8_sdwa v89, v78 src0_sel:BYTE_3
	v_cvt_f32_fp8_sdwa v78, v77 src0_sel:BYTE_1
	v_cvt_f32_fp8_sdwa v79, v77 src0_sel:BYTE_3
	v_cvt_f32_fp8_sdwa v77, v75 src0_sel:BYTE_3
	v_cvt_f32_fp8_sdwa v92, v74 src0_sel:BYTE_1
	v_cvt_f32_fp8_sdwa v74, v73 src0_sel:BYTE_1
	v_cvt_f32_fp8_sdwa v75, v73 src0_sel:BYTE_3
	v_cvt_f32_fp8_sdwa v73, v71 src0_sel:BYTE_3
	v_pk_add_f32 v[70:71], v[64:65], v[78:79]
	v_pk_add_f32 v[64:65], v[64:65], v[78:79] neg_lo:[0,1] neg_hi:[0,1]
	v_pk_add_f32 v[78:79], v[82:83], v[74:75]
	v_pk_add_f32 v[74:75], v[82:83], v[74:75] neg_lo:[0,1] neg_hi:[0,1]
	v_pk_add_f32 v[82:83], v[70:71], v[78:79]
	v_pk_add_f32 v[70:71], v[70:71], v[78:79] neg_lo:[0,1] neg_hi:[0,1]
	v_pk_add_f32 v[78:79], v[64:65], v[74:75] op_sel:[0,1] op_sel_hi:[1,0] neg_hi:[0,1]
	v_pk_add_f32 v[64:65], v[64:65], v[74:75] op_sel:[0,1] op_sel_hi:[1,0] neg_lo:[0,1]
	v_pk_add_f32 v[74:75], v[66:67], v[90:91]
	v_pk_add_f32 v[66:67], v[66:67], v[90:91] neg_lo:[0,1] neg_hi:[0,1]
	v_pk_add_f32 v[90:91], v[86:87], v[94:95]
	v_pk_add_f32 v[86:87], v[86:87], v[94:95] neg_lo:[0,1] neg_hi:[0,1]
	v_pk_add_f32 v[94:95], v[74:75], v[90:91]
	v_pk_add_f32 v[74:75], v[74:75], v[90:91] neg_lo:[0,1] neg_hi:[0,1]
	v_pk_add_f32 v[90:91], v[66:67], v[86:87] op_sel:[0,1] op_sel_hi:[1,0] neg_hi:[0,1]
	v_pk_add_f32 v[66:67], v[66:67], v[86:87] op_sel:[0,1] op_sel_hi:[1,0] neg_lo:[0,1]
	v_pk_add_f32 v[86:87], v[68:69], v[76:77]
	v_pk_add_f32 v[68:69], v[68:69], v[76:77] neg_lo:[0,1] neg_hi:[0,1]
	v_pk_add_f32 v[76:77], v[80:81], v[72:73]
	v_pk_add_f32 v[72:73], v[80:81], v[72:73] neg_lo:[0,1] neg_hi:[0,1]
	v_pk_add_f32 v[80:81], v[86:87], v[76:77]
	v_pk_add_f32 v[76:77], v[86:87], v[76:77] neg_lo:[0,1] neg_hi:[0,1]
	v_pk_add_f32 v[86:87], v[68:69], v[72:73] op_sel:[0,1] op_sel_hi:[1,0] neg_hi:[0,1]
	v_pk_add_f32 v[68:69], v[68:69], v[72:73] op_sel:[0,1] op_sel_hi:[1,0] neg_lo:[0,1]
	v_pk_add_f32 v[72:73], v[84:85], v[92:93]
	v_pk_add_f32 v[84:85], v[84:85], v[92:93] neg_lo:[0,1] neg_hi:[0,1]
	v_pk_add_f32 v[92:93], v[88:89], v[98:99]
	v_pk_add_f32 v[88:89], v[88:89], v[98:99] neg_lo:[0,1] neg_hi:[0,1]
	v_pk_add_f32 v[98:99], v[72:73], v[92:93]
	v_pk_add_f32 v[72:73], v[72:73], v[92:93] neg_lo:[0,1] neg_hi:[0,1]
	v_pk_add_f32 v[92:93], v[84:85], v[88:89] op_sel:[0,1] op_sel_hi:[1,0] neg_hi:[0,1]
	v_pk_add_f32 v[84:85], v[84:85], v[88:89] op_sel:[0,1] op_sel_hi:[1,0] neg_lo:[0,1]
	v_pk_mul_f32 v[88:89], v[90:91], s[6:7] op_sel:[0,0] op_sel_hi:[0,1]
	v_pk_fma_f32 v[88:89], v[90:91], s[6:7], v[88:89] op_sel:[1,1,0] op_sel_hi:[1,0,1] neg_lo:[0,1,0]
	v_pk_mul_f32 v[90:91], v[66:67], s[10:11] op_sel:[0,0] op_sel_hi:[0,1]
	v_pk_fma_f32 v[90:91], v[66:67], s[10:11], v[90:91] op_sel:[1,1,0] op_sel_hi:[1,0,1] neg_lo:[0,1,0]
	v_pk_add_f32 v[66:67], v[86:87], v[86:87] op_sel:[0,1] op_sel_hi:[1,0] neg_hi:[0,1]
	s_nop 0
	v_pk_add_f32 v[72:73], v[72:73], v[72:73] op_sel:[0,1] op_sel_hi:[1,0] neg_lo:[0,1]
	v_pk_mul_f32 v[86:87], v[92:93], s[10:11] op_sel:[0,0] op_sel_hi:[0,1]
	v_pk_fma_f32 v[86:87], v[92:93], s[10:11], v[86:87] op_sel:[1,1,0] op_sel_hi:[1,0,1] neg_lo:[0,1,0]
	s_mov_b32 s14, s11
	v_pk_mul_f32 v[66:67], v[66:67], s[8:9]
	s_mov_b32 s15, s10
	v_pk_mul_f32 v[92:93], v[84:85], s[14:15] op_sel:[0,0] op_sel_hi:[0,1]
	v_pk_fma_f32 v[92:93], v[84:85], s[14:15], v[92:93] op_sel:[1,1,0] op_sel_hi:[1,0,1] neg_lo:[0,1,0]
	v_pk_add_f32 v[84:85], v[82:83], v[80:81]
	v_pk_add_f32 v[80:81], v[82:83], v[80:81] neg_lo:[0,1] neg_hi:[0,1]
	v_pk_add_f32 v[82:83], v[94:95], v[98:99]
	v_pk_add_f32 v[94:95], v[94:95], v[98:99] neg_lo:[0,1] neg_hi:[0,1]
	v_pk_add_f32 v[74:75], v[74:75], v[74:75] op_sel:[0,1] op_sel_hi:[1,0] neg_hi:[0,1]
	v_pk_add_f32 v[68:69], v[68:69], v[68:69] op_sel:[0,1] op_sel_hi:[1,0] neg_lo:[0,1]
	s_mov_b32 s13, s12
	v_pk_mul_f32 v[72:73], v[72:73], s[12:13]
	v_pk_add_f32 v[98:99], v[84:85], v[82:83]
	v_pk_add_f32 v[82:83], v[84:85], v[82:83] neg_lo:[0,1] neg_hi:[0,1]
	v_pk_add_f32 v[84:85], v[80:81], v[94:95] op_sel:[0,1] op_sel_hi:[1,0] neg_hi:[0,1]
	v_pk_add_f32 v[80:81], v[80:81], v[94:95] op_sel:[0,1] op_sel_hi:[1,0] neg_lo:[0,1]
	v_pk_add_f32 v[94:95], v[78:79], v[66:67]
	v_pk_add_f32 v[66:67], v[78:79], v[66:67] neg_lo:[0,1] neg_hi:[0,1]
	v_pk_add_f32 v[78:79], v[88:89], v[86:87]
	v_pk_add_f32 v[86:87], v[88:89], v[86:87] neg_lo:[0,1] neg_hi:[0,1]
	v_pk_mul_f32 v[74:75], v[74:75], s[8:9]
	v_pk_mul_f32 v[68:69], v[68:69], s[12:13]
	v_pk_add_f32 v[88:89], v[94:95], v[78:79]
	v_pk_add_f32 v[78:79], v[94:95], v[78:79] neg_lo:[0,1] neg_hi:[0,1]
	v_pk_add_f32 v[94:95], v[66:67], v[86:87] op_sel:[0,1] op_sel_hi:[1,0] neg_hi:[0,1]
	v_pk_add_f32 v[66:67], v[66:67], v[86:87] op_sel:[0,1] op_sel_hi:[1,0] neg_lo:[0,1]
	v_pk_add_f32 v[86:87], v[70:71], v[76:77] op_sel:[0,1] op_sel_hi:[1,0] neg_hi:[0,1]
	v_pk_add_f32 v[70:71], v[70:71], v[76:77] op_sel:[0,1] op_sel_hi:[1,0] neg_lo:[0,1]
	v_pk_add_f32 v[76:77], v[74:75], v[72:73]
	v_pk_add_f32 v[72:73], v[74:75], v[72:73] neg_lo:[0,1] neg_hi:[0,1]
	v_pk_add_f32 v[74:75], v[76:77], v[86:87]
	v_pk_add_f32 v[76:77], v[86:87], v[76:77] neg_lo:[0,1] neg_hi:[0,1]
	v_pk_add_f32 v[86:87], v[70:71], v[72:73] op_sel:[0,1] op_sel_hi:[1,0] neg_hi:[0,1]
	v_pk_add_f32 v[70:71], v[70:71], v[72:73] op_sel:[0,1] op_sel_hi:[1,0] neg_lo:[0,1]
	v_pk_add_f32 v[72:73], v[64:65], v[68:69]
	v_pk_add_f32 v[64:65], v[64:65], v[68:69] neg_lo:[0,1] neg_hi:[0,1]
	v_pk_add_f32 v[68:69], v[90:91], v[92:93]
	v_pk_add_f32 v[90:91], v[90:91], v[92:93] neg_lo:[0,1] neg_hi:[0,1]
	v_pk_add_f32 v[92:93], v[72:73], v[68:69]
	v_pk_add_f32 v[68:69], v[72:73], v[68:69] neg_lo:[0,1] neg_hi:[0,1]
	v_pk_add_f32 v[72:73], v[64:65], v[90:91] op_sel:[0,1] op_sel_hi:[1,0] neg_hi:[0,1]
	v_pk_add_f32 v[64:65], v[64:65], v[90:91] op_sel:[0,1] op_sel_hi:[1,0] neg_lo:[0,1]
	v_pk_mul_f32 v[90:91], v[88:89], v[30:31] op_sel:[0,0] op_sel_hi:[0,1]
	v_pk_fma_f32 v[90:91], v[88:89], v[30:31], v[90:91] op_sel:[1,1,0] op_sel_hi:[1,0,1] neg_lo:[0,1,0]
	v_pk_mul_f32 v[88:89], v[74:75], v[28:29] op_sel:[0,0] op_sel_hi:[0,1]
	v_pk_fma_f32 v[88:89], v[74:75], v[28:29], v[88:89] op_sel:[1,1,0] op_sel_hi:[1,0,1] neg_lo:[0,1,0]
	v_pk_mul_f32 v[74:75], v[92:93], v[26:27] op_sel:[0,0] op_sel_hi:[0,1]
	v_pk_fma_f32 v[74:75], v[92:93], v[26:27], v[74:75] op_sel:[1,1,0] op_sel_hi:[1,0,1] neg_lo:[0,1,0]
	s_barrier
	ds_write_b64 v1, v[74:75] offset:6552
	v_pk_mul_f32 v[74:75], v[84:85], v[24:25] op_sel:[0,0] op_sel_hi:[0,1]
	v_pk_fma_f32 v[74:75], v[84:85], v[24:25], v[74:75] op_sel:[1,1,0] op_sel_hi:[1,0,1] neg_lo:[0,1,0]
	ds_write_b64 v1, v[74:75] offset:8736
	v_pk_mul_f32 v[74:75], v[94:95], v[20:21] op_sel:[0,0] op_sel_hi:[0,1]
	v_pk_fma_f32 v[74:75], v[94:95], v[20:21], v[74:75] op_sel:[1,1,0] op_sel_hi:[1,0,1] neg_lo:[0,1,0]
	ds_write_b64 v1, v[74:75] offset:10920
	v_pk_mul_f32 v[74:75], v[86:87], v[16:17] op_sel:[0,0] op_sel_hi:[0,1]
	v_pk_fma_f32 v[74:75], v[86:87], v[16:17], v[74:75] op_sel:[1,1,0] op_sel_hi:[1,0,1] neg_lo:[0,1,0]
	ds_write_b64 v1, v[74:75] offset:13104
	v_pk_mul_f32 v[74:75], v[72:73], v[10:11] op_sel:[0,0] op_sel_hi:[0,1]
	v_pk_fma_f32 v[74:75], v[72:73], v[10:11], v[74:75] op_sel:[1,1,0] op_sel_hi:[1,0,1] neg_lo:[0,1,0]
	v_pk_mul_f32 v[72:73], v[82:83], v[22:23] op_sel:[0,0] op_sel_hi:[0,1]
	v_pk_fma_f32 v[72:73], v[82:83], v[22:23], v[72:73] op_sel:[1,1,0] op_sel_hi:[1,0,1] neg_lo:[0,1,0]
	ds_write_b64 v1, v[72:73] offset:17472
	v_pk_mul_f32 v[72:73], v[78:79], v[18:19] op_sel:[0,0] op_sel_hi:[0,1]
	v_pk_fma_f32 v[72:73], v[78:79], v[18:19], v[72:73] op_sel:[1,1,0] op_sel_hi:[1,0,1] neg_lo:[0,1,0]
	ds_write_b64 v1, v[72:73] offset:19656
	v_pk_mul_f32 v[72:73], v[76:77], v[12:13] op_sel:[0,0] op_sel_hi:[0,1]
	v_pk_fma_f32 v[72:73], v[76:77], v[12:13], v[72:73] op_sel:[1,1,0] op_sel_hi:[1,0,1] neg_lo:[0,1,0]
	ds_write_b64 v1, v[72:73] offset:21840
	v_pk_mul_f32 v[72:73], v[68:69], v[14:15] op_sel:[0,0] op_sel_hi:[0,1]
	v_pk_fma_f32 v[72:73], v[68:69], v[14:15], v[72:73] op_sel:[1,1,0] op_sel_hi:[1,0,1] neg_lo:[0,1,0]
	v_pk_mul_f32 v[68:69], v[80:81], v[6:7] op_sel:[0,0] op_sel_hi:[0,1]
	v_pk_fma_f32 v[68:69], v[80:81], v[6:7], v[68:69] op_sel:[1,1,0] op_sel_hi:[1,0,1] neg_lo:[0,1,0]
	ds_write_b64 v1, v[68:69] offset:26208
	v_pk_mul_f32 v[68:69], v[66:67], v[8:9] op_sel:[0,0] op_sel_hi:[0,1]
	v_pk_fma_f32 v[68:69], v[66:67], v[8:9], v[68:69] op_sel:[1,1,0] op_sel_hi:[1,0,1] neg_lo:[0,1,0]
	v_pk_mul_f32 v[66:67], v[70:71], v[4:5] op_sel:[0,0] op_sel_hi:[0,1]
	v_pk_fma_f32 v[66:67], v[70:71], v[4:5], v[66:67] op_sel:[1,1,0] op_sel_hi:[1,0,1] neg_lo:[0,1,0]
	ds_write_b64 v1, v[66:67] offset:30576
	v_pk_mul_f32 v[66:67], v[64:65], v[2:3] op_sel:[0,0] op_sel_hi:[0,1]
	v_pk_fma_f32 v[66:67], v[64:65], v[2:3], v[66:67] op_sel:[1,1,0] op_sel_hi:[1,0,1] neg_lo:[0,1,0]
	ds_write_b64 v1, v[98:99]
	ds_write_b64 v1, v[90:91] offset:2184
	ds_write_b64 v1, v[88:89] offset:4368
	ds_write_b64 v1, v[74:75] offset:15288
	ds_write_b64 v1, v[72:73] offset:24024
	ds_write_b64 v1, v[68:69] offset:28392
	ds_write_b64 v1, v[66:67] offset:32760
	s_waitcnt lgkmcnt(0)
	s_barrier
	ds_read2_b64 v[64:67], v96 offset1:16
	ds_read2_b64 v[68:71], v96 offset0:32 offset1:48
	ds_read2_b64 v[72:75], v96 offset0:64 offset1:80
	ds_read2_b64 v[76:79], v96 offset0:128 offset1:144
	ds_read2_b64 v[80:83], v96 offset0:96 offset1:112
	ds_read2_b64 v[84:87], v96 offset0:192 offset1:208
	ds_read2_b64 v[88:91], v96 offset0:160 offset1:176
	ds_read2_b64 v[92:95], v96 offset0:224 offset1:240
	s_waitcnt lgkmcnt(4)
	v_pk_add_f32 v[98:99], v[64:65], v[76:77]
	v_pk_add_f32 v[64:65], v[64:65], v[76:77] neg_lo:[0,1] neg_hi:[0,1]
	s_waitcnt lgkmcnt(2)
	v_pk_add_f32 v[76:77], v[72:73], v[84:85]
	v_pk_add_f32 v[72:73], v[72:73], v[84:85] neg_lo:[0,1] neg_hi:[0,1]
	v_pk_add_f32 v[84:85], v[98:99], v[76:77]
	v_pk_add_f32 v[76:77], v[98:99], v[76:77] neg_lo:[0,1] neg_hi:[0,1]
	v_pk_add_f32 v[98:99], v[64:65], v[72:73] op_sel:[0,1] op_sel_hi:[1,0] neg_hi:[0,1]
	v_pk_add_f32 v[64:65], v[64:65], v[72:73] op_sel:[0,1] op_sel_hi:[1,0] neg_lo:[0,1]
	v_pk_add_f32 v[72:73], v[66:67], v[78:79]
	v_pk_add_f32 v[66:67], v[66:67], v[78:79] neg_lo:[0,1] neg_hi:[0,1]
	v_pk_add_f32 v[78:79], v[74:75], v[86:87]
	v_pk_add_f32 v[74:75], v[74:75], v[86:87] neg_lo:[0,1] neg_hi:[0,1]
	v_pk_add_f32 v[86:87], v[72:73], v[78:79]
	v_pk_add_f32 v[72:73], v[72:73], v[78:79] neg_lo:[0,1] neg_hi:[0,1]
	v_pk_add_f32 v[78:79], v[66:67], v[74:75] op_sel:[0,1] op_sel_hi:[1,0] neg_hi:[0,1]
	v_pk_add_f32 v[66:67], v[66:67], v[74:75] op_sel:[0,1] op_sel_hi:[1,0] neg_lo:[0,1]
	s_waitcnt lgkmcnt(1)
	v_pk_add_f32 v[74:75], v[68:69], v[88:89]
	v_pk_add_f32 v[68:69], v[68:69], v[88:89] neg_lo:[0,1] neg_hi:[0,1]
	s_waitcnt lgkmcnt(0)
	v_pk_add_f32 v[88:89], v[80:81], v[92:93]
	v_pk_add_f32 v[80:81], v[80:81], v[92:93] neg_lo:[0,1] neg_hi:[0,1]
	v_pk_add_f32 v[92:93], v[74:75], v[88:89]
	v_pk_add_f32 v[74:75], v[74:75], v[88:89] neg_lo:[0,1] neg_hi:[0,1]
	v_pk_add_f32 v[88:89], v[68:69], v[80:81] op_sel:[0,1] op_sel_hi:[1,0] neg_hi:[0,1]
	v_pk_add_f32 v[68:69], v[68:69], v[80:81] op_sel:[0,1] op_sel_hi:[1,0] neg_lo:[0,1]
	v_pk_add_f32 v[80:81], v[70:71], v[90:91]
	v_pk_add_f32 v[70:71], v[70:71], v[90:91] neg_lo:[0,1] neg_hi:[0,1]
	v_pk_add_f32 v[90:91], v[82:83], v[94:95]
	v_pk_add_f32 v[82:83], v[82:83], v[94:95] neg_lo:[0,1] neg_hi:[0,1]
	v_pk_add_f32 v[94:95], v[80:81], v[90:91]
	v_pk_add_f32 v[80:81], v[80:81], v[90:91] neg_lo:[0,1] neg_hi:[0,1]
	v_pk_add_f32 v[90:91], v[70:71], v[82:83] op_sel:[0,1] op_sel_hi:[1,0] neg_hi:[0,1]
	v_pk_add_f32 v[70:71], v[70:71], v[82:83] op_sel:[0,1] op_sel_hi:[1,0] neg_lo:[0,1]
	v_pk_mul_f32 v[82:83], v[78:79], s[6:7] op_sel:[0,0] op_sel_hi:[0,1]
	v_pk_fma_f32 v[82:83], v[78:79], s[6:7], v[82:83] op_sel:[1,1,0] op_sel_hi:[1,0,1] neg_lo:[0,1,0]
	v_pk_mul_f32 v[78:79], v[66:67], s[10:11] op_sel:[0,0] op_sel_hi:[0,1]
	v_pk_fma_f32 v[78:79], v[66:67], s[10:11], v[78:79] op_sel:[1,1,0] op_sel_hi:[1,0,1] neg_lo:[0,1,0]
	v_pk_add_f32 v[66:67], v[88:89], v[88:89] op_sel:[0,1] op_sel_hi:[1,0] neg_hi:[0,1]
	v_pk_add_f32 v[72:73], v[72:73], v[72:73] op_sel:[0,1] op_sel_hi:[1,0] neg_hi:[0,1]
	s_nop 0
	v_pk_mul_f32 v[88:89], v[90:91], s[10:11] op_sel:[0,0] op_sel_hi:[0,1]
	v_pk_fma_f32 v[88:89], v[90:91], s[10:11], v[88:89] op_sel:[1,1,0] op_sel_hi:[1,0,1] neg_lo:[0,1,0]
	v_pk_mul_f32 v[90:91], v[70:71], s[14:15] op_sel:[0,0] op_sel_hi:[0,1]
	v_pk_fma_f32 v[90:91], v[70:71], s[14:15], v[90:91] op_sel:[1,1,0] op_sel_hi:[1,0,1] neg_lo:[0,1,0]
	v_pk_add_f32 v[70:71], v[84:85], v[92:93]
	v_pk_mul_f32 v[66:67], v[66:67], s[8:9]
	v_pk_add_f32 v[84:85], v[84:85], v[92:93] neg_lo:[0,1] neg_hi:[0,1]
	v_pk_add_f32 v[92:93], v[86:87], v[94:95]
	v_pk_add_f32 v[86:87], v[86:87], v[94:95] neg_lo:[0,1] neg_hi:[0,1]
	v_pk_add_f32 v[68:69], v[68:69], v[68:69] op_sel:[0,1] op_sel_hi:[1,0] neg_lo:[0,1]
	v_pk_add_f32 v[80:81], v[80:81], v[80:81] op_sel:[0,1] op_sel_hi:[1,0] neg_lo:[0,1]
	v_pk_add_f32 v[94:95], v[70:71], v[92:93]
	v_pk_add_f32 v[92:93], v[70:71], v[92:93] neg_lo:[0,1] neg_hi:[0,1]
	v_pk_add_f32 v[100:101], v[84:85], v[86:87] op_sel:[0,1] op_sel_hi:[1,0] neg_hi:[0,1]
	v_pk_add_f32 v[84:85], v[84:85], v[86:87] op_sel:[0,1] op_sel_hi:[1,0] neg_lo:[0,1]
	v_pk_add_f32 v[70:71], v[98:99], v[66:67]
	v_pk_add_f32 v[66:67], v[98:99], v[66:67] neg_lo:[0,1] neg_hi:[0,1]
	v_pk_add_f32 v[86:87], v[82:83], v[88:89]
	v_pk_add_f32 v[82:83], v[82:83], v[88:89] neg_lo:[0,1] neg_hi:[0,1]
	v_pk_mul_f32 v[72:73], v[72:73], s[8:9]
	v_pk_mul_f32 v[68:69], v[68:69], s[12:13]
	v_pk_mul_f32 v[80:81], v[80:81], s[12:13]
	v_pk_add_f32 v[88:89], v[70:71], v[86:87]
	v_pk_add_f32 v[86:87], v[70:71], v[86:87] neg_lo:[0,1] neg_hi:[0,1]
	v_pk_add_f32 v[98:99], v[66:67], v[82:83] op_sel:[0,1] op_sel_hi:[1,0] neg_hi:[0,1]
	v_pk_add_f32 v[82:83], v[66:67], v[82:83] op_sel:[0,1] op_sel_hi:[1,0] neg_lo:[0,1]
	v_pk_add_f32 v[66:67], v[76:77], v[74:75] op_sel:[0,1] op_sel_hi:[1,0] neg_hi:[0,1]
	v_pk_add_f32 v[70:71], v[76:77], v[74:75] op_sel:[0,1] op_sel_hi:[1,0] neg_lo:[0,1]
	v_pk_add_f32 v[74:75], v[72:73], v[80:81]
	v_pk_add_f32 v[72:73], v[72:73], v[80:81] neg_lo:[0,1] neg_hi:[0,1]
	v_pk_add_f32 v[76:77], v[74:75], v[66:67]
	v_pk_add_f32 v[74:75], v[66:67], v[74:75] neg_lo:[0,1] neg_hi:[0,1]
	v_pk_add_f32 v[66:67], v[64:65], v[68:69]
	v_pk_add_f32 v[64:65], v[64:65], v[68:69] neg_lo:[0,1] neg_hi:[0,1]
	v_pk_add_f32 v[68:69], v[78:79], v[90:91]
	v_pk_add_f32 v[80:81], v[70:71], v[72:73] op_sel:[0,1] op_sel_hi:[1,0] neg_hi:[0,1]
	v_pk_add_f32 v[72:73], v[70:71], v[72:73] op_sel:[0,1] op_sel_hi:[1,0] neg_lo:[0,1]
	v_pk_add_f32 v[70:71], v[78:79], v[90:91] neg_lo:[0,1] neg_hi:[0,1]
	v_pk_add_f32 v[78:79], v[66:67], v[68:69]
	v_pk_add_f32 v[90:91], v[66:67], v[68:69] neg_lo:[0,1] neg_hi:[0,1]
	v_mov_b32_e32 v68, v0
	v_pk_add_f32 v[102:103], v[64:65], v[70:71] op_sel:[0,1] op_sel_hi:[1,0] neg_hi:[0,1]
	v_pk_add_f32 v[104:105], v[64:65], v[70:71] op_sel:[0,1] op_sel_hi:[1,0] neg_lo:[0,1]
	s_nop 0
	v_ashrrev_i32_e32 v64, 4, v68
	v_lshlrev_b32_e32 v97, 3, v64
	v_add_u32_e32 v108, 0x8800, v97
	v_and_b32_e32 v68, 15, v68
	v_mad_u32_u24 v109, v68, s5, v97
	ds_read_b64 v[68:69], v108 offset:128
	s_waitcnt lgkmcnt(0)
	v_pk_mul_f32 v[106:107], v[88:89], v[68:69] op_sel:[0,0] op_sel_hi:[0,1]
	v_pk_fma_f32 v[106:107], v[88:89], v[68:69], v[106:107] op_sel:[1,1,0] op_sel_hi:[1,0,1] neg_lo:[0,1,0]
	v_pk_mul_f32 v[64:65], v[68:69], v[68:69] op_sel:[0,0] op_sel_hi:[0,1]
	v_pk_fma_f32 v[64:65], v[68:69], v[68:69], v[64:65] op_sel:[1,1,0] op_sel_hi:[1,0,1] neg_lo:[0,1,0]
	v_pk_mul_f32 v[88:89], v[76:77], v[64:65] op_sel:[0,0] op_sel_hi:[0,1]
	v_pk_fma_f32 v[88:89], v[76:77], v[64:65], v[88:89] op_sel:[1,1,0] op_sel_hi:[1,0,1] neg_lo:[0,1,0]
	v_pk_mul_f32 v[66:67], v[64:65], v[68:69] op_sel:[0,0] op_sel_hi:[0,1]
	v_pk_fma_f32 v[66:67], v[64:65], v[68:69], v[66:67] op_sel:[1,1,0] op_sel_hi:[1,0,1] neg_lo:[0,1,0]
	v_pk_mul_f32 v[76:77], v[78:79], v[66:67] op_sel:[0,0] op_sel_hi:[0,1]
	v_pk_fma_f32 v[76:77], v[78:79], v[66:67], v[76:77] op_sel:[1,1,0] op_sel_hi:[1,0,1] neg_lo:[0,1,0]
	ds_write2_b64 v109, v[88:89], v[76:77] offset0:32 offset1:48
	v_pk_mul_f32 v[64:65], v[66:67], v[68:69] op_sel:[0,0] op_sel_hi:[0,1]
	v_pk_fma_f32 v[64:65], v[66:67], v[68:69], v[64:65] op_sel:[1,1,0] op_sel_hi:[1,0,1] neg_lo:[0,1,0]
	v_pk_mul_f32 v[76:77], v[100:101], v[64:65] op_sel:[0,0] op_sel_hi:[0,1]
	v_pk_fma_f32 v[76:77], v[100:101], v[64:65], v[76:77] op_sel:[1,1,0] op_sel_hi:[1,0,1] neg_lo:[0,1,0]
	v_pk_mul_f32 v[66:67], v[64:65], v[68:69] op_sel:[0,0] op_sel_hi:[0,1]
	v_pk_fma_f32 v[66:67], v[64:65], v[68:69], v[66:67] op_sel:[1,1,0] op_sel_hi:[1,0,1] neg_lo:[0,1,0]
	v_pk_mul_f32 v[78:79], v[98:99], v[66:67] op_sel:[0,0] op_sel_hi:[0,1]
	v_pk_fma_f32 v[78:79], v[98:99], v[66:67], v[78:79] op_sel:[1,1,0] op_sel_hi:[1,0,1] neg_lo:[0,1,0]
	ds_write2_b64 v109, v[76:77], v[78:79] offset0:64 offset1:80
	v_pk_mul_f32 v[64:65], v[66:67], v[68:69] op_sel:[0,0] op_sel_hi:[0,1]
	v_pk_fma_f32 v[64:65], v[66:67], v[68:69], v[64:65] op_sel:[1,1,0] op_sel_hi:[1,0,1] neg_lo:[0,1,0]
	v_pk_mul_f32 v[76:77], v[80:81], v[64:65] op_sel:[0,0] op_sel_hi:[0,1]
	v_pk_fma_f32 v[76:77], v[80:81], v[64:65], v[76:77] op_sel:[1,1,0] op_sel_hi:[1,0,1] neg_lo:[0,1,0]
	v_pk_mul_f32 v[66:67], v[64:65], v[68:69] op_sel:[0,0] op_sel_hi:[0,1]
	v_pk_fma_f32 v[66:67], v[64:65], v[68:69], v[66:67] op_sel:[1,1,0] op_sel_hi:[1,0,1] neg_lo:[0,1,0]
	v_pk_mul_f32 v[78:79], v[102:103], v[66:67] op_sel:[0,0] op_sel_hi:[0,1]
	v_pk_fma_f32 v[78:79], v[102:103], v[66:67], v[78:79] op_sel:[1,1,0] op_sel_hi:[1,0,1] neg_lo:[0,1,0]
	ds_write2_b64 v109, v[76:77], v[78:79] offset0:96 offset1:112
	v_pk_mul_f32 v[64:65], v[66:67], v[68:69] op_sel:[0,0] op_sel_hi:[0,1]
	v_pk_fma_f32 v[64:65], v[66:67], v[68:69], v[64:65] op_sel:[1,1,0] op_sel_hi:[1,0,1] neg_lo:[0,1,0]
	v_pk_mul_f32 v[76:77], v[92:93], v[64:65] op_sel:[0,0] op_sel_hi:[0,1]
	v_pk_fma_f32 v[76:77], v[92:93], v[64:65], v[76:77] op_sel:[1,1,0] op_sel_hi:[1,0,1] neg_lo:[0,1,0]
	v_pk_mul_f32 v[66:67], v[64:65], v[68:69] op_sel:[0,0] op_sel_hi:[0,1]
	v_pk_fma_f32 v[66:67], v[64:65], v[68:69], v[66:67] op_sel:[1,1,0] op_sel_hi:[1,0,1] neg_lo:[0,1,0]
	v_pk_mul_f32 v[78:79], v[86:87], v[66:67] op_sel:[0,0] op_sel_hi:[0,1]
	v_pk_fma_f32 v[78:79], v[86:87], v[66:67], v[78:79] op_sel:[1,1,0] op_sel_hi:[1,0,1] neg_lo:[0,1,0]
	ds_write2_b64 v109, v[76:77], v[78:79] offset0:128 offset1:144
	v_pk_mul_f32 v[64:65], v[66:67], v[68:69] op_sel:[0,0] op_sel_hi:[0,1]
	v_pk_fma_f32 v[64:65], v[66:67], v[68:69], v[64:65] op_sel:[1,1,0] op_sel_hi:[1,0,1] neg_lo:[0,1,0]
	v_pk_mul_f32 v[76:77], v[74:75], v[64:65] op_sel:[0,0] op_sel_hi:[0,1]
	v_pk_fma_f32 v[76:77], v[74:75], v[64:65], v[76:77] op_sel:[1,1,0] op_sel_hi:[1,0,1] neg_lo:[0,1,0]
	v_pk_mul_f32 v[66:67], v[64:65], v[68:69] op_sel:[0,0] op_sel_hi:[0,1]
	v_pk_fma_f32 v[66:67], v[64:65], v[68:69], v[66:67] op_sel:[1,1,0] op_sel_hi:[1,0,1] neg_lo:[0,1,0]
	v_pk_mul_f32 v[74:75], v[90:91], v[66:67] op_sel:[0,0] op_sel_hi:[0,1]
	v_pk_fma_f32 v[74:75], v[90:91], v[66:67], v[74:75] op_sel:[1,1,0] op_sel_hi:[1,0,1] neg_lo:[0,1,0]
	ds_write2_b64 v109, v[76:77], v[74:75] offset0:160 offset1:176
	v_pk_mul_f32 v[64:65], v[66:67], v[68:69] op_sel:[0,0] op_sel_hi:[0,1]
	v_pk_fma_f32 v[64:65], v[66:67], v[68:69], v[64:65] op_sel:[1,1,0] op_sel_hi:[1,0,1] neg_lo:[0,1,0]
	v_pk_mul_f32 v[74:75], v[84:85], v[64:65] op_sel:[0,0] op_sel_hi:[0,1]
	v_pk_fma_f32 v[74:75], v[84:85], v[64:65], v[74:75] op_sel:[1,1,0] op_sel_hi:[1,0,1] neg_lo:[0,1,0]
	v_pk_mul_f32 v[66:67], v[64:65], v[68:69] op_sel:[0,0] op_sel_hi:[0,1]
	v_pk_fma_f32 v[66:67], v[64:65], v[68:69], v[66:67] op_sel:[1,1,0] op_sel_hi:[1,0,1] neg_lo:[0,1,0]
	v_pk_mul_f32 v[70:71], v[82:83], v[66:67] op_sel:[0,0] op_sel_hi:[0,1]
	v_pk_fma_f32 v[70:71], v[82:83], v[66:67], v[70:71] op_sel:[1,1,0] op_sel_hi:[1,0,1] neg_lo:[0,1,0]
	v_pk_mul_f32 v[64:65], v[66:67], v[68:69] op_sel:[0,0] op_sel_hi:[0,1]
	v_pk_fma_f32 v[64:65], v[66:67], v[68:69], v[64:65] op_sel:[1,1,0] op_sel_hi:[1,0,1] neg_lo:[0,1,0]
	v_pk_mul_f32 v[78:79], v[72:73], v[64:65] op_sel:[0,0] op_sel_hi:[0,1]
	v_pk_fma_f32 v[78:79], v[72:73], v[64:65], v[78:79] op_sel:[1,1,0] op_sel_hi:[1,0,1] neg_lo:[0,1,0]
	v_pk_mul_f32 v[66:67], v[64:65], v[68:69] op_sel:[0,0] op_sel_hi:[0,1]
	v_pk_fma_f32 v[66:67], v[64:65], v[68:69], v[66:67] op_sel:[1,1,0] op_sel_hi:[1,0,1] neg_lo:[0,1,0]
	v_pk_mul_f32 v[76:77], v[104:105], v[66:67] op_sel:[0,0] op_sel_hi:[0,1]
	v_pk_fma_f32 v[76:77], v[104:105], v[66:67], v[76:77] op_sel:[1,1,0] op_sel_hi:[1,0,1] neg_lo:[0,1,0]
	ds_write2_b64 v109, v[78:79], v[76:77] offset0:224 offset1:240
	v_mov_b32_e32 v64, v0
	ds_write2_b64 v109, v[94:95], v[106:107] offset1:16
	ds_write2_b64 v109, v[74:75], v[70:71] offset0:192 offset1:208
	s_waitcnt lgkmcnt(0)
	s_barrier
	s_nop 0
	v_and_b32_e32 v65, 15, v64
	v_and_b32_e32 v64, 0x1ffffff0, v64
	v_lshlrev_b32_e32 v64, 3, v64
	v_mad_u32_u24 v92, v65, s5, v64
	ds_read2_b64 v[64:67], v92 offset1:1
	ds_read2_b64 v[68:71], v92 offset0:2 offset1:3
	ds_read2_b64 v[72:75], v92 offset0:8 offset1:9
	ds_read2_b64 v[76:79], v92 offset0:4 offset1:5
	ds_read2_b64 v[80:83], v92 offset0:6 offset1:7
	ds_read2_b64 v[84:87], v92 offset0:12 offset1:13
	ds_read2_b64 v[88:91], v92 offset0:10 offset1:11
	ds_read2_b64 v[92:95], v92 offset0:14 offset1:15
	s_waitcnt lgkmcnt(5)
	v_pk_add_f32 v[98:99], v[64:65], v[72:73]
	v_pk_add_f32 v[64:65], v[64:65], v[72:73] neg_lo:[0,1] neg_hi:[0,1]
	s_waitcnt lgkmcnt(2)
	v_pk_add_f32 v[72:73], v[76:77], v[84:85]
	v_pk_add_f32 v[76:77], v[76:77], v[84:85] neg_lo:[0,1] neg_hi:[0,1]
	v_pk_add_f32 v[84:85], v[98:99], v[72:73]
	v_pk_add_f32 v[98:99], v[98:99], v[72:73] neg_lo:[0,1] neg_hi:[0,1]
	v_pk_add_f32 v[100:101], v[64:65], v[76:77] op_sel:[0,1] op_sel_hi:[1,0] neg_hi:[0,1]
	v_pk_add_f32 v[102:103], v[64:65], v[76:77] op_sel:[0,1] op_sel_hi:[1,0] neg_lo:[0,1]
	v_pk_add_f32 v[64:65], v[66:67], v[74:75]
	v_pk_add_f32 v[72:73], v[78:79], v[86:87]
	v_pk_add_f32 v[66:67], v[66:67], v[74:75] neg_lo:[0,1] neg_hi:[0,1]
	v_pk_add_f32 v[74:75], v[78:79], v[86:87] neg_lo:[0,1] neg_hi:[0,1]
	v_pk_add_f32 v[76:77], v[64:65], v[72:73]
	v_pk_add_f32 v[64:65], v[64:65], v[72:73] neg_lo:[0,1] neg_hi:[0,1]
	v_pk_add_f32 v[72:73], v[66:67], v[74:75] op_sel:[0,1] op_sel_hi:[1,0] neg_hi:[0,1]
	v_pk_add_f32 v[66:67], v[66:67], v[74:75] op_sel:[0,1] op_sel_hi:[1,0] neg_lo:[0,1]
	s_waitcnt lgkmcnt(1)
	v_pk_add_f32 v[74:75], v[68:69], v[88:89]
	s_waitcnt lgkmcnt(0)
	v_pk_add_f32 v[78:79], v[80:81], v[92:93]
	v_pk_add_f32 v[64:65], v[64:65], v[64:65] op_sel:[0,1] op_sel_hi:[1,0] neg_hi:[0,1]
	v_pk_add_f32 v[68:69], v[68:69], v[88:89] neg_lo:[0,1] neg_hi:[0,1]
	v_pk_add_f32 v[80:81], v[80:81], v[92:93] neg_lo:[0,1] neg_hi:[0,1]
	v_pk_add_f32 v[86:87], v[74:75], v[78:79]
	v_pk_add_f32 v[78:79], v[74:75], v[78:79] neg_lo:[0,1] neg_hi:[0,1]
	v_pk_add_f32 v[74:75], v[68:69], v[80:81] op_sel:[0,1] op_sel_hi:[1,0] neg_hi:[0,1]
	v_pk_mul_f32 v[92:93], v[64:65], s[8:9]
	v_pk_add_f32 v[68:69], v[68:69], v[80:81] op_sel:[0,1] op_sel_hi:[1,0] neg_lo:[0,1]
	v_pk_add_f32 v[80:81], v[70:71], v[90:91]
	v_pk_add_f32 v[64:65], v[74:75], v[74:75] op_sel:[0,1] op_sel_hi:[1,0] neg_hi:[0,1]
	v_pk_add_f32 v[70:71], v[70:71], v[90:91] neg_lo:[0,1] neg_hi:[0,1]
	v_pk_add_f32 v[88:89], v[82:83], v[94:95]
	v_pk_add_f32 v[82:83], v[82:83], v[94:95] neg_lo:[0,1] neg_hi:[0,1]
	v_pk_mul_f32 v[94:95], v[66:67], s[10:11] op_sel:[0,0] op_sel_hi:[0,1]
	v_pk_fma_f32 v[94:95], v[66:67], s[10:11], v[94:95] op_sel:[1,1,0] op_sel_hi:[1,0,1] neg_lo:[0,1,0]
	v_pk_mul_f32 v[66:67], v[64:65], s[8:9]
	v_pk_add_f32 v[64:65], v[68:69], v[68:69] op_sel:[0,1] op_sel_hi:[1,0] neg_lo:[0,1]
	v_pk_add_f32 v[90:91], v[80:81], v[88:89]
	v_pk_add_f32 v[80:81], v[80:81], v[88:89] neg_lo:[0,1] neg_hi:[0,1]
	v_pk_add_f32 v[88:89], v[70:71], v[82:83] op_sel:[0,1] op_sel_hi:[1,0] neg_hi:[0,1]
	v_pk_add_f32 v[70:71], v[70:71], v[82:83] op_sel:[0,1] op_sel_hi:[1,0] neg_lo:[0,1]
	v_pk_mul_f32 v[104:105], v[64:65], s[12:13]
	v_pk_mul_f32 v[82:83], v[72:73], s[6:7] op_sel:[0,0] op_sel_hi:[0,1]
	v_pk_fma_f32 v[82:83], v[72:73], s[6:7], v[82:83] op_sel:[1,1,0] op_sel_hi:[1,0,1] neg_lo:[0,1,0]
	v_pk_add_f32 v[72:73], v[76:77], v[90:91]
	v_pk_add_f32 v[64:65], v[80:81], v[80:81] op_sel:[0,1] op_sel_hi:[1,0] neg_lo:[0,1]
	v_pk_mul_f32 v[68:69], v[88:89], s[10:11] op_sel:[0,0] op_sel_hi:[0,1]
	v_pk_fma_f32 v[68:69], v[88:89], s[10:11], v[68:69] op_sel:[1,1,0] op_sel_hi:[1,0,1] neg_lo:[0,1,0]
	v_pk_mul_f32 v[108:109], v[70:71], s[14:15] op_sel:[0,0] op_sel_hi:[0,1]
	v_pk_fma_f32 v[108:109], v[70:71], s[14:15], v[108:109] op_sel:[1,1,0] op_sel_hi:[1,0,1] neg_lo:[0,1,0]
	v_pk_add_f32 v[70:71], v[84:85], v[86:87] neg_lo:[0,1] neg_hi:[0,1]
	v_pk_mul_f32 v[106:107], v[64:65], s[12:13]
	v_pk_add_f32 v[64:65], v[84:85], v[86:87]
	v_pk_add_f32 v[74:75], v[76:77], v[90:91] neg_lo:[0,1] neg_hi:[0,1]
	v_pk_add_f32 v[88:89], v[64:65], v[72:73]
	v_pk_add_f32 v[72:73], v[64:65], v[72:73] neg_lo:[0,1] neg_hi:[0,1]
	v_pk_add_f32 v[80:81], v[70:71], v[74:75] op_sel:[0,1] op_sel_hi:[1,0] neg_hi:[0,1]
	v_pk_add_f32 v[64:65], v[70:71], v[74:75] op_sel:[0,1] op_sel_hi:[1,0] neg_lo:[0,1]
	v_pk_add_f32 v[70:71], v[100:101], v[66:67]
	v_pk_add_f32 v[66:67], v[100:101], v[66:67] neg_lo:[0,1] neg_hi:[0,1]
	v_pk_add_f32 v[74:75], v[82:83], v[68:69]
	v_pk_add_f32 v[68:69], v[82:83], v[68:69] neg_lo:[0,1] neg_hi:[0,1]
	v_pk_add_f32 v[90:91], v[70:71], v[74:75]
	v_pk_add_f32 v[74:75], v[70:71], v[74:75] neg_lo:[0,1] neg_hi:[0,1]
	v_pk_add_f32 v[82:83], v[66:67], v[68:69] op_sel:[0,1] op_sel_hi:[1,0] neg_hi:[0,1]
	v_pk_add_f32 v[66:67], v[66:67], v[68:69] op_sel:[0,1] op_sel_hi:[1,0] neg_lo:[0,1]
	v_pk_add_f32 v[68:69], v[98:99], v[78:79] op_sel:[0,1] op_sel_hi:[1,0] neg_hi:[0,1]
	v_pk_add_f32 v[70:71], v[98:99], v[78:79] op_sel:[0,1] op_sel_hi:[1,0] neg_lo:[0,1]
	v_pk_add_f32 v[76:77], v[92:93], v[106:107]
	v_pk_add_f32 v[78:79], v[92:93], v[106:107] neg_lo:[0,1] neg_hi:[0,1]
	v_pk_add_f32 v[92:93], v[76:77], v[68:69]
	v_pk_add_f32 v[76:77], v[68:69], v[76:77] neg_lo:[0,1] neg_hi:[0,1]
	v_pk_add_f32 v[86:87], v[70:71], v[78:79] op_sel:[0,1] op_sel_hi:[1,0] neg_hi:[0,1]
	v_pk_add_f32 v[68:69], v[70:71], v[78:79] op_sel:[0,1] op_sel_hi:[1,0] neg_lo:[0,1]
	v_pk_add_f32 v[70:71], v[102:103], v[104:105]
	v_pk_add_f32 v[98:99], v[102:103], v[104:105] neg_lo:[0,1] neg_hi:[0,1]
	v_pk_add_f32 v[78:79], v[94:95], v[108:109]
	v_pk_add_f32 v[100:101], v[94:95], v[108:109] neg_lo:[0,1] neg_hi:[0,1]
	v_pk_add_f32 v[94:95], v[70:71], v[78:79]
	v_pk_add_f32 v[78:79], v[70:71], v[78:79] neg_lo:[0,1] neg_hi:[0,1]
	v_pk_add_f32 v[84:85], v[98:99], v[100:101] op_sel:[0,1] op_sel_hi:[1,0] neg_hi:[0,1]
	v_pk_add_f32 v[70:71], v[98:99], v[100:101] op_sel:[0,1] op_sel_hi:[1,0] neg_lo:[0,1]
	v_mov_b32_e32 v98, v0
	s_nop 0
	v_and_b32_e32 v97, -16, v98
	v_and_b32_e32 v99, 15, v98
	v_lshlrev_b32_e32 v100, 3, v97
	v_mad_u32_u24 v100, v99, s5, v100
	v_cmp_ne_u32_e32 vcc, 0, v99
	ds_write2_b64 v100, v[88:89], v[90:91] offset1:1
	ds_write2_b64 v100, v[92:93], v[94:95] offset0:2 offset1:3
	ds_write2_b64 v100, v[80:81], v[82:83] offset0:4 offset1:5
	ds_write2_b64 v100, v[86:87], v[84:85] offset0:6 offset1:7
	ds_write2_b64 v100, v[72:73], v[74:75] offset0:8 offset1:9
	ds_write2_b64 v100, v[76:77], v[78:79] offset0:10 offset1:11
	ds_write2_b64 v100, v[64:65], v[66:67] offset0:12 offset1:13
	ds_write2_b64 v100, v[68:69], v[70:71] offset0:14 offset1:15
	s_waitcnt lgkmcnt(0)
	s_barrier
	s_and_saveexec_b64 s[6:7], vcc
	s_xor_b64 s[6:7], exec, s[6:7]
	v_sub_u32_e32 v99, 16, v99
	v_mul_u32_u24_e32 v99, 0x111, v99
	v_sub_u32_e32 v97, v99, v97
	v_add_u32_e32 v100, 0xf0, v97
	s_andn2_saveexec_b64 s[6:7], s[6:7]
	v_sub_u32_e32 v97, 0x100, v98
	v_cmp_lt_u32_e32 vcc, 15, v98
	s_nop 1
	v_cndmask_b32_e32 v100, 1, v97, vcc
	s_or_b64 exec, exec, s[6:7]
	v_mov_b32_e32 v97, 0
	v_lshlrev_b32_e32 v110, 3, v100
	ds_read_b64 v[108:109], v97
	ds_read2_b64 v[100:103], v110 offset0:14 offset1:15
	v_cmp_eq_u32_e32 vcc, 0, v98
	ds_read2_b64 v[104:107], v110 offset0:12 offset1:13
	s_mov_b32 s6, 0x3f6c835e
	s_mov_b32 s7, 0xbec3ef15
	s_waitcnt lgkmcnt(1)
	v_cndmask_b32_e32 v99, v103, v109, vcc
	v_cndmask_b32_e32 v98, v102, v108, vcc
	v_pk_add_f32 v[102:103], v[88:89], v[98:99] neg_hi:[0,1]
	v_pk_add_f32 v[88:89], v[88:89], v[98:99] neg_lo:[0,1]
	s_mov_b32 s9, s8
	v_pk_mul_f32 v[98:99], v[102:103], v[88:89] op_sel:[0,0] op_sel_hi:[0,1]
	v_pk_fma_f32 v[98:99], v[102:103], v[88:89], v[98:99] op_sel:[1,1,0] op_sel_hi:[1,0,1] neg_hi:[0,1,0]
	v_pk_add_f32 v[88:89], v[90:91], v[100:101] neg_hi:[0,1]
	v_pk_add_f32 v[90:91], v[90:91], v[100:101] neg_lo:[0,1]
	s_mov_b32 s14, s11
	v_pk_add_f32 v[62:63], v[62:63], v[98:99] op_sel:[1,0] op_sel_hi:[0,1] neg_lo:[0,1] neg_hi:[1,1]
	v_pk_mul_f32 v[98:99], v[88:89], v[90:91] op_sel:[0,0] op_sel_hi:[0,1]
	v_pk_fma_f32 v[98:99], v[88:89], v[90:91], v[98:99] op_sel:[1,1,0] op_sel_hi:[1,0,1] neg_hi:[0,1,0]
	s_waitcnt lgkmcnt(0)
	v_pk_add_f32 v[88:89], v[92:93], v[106:107] neg_hi:[0,1]
	v_pk_add_f32 v[90:91], v[92:93], v[106:107] neg_lo:[0,1]
	s_mov_b32 s15, s10
	v_pk_mul_f32 v[92:93], v[88:89], v[90:91] op_sel:[0,0] op_sel_hi:[0,1]
	v_pk_fma_f32 v[92:93], v[88:89], v[90:91], v[92:93] op_sel:[1,1,0] op_sel_hi:[1,0,1] neg_hi:[0,1,0]
	v_pk_add_f32 v[60:61], v[60:61], v[98:99] op_sel:[1,0] op_sel_hi:[0,1] neg_lo:[0,1] neg_hi:[1,1]
	ds_read2_b64 v[88:91], v110 offset0:10 offset1:11
	v_pk_add_f32 v[58:59], v[58:59], v[92:93] op_sel:[1,0] op_sel_hi:[0,1] neg_lo:[0,1] neg_hi:[1,1]
	v_pk_add_f32 v[92:93], v[94:95], v[104:105] neg_hi:[0,1]
	v_pk_add_f32 v[94:95], v[94:95], v[104:105] neg_lo:[0,1]
	s_mov_b32 s13, s12
	v_pk_mul_f32 v[98:99], v[92:93], v[94:95] op_sel:[0,0] op_sel_hi:[0,1]
	v_pk_fma_f32 v[98:99], v[92:93], v[94:95], v[98:99] op_sel:[1,1,0] op_sel_hi:[1,0,1] neg_hi:[0,1,0]
	ds_read2_b64 v[92:95], v110 offset0:8 offset1:9
	v_pk_add_f32 v[56:57], v[56:57], v[98:99] op_sel:[1,0] op_sel_hi:[0,1] neg_lo:[0,1] neg_hi:[1,1]
	s_waitcnt lgkmcnt(1)
	v_pk_add_f32 v[98:99], v[80:81], v[90:91] neg_hi:[0,1]
	v_pk_add_f32 v[80:81], v[80:81], v[90:91] neg_lo:[0,1]
	s_add_u32 s2, s2, 0x2000000
	v_pk_mul_f32 v[90:91], v[98:99], v[80:81] op_sel:[0,0] op_sel_hi:[0,1]
	v_pk_fma_f32 v[90:91], v[98:99], v[80:81], v[90:91] op_sel:[1,1,0] op_sel_hi:[1,0,1] neg_hi:[0,1,0]
	v_pk_add_f32 v[80:81], v[82:83], v[88:89] neg_hi:[0,1]
	v_pk_add_f32 v[82:83], v[82:83], v[88:89] neg_lo:[0,1]
	s_addc_u32 s3, s3, 0
	v_pk_mul_f32 v[88:89], v[80:81], v[82:83] op_sel:[0,0] op_sel_hi:[0,1]
	v_pk_fma_f32 v[88:89], v[80:81], v[82:83], v[88:89] op_sel:[1,1,0] op_sel_hi:[1,0,1] neg_hi:[0,1,0]
	s_waitcnt lgkmcnt(0)
	v_pk_add_f32 v[80:81], v[86:87], v[94:95] neg_lo:[0,1]
	v_pk_add_f32 v[54:55], v[54:55], v[90:91] op_sel:[1,0] op_sel_hi:[0,1] neg_lo:[0,1] neg_hi:[1,1]
	s_load_dwordx2 s[0:1], s[0:1], 0x8
	v_pk_add_f32 v[88:89], v[52:53], v[88:89] op_sel:[1,0] op_sel_hi:[0,1] neg_lo:[0,1] neg_hi:[1,1]
	v_pk_add_f32 v[52:53], v[86:87], v[94:95] neg_hi:[0,1]
	s_nop 0
	v_pk_mul_f32 v[82:83], v[52:53], v[80:81] op_sel:[0,0] op_sel_hi:[0,1]
	v_pk_fma_f32 v[82:83], v[52:53], v[80:81], v[82:83] op_sel:[1,1,0] op_sel_hi:[1,0,1] neg_hi:[0,1,0]
	v_pk_add_f32 v[80:81], v[84:85], v[92:93] neg_hi:[0,1]
	s_nop 0
	v_pk_add_f32 v[86:87], v[50:51], v[82:83] op_sel:[1,0] op_sel_hi:[0,1] neg_lo:[0,1] neg_hi:[1,1]
	ds_read2_b64 v[50:53], v110 offset0:6 offset1:7
	v_pk_add_f32 v[82:83], v[84:85], v[92:93] neg_lo:[0,1]
	s_nop 0
	v_pk_mul_f32 v[84:85], v[80:81], v[82:83] op_sel:[0,0] op_sel_hi:[0,1]
	v_pk_fma_f32 v[84:85], v[80:81], v[82:83], v[84:85] op_sel:[1,1,0] op_sel_hi:[1,0,1] neg_hi:[0,1,0]
	ds_read2_b64 v[80:83], v110 offset0:4 offset1:5
	v_pk_add_f32 v[84:85], v[48:49], v[84:85] op_sel:[1,0] op_sel_hi:[0,1] neg_lo:[0,1] neg_hi:[1,1]
	s_waitcnt lgkmcnt(0)
	v_pk_add_f32 v[48:49], v[72:73], v[52:53] neg_hi:[0,1]
	v_pk_add_f32 v[52:53], v[72:73], v[52:53] neg_lo:[0,1]
	s_nop 0
	v_pk_mul_f32 v[72:73], v[48:49], v[52:53] op_sel:[0,0] op_sel_hi:[0,1]
	v_pk_fma_f32 v[72:73], v[48:49], v[52:53], v[72:73] op_sel:[1,1,0] op_sel_hi:[1,0,1] neg_hi:[0,1,0]
	v_pk_add_f32 v[48:49], v[74:75], v[50:51] neg_lo:[0,1]
	s_nop 0
	v_pk_add_f32 v[52:53], v[46:47], v[72:73] op_sel:[1,0] op_sel_hi:[0,1] neg_lo:[0,1] neg_hi:[1,1]
	v_pk_add_f32 v[46:47], v[74:75], v[50:51] neg_hi:[0,1]
	s_nop 0
	v_pk_mul_f32 v[50:51], v[46:47], v[48:49] op_sel:[0,0] op_sel_hi:[0,1]
	v_pk_fma_f32 v[50:51], v[46:47], v[48:49], v[50:51] op_sel:[1,1,0] op_sel_hi:[1,0,1] neg_hi:[0,1,0]
	v_pk_add_f32 v[46:47], v[76:77], v[82:83] neg_lo:[0,1]
	s_nop 0
	v_pk_add_f32 v[50:51], v[44:45], v[50:51] op_sel:[1,0] op_sel_hi:[0,1] neg_lo:[0,1] neg_hi:[1,1]
	v_pk_add_f32 v[44:45], v[76:77], v[82:83] neg_hi:[0,1]
	s_nop 0
	v_pk_mul_f32 v[48:49], v[44:45], v[46:47] op_sel:[0,0] op_sel_hi:[0,1]
	v_pk_fma_f32 v[48:49], v[44:45], v[46:47], v[48:49] op_sel:[1,1,0] op_sel_hi:[1,0,1] neg_hi:[0,1,0]
	v_pk_add_f32 v[46:47], v[78:79], v[80:81] neg_hi:[0,1]
	s_nop 0
	v_pk_add_f32 v[72:73], v[42:43], v[48:49] op_sel:[1,0] op_sel_hi:[0,1] neg_lo:[0,1] neg_hi:[1,1]
	ds_read2_b64 v[42:45], v110 offset0:2 offset1:3
	v_pk_add_f32 v[48:49], v[78:79], v[80:81] neg_lo:[0,1]
	s_nop 0
	v_pk_mul_f32 v[74:75], v[46:47], v[48:49] op_sel:[0,0] op_sel_hi:[0,1]
	v_pk_fma_f32 v[74:75], v[46:47], v[48:49], v[74:75] op_sel:[1,1,0] op_sel_hi:[1,0,1] neg_hi:[0,1,0]
	ds_read2_b64 v[46:49], v110 offset1:1
	v_pk_add_f32 v[40:41], v[40:41], v[74:75] op_sel:[1,0] op_sel_hi:[0,1] neg_lo:[0,1] neg_hi:[1,1]
	s_waitcnt lgkmcnt(1)
	v_pk_add_f32 v[74:75], v[64:65], v[44:45] neg_hi:[0,1]
	v_pk_add_f32 v[44:45], v[64:65], v[44:45] neg_lo:[0,1]
	s_waitcnt lgkmcnt(0)
	v_pk_mul_f32 v[64:65], v[74:75], v[44:45] op_sel:[0,0] op_sel_hi:[0,1]
	v_pk_fma_f32 v[64:65], v[74:75], v[44:45], v[64:65] op_sel:[1,1,0] op_sel_hi:[1,0,1] neg_hi:[0,1,0]
	v_pk_add_f32 v[44:45], v[66:67], v[42:43] neg_hi:[0,1]
	v_pk_add_f32 v[42:43], v[66:67], v[42:43] neg_lo:[0,1]
	s_barrier
	v_pk_add_f32 v[38:39], v[38:39], v[64:65] op_sel:[1,0] op_sel_hi:[0,1] neg_lo:[0,1] neg_hi:[1,1]
	v_pk_mul_f32 v[64:65], v[44:45], v[42:43] op_sel:[0,0] op_sel_hi:[0,1]
	v_pk_fma_f32 v[64:65], v[44:45], v[42:43], v[64:65] op_sel:[1,1,0] op_sel_hi:[1,0,1] neg_hi:[0,1,0]
	v_pk_add_f32 v[42:43], v[68:69], v[48:49] neg_hi:[0,1]
	v_pk_add_f32 v[44:45], v[68:69], v[48:49] neg_lo:[0,1]
	s_nop 0
	v_pk_mul_f32 v[48:49], v[42:43], v[44:45] op_sel:[0,0] op_sel_hi:[0,1]
	v_pk_fma_f32 v[48:49], v[42:43], v[44:45], v[48:49] op_sel:[1,1,0] op_sel_hi:[1,0,1] neg_hi:[0,1,0]
	v_pk_add_f32 v[42:43], v[70:71], v[46:47] neg_hi:[0,1]
	v_pk_add_f32 v[44:45], v[70:71], v[46:47] neg_lo:[0,1]
	v_pk_add_f32 v[36:37], v[36:37], v[64:65] op_sel:[1,0] op_sel_hi:[0,1] neg_lo:[0,1] neg_hi:[1,1]
	s_nop 0
	v_pk_mul_f32 v[46:47], v[42:43], v[44:45] op_sel:[0,0] op_sel_hi:[0,1]
	v_pk_fma_f32 v[46:47], v[42:43], v[44:45], v[46:47] op_sel:[1,1,0] op_sel_hi:[1,0,1] neg_hi:[0,1,0]
	v_pk_add_f32 v[42:43], v[62:63], v[52:53]
	v_pk_add_f32 v[32:33], v[32:33], v[46:47] op_sel:[1,0] op_sel_hi:[0,1] neg_lo:[0,1] neg_hi:[1,1]
	v_pk_add_f32 v[44:45], v[62:63], v[52:53] neg_lo:[0,1] neg_hi:[0,1]
	v_pk_add_f32 v[46:47], v[54:55], v[38:39]
	v_pk_add_f32 v[38:39], v[54:55], v[38:39] neg_lo:[0,1] neg_hi:[0,1]
	v_pk_add_f32 v[34:35], v[34:35], v[48:49] op_sel:[1,0] op_sel_hi:[0,1] neg_lo:[0,1] neg_hi:[1,1]
	v_pk_add_f32 v[48:49], v[42:43], v[46:47]
	v_pk_add_f32 v[42:43], v[42:43], v[46:47] neg_lo:[0,1] neg_hi:[0,1]
	v_pk_add_f32 v[46:47], v[44:45], v[38:39] op_sel:[0,1] op_sel_hi:[1,0] neg_hi:[0,1]
	v_pk_add_f32 v[38:39], v[44:45], v[38:39] op_sel:[0,1] op_sel_hi:[1,0] neg_lo:[0,1]
	v_pk_add_f32 v[44:45], v[60:61], v[50:51]
	v_pk_add_f32 v[50:51], v[60:61], v[50:51] neg_lo:[0,1] neg_hi:[0,1]
	v_pk_add_f32 v[52:53], v[88:89], v[36:37]
	v_pk_add_f32 v[36:37], v[88:89], v[36:37] neg_lo:[0,1] neg_hi:[0,1]
	v_pk_add_f32 v[54:55], v[44:45], v[52:53]
	v_pk_add_f32 v[44:45], v[44:45], v[52:53] neg_lo:[0,1] neg_hi:[0,1]
	v_pk_add_f32 v[52:53], v[50:51], v[36:37] op_sel:[0,1] op_sel_hi:[1,0] neg_hi:[0,1]
	v_pk_add_f32 v[36:37], v[50:51], v[36:37] op_sel:[0,1] op_sel_hi:[1,0] neg_lo:[0,1]
	v_pk_add_f32 v[50:51], v[58:59], v[72:73]
	v_pk_add_f32 v[58:59], v[58:59], v[72:73] neg_lo:[0,1] neg_hi:[0,1]
	v_pk_add_f32 v[60:61], v[86:87], v[34:35]
	v_pk_add_f32 v[34:35], v[86:87], v[34:35] neg_lo:[0,1] neg_hi:[0,1]
	v_pk_add_f32 v[62:63], v[50:51], v[60:61]
	v_pk_add_f32 v[50:51], v[50:51], v[60:61] neg_lo:[0,1] neg_hi:[0,1]
	v_pk_add_f32 v[60:61], v[58:59], v[34:35] op_sel:[0,1] op_sel_hi:[1,0] neg_hi:[0,1]
	v_pk_add_f32 v[34:35], v[58:59], v[34:35] op_sel:[0,1] op_sel_hi:[1,0] neg_lo:[0,1]
	v_pk_add_f32 v[58:59], v[56:57], v[40:41]
	v_pk_add_f32 v[40:41], v[56:57], v[40:41] neg_lo:[0,1] neg_hi:[0,1]
	v_pk_add_f32 v[56:57], v[84:85], v[32:33]
	v_pk_add_f32 v[32:33], v[84:85], v[32:33] neg_lo:[0,1] neg_hi:[0,1]
	v_pk_add_f32 v[64:65], v[58:59], v[56:57]
	v_pk_add_f32 v[56:57], v[58:59], v[56:57] neg_lo:[0,1] neg_hi:[0,1]
	v_pk_add_f32 v[58:59], v[40:41], v[32:33] op_sel:[0,1] op_sel_hi:[1,0] neg_hi:[0,1]
	v_pk_add_f32 v[32:33], v[40:41], v[32:33] op_sel:[0,1] op_sel_hi:[1,0] neg_lo:[0,1]
	v_pk_mul_f32 v[40:41], v[52:53], s[6:7] op_sel:[0,0] op_sel_hi:[0,1]
	v_pk_fma_f32 v[40:41], v[52:53], s[6:7], v[40:41] op_sel:[1,1,0] op_sel_hi:[1,0,1] neg_lo:[0,1,0]
	v_pk_mul_f32 v[52:53], v[36:37], s[10:11] op_sel:[0,0] op_sel_hi:[0,1]
	v_pk_fma_f32 v[52:53], v[36:37], s[10:11], v[52:53] op_sel:[1,1,0] op_sel_hi:[1,0,1] neg_lo:[0,1,0]
	v_pk_add_f32 v[36:37], v[60:61], v[60:61] op_sel:[0,1] op_sel_hi:[1,0] neg_hi:[0,1]
	v_pk_add_f32 v[44:45], v[44:45], v[44:45] op_sel:[0,1] op_sel_hi:[1,0] neg_hi:[0,1]
	s_nop 0
	v_pk_mul_f32 v[60:61], v[58:59], s[10:11] op_sel:[0,0] op_sel_hi:[0,1]
	v_pk_fma_f32 v[60:61], v[58:59], s[10:11], v[60:61] op_sel:[1,1,0] op_sel_hi:[1,0,1] neg_lo:[0,1,0]
	v_pk_mul_f32 v[58:59], v[32:33], s[14:15] op_sel:[0,0] op_sel_hi:[0,1]
	v_pk_fma_f32 v[58:59], v[32:33], s[14:15], v[58:59] op_sel:[1,1,0] op_sel_hi:[1,0,1] neg_lo:[0,1,0]
	v_pk_add_f32 v[32:33], v[48:49], v[62:63]
	v_pk_mul_f32 v[36:37], v[36:37], s[8:9]
	v_pk_add_f32 v[48:49], v[48:49], v[62:63] neg_lo:[0,1] neg_hi:[0,1]
	v_pk_add_f32 v[62:63], v[54:55], v[64:65]
	v_pk_add_f32 v[54:55], v[54:55], v[64:65] neg_lo:[0,1] neg_hi:[0,1]
	v_pk_mul_f32 v[44:45], v[44:45], s[8:9]
	v_pk_add_f32 v[34:35], v[34:35], v[34:35] op_sel:[0,1] op_sel_hi:[1,0] neg_lo:[0,1]
	v_pk_add_f32 v[56:57], v[56:57], v[56:57] op_sel:[0,1] op_sel_hi:[1,0] neg_lo:[0,1]
	v_pk_add_f32 v[64:65], v[32:33], v[62:63]
	v_pk_add_f32 v[32:33], v[32:33], v[62:63] neg_lo:[0,1] neg_hi:[0,1]
	v_pk_add_f32 v[62:63], v[48:49], v[54:55] op_sel:[0,1] op_sel_hi:[1,0] neg_hi:[0,1]
	v_pk_add_f32 v[48:49], v[48:49], v[54:55] op_sel:[0,1] op_sel_hi:[1,0] neg_lo:[0,1]
	v_pk_add_f32 v[54:55], v[46:47], v[36:37]
	v_pk_add_f32 v[36:37], v[46:47], v[36:37] neg_lo:[0,1] neg_hi:[0,1]
	v_pk_add_f32 v[46:47], v[40:41], v[60:61]
	v_pk_add_f32 v[40:41], v[40:41], v[60:61] neg_lo:[0,1] neg_hi:[0,1]
	v_pk_mul_f32 v[34:35], v[34:35], s[12:13]
	v_pk_mul_f32 v[56:57], v[56:57], s[12:13]
	v_pk_add_f32 v[60:61], v[54:55], v[46:47]
	v_pk_add_f32 v[46:47], v[54:55], v[46:47] neg_lo:[0,1] neg_hi:[0,1]
	v_pk_add_f32 v[54:55], v[36:37], v[40:41] op_sel:[0,1] op_sel_hi:[1,0] neg_hi:[0,1]
	v_pk_add_f32 v[36:37], v[36:37], v[40:41] op_sel:[0,1] op_sel_hi:[1,0] neg_lo:[0,1]
	v_pk_add_f32 v[40:41], v[42:43], v[50:51] op_sel:[0,1] op_sel_hi:[1,0] neg_hi:[0,1]
	v_pk_add_f32 v[42:43], v[42:43], v[50:51] op_sel:[0,1] op_sel_hi:[1,0] neg_lo:[0,1]
	v_pk_add_f32 v[50:51], v[44:45], v[56:57]
	v_pk_add_f32 v[44:45], v[44:45], v[56:57] neg_lo:[0,1] neg_hi:[0,1]
	v_pk_add_f32 v[56:57], v[50:51], v[40:41]
	v_pk_add_f32 v[40:41], v[40:41], v[50:51] neg_lo:[0,1] neg_hi:[0,1]
	v_pk_add_f32 v[50:51], v[42:43], v[44:45] op_sel:[0,1] op_sel_hi:[1,0] neg_hi:[0,1]
	v_pk_add_f32 v[42:43], v[42:43], v[44:45] op_sel:[0,1] op_sel_hi:[1,0] neg_lo:[0,1]
	v_pk_add_f32 v[44:45], v[38:39], v[34:35]
	v_pk_add_f32 v[34:35], v[38:39], v[34:35] neg_lo:[0,1] neg_hi:[0,1]
	v_pk_add_f32 v[38:39], v[52:53], v[58:59]
	v_pk_add_f32 v[52:53], v[52:53], v[58:59] neg_lo:[0,1] neg_hi:[0,1]
	v_pk_add_f32 v[58:59], v[44:45], v[38:39]
	v_pk_add_f32 v[38:39], v[44:45], v[38:39] neg_lo:[0,1] neg_hi:[0,1]
	v_pk_add_f32 v[44:45], v[34:35], v[52:53] op_sel:[0,1] op_sel_hi:[1,0] neg_hi:[0,1]
	v_pk_add_f32 v[34:35], v[34:35], v[52:53] op_sel:[0,1] op_sel_hi:[1,0] neg_lo:[0,1]
	v_pk_mul_f32 v[52:53], v[60:61], v[30:31] op_sel:[0,0] op_sel_hi:[0,1]
	v_pk_fma_f32 v[52:53], v[60:61], v[30:31], v[52:53] op_sel:[1,1,0] op_sel_hi:[1,0,1] neg_lo:[0,1,0]
	v_pk_mul_f32 v[30:31], v[56:57], v[28:29] op_sel:[0,0] op_sel_hi:[0,1]
	v_pk_fma_f32 v[30:31], v[56:57], v[28:29], v[30:31] op_sel:[1,1,0] op_sel_hi:[1,0,1] neg_lo:[0,1,0]
	v_pk_mul_f32 v[28:29], v[58:59], v[26:27] op_sel:[0,0] op_sel_hi:[0,1]
	v_pk_fma_f32 v[28:29], v[58:59], v[26:27], v[28:29] op_sel:[1,1,0] op_sel_hi:[1,0,1] neg_lo:[0,1,0]
	v_pk_mul_f32 v[26:27], v[62:63], v[24:25] op_sel:[0,0] op_sel_hi:[0,1]
	v_pk_fma_f32 v[26:27], v[62:63], v[24:25], v[26:27] op_sel:[1,1,0] op_sel_hi:[1,0,1] neg_lo:[0,1,0]
	v_pk_mul_f32 v[24:25], v[54:55], v[20:21] op_sel:[0,0] op_sel_hi:[0,1]
	v_pk_fma_f32 v[24:25], v[54:55], v[20:21], v[24:25] op_sel:[1,1,0] op_sel_hi:[1,0,1] neg_lo:[0,1,0]
	v_pk_mul_f32 v[20:21], v[50:51], v[16:17] op_sel:[0,0] op_sel_hi:[0,1]
	v_pk_fma_f32 v[20:21], v[50:51], v[16:17], v[20:21] op_sel:[1,1,0] op_sel_hi:[1,0,1] neg_lo:[0,1,0]
	s_nop 0
	v_pk_mul_f32 v[16:17], v[44:45], v[10:11] op_sel:[0,0] op_sel_hi:[0,1]
	v_pk_fma_f32 v[16:17], v[44:45], v[10:11], v[16:17] op_sel:[1,1,0] op_sel_hi:[1,0,1] neg_lo:[0,1,0]
	v_pk_mul_f32 v[10:11], v[32:33], v[22:23] op_sel:[0,0] op_sel_hi:[0,1]
	v_pk_fma_f32 v[10:11], v[32:33], v[22:23], v[10:11] op_sel:[1,1,0] op_sel_hi:[1,0,1] neg_lo:[0,1,0]
	ds_write_b64 v1, v[10:11] offset:17472
	v_pk_mul_f32 v[10:11], v[46:47], v[18:19] op_sel:[0,0] op_sel_hi:[0,1]
	v_pk_fma_f32 v[10:11], v[46:47], v[18:19], v[10:11] op_sel:[1,1,0] op_sel_hi:[1,0,1] neg_lo:[0,1,0]
	ds_write_b64 v1, v[10:11] offset:19656
	v_pk_mul_f32 v[10:11], v[40:41], v[12:13] op_sel:[0,0] op_sel_hi:[0,1]
	v_pk_fma_f32 v[10:11], v[40:41], v[12:13], v[10:11] op_sel:[1,1,0] op_sel_hi:[1,0,1] neg_lo:[0,1,0]
	ds_write_b64 v1, v[10:11] offset:21840
	v_pk_mul_f32 v[10:11], v[38:39], v[14:15] op_sel:[0,0] op_sel_hi:[0,1]
	v_pk_fma_f32 v[10:11], v[38:39], v[14:15], v[10:11] op_sel:[1,1,0] op_sel_hi:[1,0,1] neg_lo:[0,1,0]
	ds_write_b64 v1, v[10:11] offset:24024
	v_pk_mul_f32 v[10:11], v[48:49], v[6:7] op_sel:[0,0] op_sel_hi:[0,1]
	v_pk_fma_f32 v[10:11], v[48:49], v[6:7], v[10:11] op_sel:[1,1,0] op_sel_hi:[1,0,1] neg_lo:[0,1,0]
	v_pk_mul_f32 v[6:7], v[36:37], v[8:9] op_sel:[0,0] op_sel_hi:[0,1]
	v_pk_fma_f32 v[6:7], v[36:37], v[8:9], v[6:7] op_sel:[1,1,0] op_sel_hi:[1,0,1] neg_lo:[0,1,0]
	ds_write_b64 v1, v[6:7] offset:28392
	v_pk_mul_f32 v[6:7], v[42:43], v[4:5] op_sel:[0,0] op_sel_hi:[0,1]
	v_pk_fma_f32 v[6:7], v[42:43], v[4:5], v[6:7] op_sel:[1,1,0] op_sel_hi:[1,0,1] neg_lo:[0,1,0]
	v_pk_mul_f32 v[4:5], v[34:35], v[2:3] op_sel:[0,0] op_sel_hi:[0,1]
	v_pk_fma_f32 v[4:5], v[34:35], v[2:3], v[4:5] op_sel:[1,1,0] op_sel_hi:[1,0,1] neg_lo:[0,1,0]
	ds_write_b64 v1, v[64:65]
	ds_write_b64 v1, v[52:53] offset:2184
	ds_write_b64 v1, v[30:31] offset:4368
	ds_write_b64 v1, v[28:29] offset:6552
	ds_write_b64 v1, v[26:27] offset:8736
	ds_write_b64 v1, v[24:25] offset:10920
	ds_write_b64 v1, v[20:21] offset:13104
	ds_write_b64 v1, v[16:17] offset:15288
	ds_write_b64 v1, v[10:11] offset:26208
	ds_write_b64 v1, v[6:7] offset:30576
	ds_write_b64 v1, v[4:5] offset:32760
	s_waitcnt lgkmcnt(0)
	s_barrier
	ds_read2_b64 v[2:5], v96 offset1:16
	ds_read2_b64 v[6:9], v96 offset0:32 offset1:48
	ds_read2_b64 v[10:13], v96 offset0:64 offset1:80
	ds_read2_b64 v[14:17], v96 offset0:128 offset1:144
	ds_read2_b64 v[18:21], v96 offset0:96 offset1:112
	ds_read2_b64 v[22:25], v96 offset0:192 offset1:208
	ds_read2_b64 v[26:29], v96 offset0:160 offset1:176
	ds_read2_b64 v[30:33], v96 offset0:224 offset1:240
	s_waitcnt lgkmcnt(4)
	v_pk_add_f32 v[34:35], v[2:3], v[14:15]
	v_pk_add_f32 v[2:3], v[2:3], v[14:15] neg_lo:[0,1] neg_hi:[0,1]
	s_waitcnt lgkmcnt(2)
	v_pk_add_f32 v[14:15], v[10:11], v[22:23]
	v_pk_add_f32 v[10:11], v[10:11], v[22:23] neg_lo:[0,1] neg_hi:[0,1]
	v_pk_add_f32 v[22:23], v[34:35], v[14:15]
	v_pk_add_f32 v[14:15], v[34:35], v[14:15] neg_lo:[0,1] neg_hi:[0,1]
	v_pk_add_f32 v[34:35], v[2:3], v[10:11] op_sel:[0,1] op_sel_hi:[1,0] neg_hi:[0,1]
	v_pk_add_f32 v[2:3], v[2:3], v[10:11] op_sel:[0,1] op_sel_hi:[1,0] neg_lo:[0,1]
	v_pk_add_f32 v[10:11], v[4:5], v[16:17]
	v_pk_add_f32 v[4:5], v[4:5], v[16:17] neg_lo:[0,1] neg_hi:[0,1]
	v_pk_add_f32 v[16:17], v[12:13], v[24:25]
	v_pk_add_f32 v[12:13], v[12:13], v[24:25] neg_lo:[0,1] neg_hi:[0,1]
	v_pk_add_f32 v[24:25], v[10:11], v[16:17]
	v_pk_add_f32 v[10:11], v[10:11], v[16:17] neg_lo:[0,1] neg_hi:[0,1]
	v_pk_add_f32 v[16:17], v[4:5], v[12:13] op_sel:[0,1] op_sel_hi:[1,0] neg_hi:[0,1]
	v_pk_add_f32 v[4:5], v[4:5], v[12:13] op_sel:[0,1] op_sel_hi:[1,0] neg_lo:[0,1]
	s_waitcnt lgkmcnt(1)
	v_pk_add_f32 v[12:13], v[6:7], v[26:27]
	v_pk_add_f32 v[6:7], v[6:7], v[26:27] neg_lo:[0,1] neg_hi:[0,1]
	s_waitcnt lgkmcnt(0)
	v_pk_add_f32 v[26:27], v[18:19], v[30:31]
	v_pk_add_f32 v[18:19], v[18:19], v[30:31] neg_lo:[0,1] neg_hi:[0,1]
	v_pk_add_f32 v[30:31], v[12:13], v[26:27]
	v_pk_add_f32 v[12:13], v[12:13], v[26:27] neg_lo:[0,1] neg_hi:[0,1]
	v_pk_add_f32 v[26:27], v[6:7], v[18:19] op_sel:[0,1] op_sel_hi:[1,0] neg_hi:[0,1]
	v_pk_add_f32 v[6:7], v[6:7], v[18:19] op_sel:[0,1] op_sel_hi:[1,0] neg_lo:[0,1]
	v_pk_add_f32 v[18:19], v[8:9], v[28:29]
	v_pk_add_f32 v[8:9], v[8:9], v[28:29] neg_lo:[0,1] neg_hi:[0,1]
	v_pk_add_f32 v[28:29], v[20:21], v[32:33]
	v_pk_add_f32 v[20:21], v[20:21], v[32:33] neg_lo:[0,1] neg_hi:[0,1]
	v_pk_add_f32 v[32:33], v[18:19], v[28:29]
	v_pk_add_f32 v[18:19], v[18:19], v[28:29] neg_lo:[0,1] neg_hi:[0,1]
	v_pk_add_f32 v[28:29], v[8:9], v[20:21] op_sel:[0,1] op_sel_hi:[1,0] neg_hi:[0,1]
	v_pk_add_f32 v[8:9], v[8:9], v[20:21] op_sel:[0,1] op_sel_hi:[1,0] neg_lo:[0,1]
	v_pk_mul_f32 v[20:21], v[16:17], s[6:7] op_sel:[0,0] op_sel_hi:[0,1]
	v_pk_fma_f32 v[20:21], v[16:17], s[6:7], v[20:21] op_sel:[1,1,0] op_sel_hi:[1,0,1] neg_lo:[0,1,0]
	v_pk_mul_f32 v[16:17], v[4:5], s[10:11] op_sel:[0,0] op_sel_hi:[0,1]
	v_pk_fma_f32 v[16:17], v[4:5], s[10:11], v[16:17] op_sel:[1,1,0] op_sel_hi:[1,0,1] neg_lo:[0,1,0]
	v_pk_add_f32 v[4:5], v[26:27], v[26:27] op_sel:[0,1] op_sel_hi:[1,0] neg_hi:[0,1]
	v_pk_add_f32 v[10:11], v[10:11], v[10:11] op_sel:[0,1] op_sel_hi:[1,0] neg_hi:[0,1]
	s_nop 0
	v_pk_mul_f32 v[26:27], v[28:29], s[10:11] op_sel:[0,0] op_sel_hi:[0,1]
	v_pk_fma_f32 v[26:27], v[28:29], s[10:11], v[26:27] op_sel:[1,1,0] op_sel_hi:[1,0,1] neg_lo:[0,1,0]
	v_pk_mul_f32 v[28:29], v[8:9], s[14:15] op_sel:[0,0] op_sel_hi:[0,1]
	v_pk_fma_f32 v[28:29], v[8:9], s[14:15], v[28:29] op_sel:[1,1,0] op_sel_hi:[1,0,1] neg_lo:[0,1,0]
	v_pk_add_f32 v[8:9], v[22:23], v[30:31]
	v_pk_mul_f32 v[4:5], v[4:5], s[8:9]
	v_pk_add_f32 v[22:23], v[22:23], v[30:31] neg_lo:[0,1] neg_hi:[0,1]
	v_pk_add_f32 v[30:31], v[24:25], v[32:33]
	v_pk_add_f32 v[24:25], v[24:25], v[32:33] neg_lo:[0,1] neg_hi:[0,1]
	v_pk_add_f32 v[18:19], v[18:19], v[18:19] op_sel:[0,1] op_sel_hi:[1,0] neg_lo:[0,1]
	v_pk_add_f32 v[32:33], v[8:9], v[30:31]
	v_pk_add_f32 v[30:31], v[8:9], v[30:31] neg_lo:[0,1] neg_hi:[0,1]
	v_pk_add_f32 v[36:37], v[22:23], v[24:25] op_sel:[0,1] op_sel_hi:[1,0] neg_hi:[0,1]
	v_pk_add_f32 v[22:23], v[22:23], v[24:25] op_sel:[0,1] op_sel_hi:[1,0] neg_lo:[0,1]
	v_pk_add_f32 v[8:9], v[34:35], v[4:5]
	v_pk_add_f32 v[4:5], v[34:35], v[4:5] neg_lo:[0,1] neg_hi:[0,1]
	v_pk_add_f32 v[24:25], v[20:21], v[26:27]
	v_pk_add_f32 v[20:21], v[20:21], v[26:27] neg_lo:[0,1] neg_hi:[0,1]
	v_pk_mul_f32 v[10:11], v[10:11], s[8:9]
	v_pk_add_f32 v[6:7], v[6:7], v[6:7] op_sel:[0,1] op_sel_hi:[1,0] neg_lo:[0,1]
	v_pk_mul_f32 v[18:19], v[18:19], s[12:13]
	v_pk_add_f32 v[26:27], v[8:9], v[24:25]
	v_pk_add_f32 v[24:25], v[8:9], v[24:25] neg_lo:[0,1] neg_hi:[0,1]
	v_pk_add_f32 v[34:35], v[4:5], v[20:21] op_sel:[0,1] op_sel_hi:[1,0] neg_hi:[0,1]
	v_pk_add_f32 v[20:21], v[4:5], v[20:21] op_sel:[0,1] op_sel_hi:[1,0] neg_lo:[0,1]
	v_pk_add_f32 v[4:5], v[14:15], v[12:13] op_sel:[0,1] op_sel_hi:[1,0] neg_hi:[0,1]
	v_pk_add_f32 v[8:9], v[14:15], v[12:13] op_sel:[0,1] op_sel_hi:[1,0] neg_lo:[0,1]
	v_pk_add_f32 v[12:13], v[10:11], v[18:19]
	v_pk_mul_f32 v[6:7], v[6:7], s[12:13]
	v_pk_add_f32 v[10:11], v[10:11], v[18:19] neg_lo:[0,1] neg_hi:[0,1]
	v_pk_add_f32 v[14:15], v[12:13], v[4:5]
	v_pk_add_f32 v[12:13], v[4:5], v[12:13] neg_lo:[0,1] neg_hi:[0,1]
	v_pk_add_f32 v[4:5], v[2:3], v[6:7]
	v_pk_add_f32 v[2:3], v[2:3], v[6:7] neg_lo:[0,1] neg_hi:[0,1]
	v_mov_b32_e32 v1, v0
	v_pk_add_f32 v[18:19], v[8:9], v[10:11] op_sel:[0,1] op_sel_hi:[1,0] neg_hi:[0,1]
	v_pk_add_f32 v[10:11], v[8:9], v[10:11] op_sel:[0,1] op_sel_hi:[1,0] neg_lo:[0,1]
	v_pk_add_f32 v[8:9], v[16:17], v[28:29] neg_lo:[0,1] neg_hi:[0,1]
	v_pk_add_f32 v[6:7], v[16:17], v[28:29]
	v_pk_add_f32 v[38:39], v[2:3], v[8:9] op_sel:[0,1] op_sel_hi:[1,0] neg_hi:[0,1]
	v_pk_add_f32 v[40:41], v[2:3], v[8:9] op_sel:[0,1] op_sel_hi:[1,0] neg_lo:[0,1]
	v_ashrrev_i32_e32 v2, 4, v1
	v_lshlrev_b32_e32 v44, 3, v2
	v_add_u32_e32 v45, 0x8800, v44
	v_and_b32_e32 v1, 15, v1
	v_pk_add_f32 v[16:17], v[4:5], v[6:7]
	v_pk_add_f32 v[28:29], v[4:5], v[6:7] neg_lo:[0,1] neg_hi:[0,1]
	v_mad_u32_u24 v1, v1, s5, v44
	ds_read_b64 v[6:7], v45 offset:128
	s_waitcnt lgkmcnt(0)
	v_pk_mul_f32 v[42:43], v[26:27], v[6:7] op_sel:[0,0] op_sel_hi:[0,1]
	v_pk_fma_f32 v[42:43], v[26:27], v[6:7], v[42:43] op_sel:[1,1,0] op_sel_hi:[1,0,1] neg_lo:[0,1,0]
	v_pk_mul_f32 v[2:3], v[6:7], v[6:7] op_sel:[0,0] op_sel_hi:[0,1]
	v_pk_fma_f32 v[2:3], v[6:7], v[6:7], v[2:3] op_sel:[1,1,0] op_sel_hi:[1,0,1] neg_lo:[0,1,0]
	v_pk_mul_f32 v[26:27], v[14:15], v[2:3] op_sel:[0,0] op_sel_hi:[0,1]
	v_pk_fma_f32 v[26:27], v[14:15], v[2:3], v[26:27] op_sel:[1,1,0] op_sel_hi:[1,0,1] neg_lo:[0,1,0]
	v_pk_mul_f32 v[4:5], v[2:3], v[6:7] op_sel:[0,0] op_sel_hi:[0,1]
	v_pk_fma_f32 v[4:5], v[2:3], v[6:7], v[4:5] op_sel:[1,1,0] op_sel_hi:[1,0,1] neg_lo:[0,1,0]
	v_pk_mul_f32 v[14:15], v[16:17], v[4:5] op_sel:[0,0] op_sel_hi:[0,1]
	v_pk_fma_f32 v[14:15], v[16:17], v[4:5], v[14:15] op_sel:[1,1,0] op_sel_hi:[1,0,1] neg_lo:[0,1,0]
	ds_write2_b64 v1, v[26:27], v[14:15] offset0:32 offset1:48
	v_pk_mul_f32 v[2:3], v[4:5], v[6:7] op_sel:[0,0] op_sel_hi:[0,1]
	v_pk_fma_f32 v[2:3], v[4:5], v[6:7], v[2:3] op_sel:[1,1,0] op_sel_hi:[1,0,1] neg_lo:[0,1,0]
	v_pk_mul_f32 v[14:15], v[36:37], v[2:3] op_sel:[0,0] op_sel_hi:[0,1]
	v_pk_fma_f32 v[14:15], v[36:37], v[2:3], v[14:15] op_sel:[1,1,0] op_sel_hi:[1,0,1] neg_lo:[0,1,0]
	v_pk_mul_f32 v[4:5], v[2:3], v[6:7] op_sel:[0,0] op_sel_hi:[0,1]
	v_pk_fma_f32 v[4:5], v[2:3], v[6:7], v[4:5] op_sel:[1,1,0] op_sel_hi:[1,0,1] neg_lo:[0,1,0]
	v_pk_mul_f32 v[16:17], v[34:35], v[4:5] op_sel:[0,0] op_sel_hi:[0,1]
	v_pk_fma_f32 v[16:17], v[34:35], v[4:5], v[16:17] op_sel:[1,1,0] op_sel_hi:[1,0,1] neg_lo:[0,1,0]
	ds_write2_b64 v1, v[14:15], v[16:17] offset0:64 offset1:80
	v_pk_mul_f32 v[2:3], v[4:5], v[6:7] op_sel:[0,0] op_sel_hi:[0,1]
	v_pk_fma_f32 v[2:3], v[4:5], v[6:7], v[2:3] op_sel:[1,1,0] op_sel_hi:[1,0,1] neg_lo:[0,1,0]
	v_pk_mul_f32 v[14:15], v[18:19], v[2:3] op_sel:[0,0] op_sel_hi:[0,1]
	v_pk_fma_f32 v[14:15], v[18:19], v[2:3], v[14:15] op_sel:[1,1,0] op_sel_hi:[1,0,1] neg_lo:[0,1,0]
	v_pk_mul_f32 v[4:5], v[2:3], v[6:7] op_sel:[0,0] op_sel_hi:[0,1]
	v_pk_fma_f32 v[4:5], v[2:3], v[6:7], v[4:5] op_sel:[1,1,0] op_sel_hi:[1,0,1] neg_lo:[0,1,0]
	v_pk_mul_f32 v[16:17], v[38:39], v[4:5] op_sel:[0,0] op_sel_hi:[0,1]
	v_pk_fma_f32 v[16:17], v[38:39], v[4:5], v[16:17] op_sel:[1,1,0] op_sel_hi:[1,0,1] neg_lo:[0,1,0]
	ds_write2_b64 v1, v[14:15], v[16:17] offset0:96 offset1:112
	v_pk_mul_f32 v[2:3], v[4:5], v[6:7] op_sel:[0,0] op_sel_hi:[0,1]
	v_pk_fma_f32 v[2:3], v[4:5], v[6:7], v[2:3] op_sel:[1,1,0] op_sel_hi:[1,0,1] neg_lo:[0,1,0]
	v_pk_mul_f32 v[14:15], v[30:31], v[2:3] op_sel:[0,0] op_sel_hi:[0,1]
	v_pk_fma_f32 v[14:15], v[30:31], v[2:3], v[14:15] op_sel:[1,1,0] op_sel_hi:[1,0,1] neg_lo:[0,1,0]
	v_pk_mul_f32 v[4:5], v[2:3], v[6:7] op_sel:[0,0] op_sel_hi:[0,1]
	v_pk_fma_f32 v[4:5], v[2:3], v[6:7], v[4:5] op_sel:[1,1,0] op_sel_hi:[1,0,1] neg_lo:[0,1,0]
	v_pk_mul_f32 v[16:17], v[24:25], v[4:5] op_sel:[0,0] op_sel_hi:[0,1]
	v_pk_fma_f32 v[16:17], v[24:25], v[4:5], v[16:17] op_sel:[1,1,0] op_sel_hi:[1,0,1] neg_lo:[0,1,0]
	ds_write2_b64 v1, v[14:15], v[16:17] offset0:128 offset1:144
	v_pk_mul_f32 v[2:3], v[4:5], v[6:7] op_sel:[0,0] op_sel_hi:[0,1]
	v_pk_fma_f32 v[2:3], v[4:5], v[6:7], v[2:3] op_sel:[1,1,0] op_sel_hi:[1,0,1] neg_lo:[0,1,0]
	v_pk_mul_f32 v[14:15], v[12:13], v[2:3] op_sel:[0,0] op_sel_hi:[0,1]
	v_pk_fma_f32 v[14:15], v[12:13], v[2:3], v[14:15] op_sel:[1,1,0] op_sel_hi:[1,0,1] neg_lo:[0,1,0]
	v_pk_mul_f32 v[4:5], v[2:3], v[6:7] op_sel:[0,0] op_sel_hi:[0,1]
	v_pk_fma_f32 v[4:5], v[2:3], v[6:7], v[4:5] op_sel:[1,1,0] op_sel_hi:[1,0,1] neg_lo:[0,1,0]
	v_pk_mul_f32 v[12:13], v[28:29], v[4:5] op_sel:[0,0] op_sel_hi:[0,1]
	v_pk_fma_f32 v[12:13], v[28:29], v[4:5], v[12:13] op_sel:[1,1,0] op_sel_hi:[1,0,1] neg_lo:[0,1,0]
	ds_write2_b64 v1, v[32:33], v[42:43] offset1:16
	ds_write2_b64 v1, v[14:15], v[12:13] offset0:160 offset1:176
	v_pk_mul_f32 v[2:3], v[4:5], v[6:7] op_sel:[0,0] op_sel_hi:[0,1]
	v_pk_fma_f32 v[2:3], v[4:5], v[6:7], v[2:3] op_sel:[1,1,0] op_sel_hi:[1,0,1] neg_lo:[0,1,0]
	v_pk_mul_f32 v[12:13], v[22:23], v[2:3] op_sel:[0,0] op_sel_hi:[0,1]
	v_pk_fma_f32 v[12:13], v[22:23], v[2:3], v[12:13] op_sel:[1,1,0] op_sel_hi:[1,0,1] neg_lo:[0,1,0]
	v_pk_mul_f32 v[4:5], v[2:3], v[6:7] op_sel:[0,0] op_sel_hi:[0,1]
	v_pk_fma_f32 v[4:5], v[2:3], v[6:7], v[4:5] op_sel:[1,1,0] op_sel_hi:[1,0,1] neg_lo:[0,1,0]
	v_pk_mul_f32 v[8:9], v[20:21], v[4:5] op_sel:[0,0] op_sel_hi:[0,1]
	v_pk_fma_f32 v[8:9], v[20:21], v[4:5], v[8:9] op_sel:[1,1,0] op_sel_hi:[1,0,1] neg_lo:[0,1,0]
	ds_write2_b64 v1, v[12:13], v[8:9] offset0:192 offset1:208
	v_pk_mul_f32 v[2:3], v[4:5], v[6:7] op_sel:[0,0] op_sel_hi:[0,1]
	v_pk_fma_f32 v[2:3], v[4:5], v[6:7], v[2:3] op_sel:[1,1,0] op_sel_hi:[1,0,1] neg_lo:[0,1,0]
	v_pk_mul_f32 v[16:17], v[10:11], v[2:3] op_sel:[0,0] op_sel_hi:[0,1]
	v_pk_fma_f32 v[16:17], v[10:11], v[2:3], v[16:17] op_sel:[1,1,0] op_sel_hi:[1,0,1] neg_lo:[0,1,0]
	v_pk_mul_f32 v[4:5], v[2:3], v[6:7] op_sel:[0,0] op_sel_hi:[0,1]
	v_pk_fma_f32 v[4:5], v[2:3], v[6:7], v[4:5] op_sel:[1,1,0] op_sel_hi:[1,0,1] neg_lo:[0,1,0]
	v_pk_mul_f32 v[14:15], v[40:41], v[4:5] op_sel:[0,0] op_sel_hi:[0,1]
	v_pk_fma_f32 v[14:15], v[40:41], v[4:5], v[14:15] op_sel:[1,1,0] op_sel_hi:[1,0,1] neg_lo:[0,1,0]
	ds_write2_b64 v1, v[16:17], v[14:15] offset0:224 offset1:240
	v_mov_b32_e32 v1, v0
	s_waitcnt lgkmcnt(0)
	s_barrier
	v_mov_b32_e32 v53, 0
	v_and_b32_e32 v2, 15, v1
	v_and_b32_e32 v1, 0x1ffffff0, v1
	v_lshlrev_b32_e32 v1, 3, v1
	v_mad_u32_u24 v1, v2, s5, v1
	ds_read2_b64 v[2:5], v1 offset1:1
	ds_read2_b64 v[6:9], v1 offset0:2 offset1:3
	ds_read2_b64 v[10:13], v1 offset0:8 offset1:9
	ds_read2_b64 v[18:21], v1 offset0:4 offset1:5
	ds_read2_b64 v[22:25], v1 offset0:6 offset1:7
	ds_read2_b64 v[26:29], v1 offset0:12 offset1:13
	ds_read2_b64 v[30:33], v1 offset0:10 offset1:11
	ds_read2_b64 v[34:37], v1 offset0:14 offset1:15
	s_waitcnt lgkmcnt(5)
	v_pk_add_f32 v[14:15], v[2:3], v[10:11]
	v_pk_add_f32 v[2:3], v[2:3], v[10:11] neg_lo:[0,1] neg_hi:[0,1]
	s_waitcnt lgkmcnt(2)
	v_pk_add_f32 v[10:11], v[18:19], v[26:27]
	v_pk_add_f32 v[18:19], v[18:19], v[26:27] neg_lo:[0,1] neg_hi:[0,1]
	v_pk_add_f32 v[26:27], v[14:15], v[10:11]
	v_pk_add_f32 v[16:17], v[14:15], v[10:11] neg_lo:[0,1] neg_hi:[0,1]
	v_pk_add_f32 v[14:15], v[2:3], v[18:19] op_sel:[0,1] op_sel_hi:[1,0] neg_hi:[0,1]
	v_pk_add_f32 v[18:19], v[2:3], v[18:19] op_sel:[0,1] op_sel_hi:[1,0] neg_lo:[0,1]
	v_pk_add_f32 v[2:3], v[4:5], v[12:13]
	v_pk_add_f32 v[10:11], v[20:21], v[28:29]
	v_pk_add_f32 v[4:5], v[4:5], v[12:13] neg_lo:[0,1] neg_hi:[0,1]
	v_pk_add_f32 v[12:13], v[20:21], v[28:29] neg_lo:[0,1] neg_hi:[0,1]
	v_pk_add_f32 v[28:29], v[2:3], v[10:11]
	v_pk_add_f32 v[2:3], v[2:3], v[10:11] neg_lo:[0,1] neg_hi:[0,1]
	v_pk_add_f32 v[10:11], v[4:5], v[12:13] op_sel:[0,1] op_sel_hi:[1,0] neg_hi:[0,1]
	v_pk_add_f32 v[4:5], v[4:5], v[12:13] op_sel:[0,1] op_sel_hi:[1,0] neg_lo:[0,1]
	s_waitcnt lgkmcnt(1)
	v_pk_add_f32 v[12:13], v[6:7], v[30:31]
	s_waitcnt lgkmcnt(0)
	v_pk_add_f32 v[20:21], v[22:23], v[34:35]
	v_pk_add_f32 v[2:3], v[2:3], v[2:3] op_sel:[0,1] op_sel_hi:[1,0] neg_hi:[0,1]
	v_pk_add_f32 v[6:7], v[6:7], v[30:31] neg_lo:[0,1] neg_hi:[0,1]
	v_pk_add_f32 v[22:23], v[22:23], v[34:35] neg_lo:[0,1] neg_hi:[0,1]
	v_pk_add_f32 v[30:31], v[12:13], v[20:21]
	v_pk_add_f32 v[20:21], v[12:13], v[20:21] neg_lo:[0,1] neg_hi:[0,1]
	v_pk_add_f32 v[12:13], v[6:7], v[22:23] op_sel:[0,1] op_sel_hi:[1,0] neg_hi:[0,1]
	v_pk_mul_f32 v[44:45], v[2:3], s[8:9]
	v_pk_add_f32 v[6:7], v[6:7], v[22:23] op_sel:[0,1] op_sel_hi:[1,0] neg_lo:[0,1]
	v_pk_add_f32 v[22:23], v[8:9], v[32:33]
	v_pk_add_f32 v[2:3], v[12:13], v[12:13] op_sel:[0,1] op_sel_hi:[1,0] neg_hi:[0,1]
	v_pk_add_f32 v[8:9], v[8:9], v[32:33] neg_lo:[0,1] neg_hi:[0,1]
	v_pk_add_f32 v[32:33], v[24:25], v[36:37]
	v_pk_mul_f32 v[12:13], v[2:3], s[8:9]
	v_pk_add_f32 v[2:3], v[6:7], v[6:7] op_sel:[0,1] op_sel_hi:[1,0] neg_lo:[0,1]
	v_pk_add_f32 v[24:25], v[24:25], v[36:37] neg_lo:[0,1] neg_hi:[0,1]
	v_pk_add_f32 v[34:35], v[22:23], v[32:33]
	v_pk_add_f32 v[32:33], v[22:23], v[32:33] neg_lo:[0,1] neg_hi:[0,1]
	v_pk_mul_f32 v[54:55], v[2:3], s[12:13]
	v_pk_add_f32 v[36:37], v[8:9], v[24:25] op_sel:[0,1] op_sel_hi:[1,0] neg_hi:[0,1]
	v_pk_add_f32 v[8:9], v[8:9], v[24:25] op_sel:[0,1] op_sel_hi:[1,0] neg_lo:[0,1]
	v_pk_mul_f32 v[22:23], v[4:5], s[10:11] op_sel:[0,0] op_sel_hi:[0,1]
	v_pk_fma_f32 v[22:23], v[4:5], s[10:11], v[22:23] op_sel:[1,1,0] op_sel_hi:[1,0,1] neg_lo:[0,1,0]
	v_pk_add_f32 v[4:5], v[28:29], v[34:35]
	v_pk_add_f32 v[2:3], v[32:33], v[32:33] op_sel:[0,1] op_sel_hi:[1,0] neg_lo:[0,1]
	v_pk_add_f32 v[28:29], v[28:29], v[34:35] neg_lo:[0,1] neg_hi:[0,1]
	v_pk_mul_f32 v[32:33], v[2:3], s[12:13]
	v_pk_add_f32 v[2:3], v[26:27], v[30:31]
	v_pk_add_f32 v[26:27], v[26:27], v[30:31] neg_lo:[0,1] neg_hi:[0,1]
	v_pk_mul_f32 v[24:25], v[10:11], s[6:7] op_sel:[0,0] op_sel_hi:[0,1]
	v_pk_fma_f32 v[24:25], v[10:11], s[6:7], v[24:25] op_sel:[1,1,0] op_sel_hi:[1,0,1] neg_lo:[0,1,0]
	v_pk_mul_f32 v[6:7], v[36:37], s[10:11] op_sel:[0,0] op_sel_hi:[0,1]
	v_pk_fma_f32 v[6:7], v[36:37], s[10:11], v[6:7] op_sel:[1,1,0] op_sel_hi:[1,0,1] neg_lo:[0,1,0]
	v_pk_mul_f32 v[56:57], v[8:9], s[14:15] op_sel:[0,0] op_sel_hi:[0,1]
	v_pk_fma_f32 v[56:57], v[8:9], s[14:15], v[56:57] op_sel:[1,1,0] op_sel_hi:[1,0,1] neg_lo:[0,1,0]
	v_pk_add_f32 v[10:11], v[2:3], v[4:5]
	v_lshlrev_b32_e32 v34, 2, v0
	v_pk_add_f32 v[4:5], v[2:3], v[4:5] neg_lo:[0,1] neg_hi:[0,1]
	v_pk_add_f32 v[8:9], v[26:27], v[28:29] op_sel:[0,1] op_sel_hi:[1,0] neg_hi:[0,1]
	v_pk_add_f32 v[2:3], v[26:27], v[28:29] op_sel:[0,1] op_sel_hi:[1,0] neg_lo:[0,1]
	v_pk_add_f32 v[26:27], v[14:15], v[12:13]
	v_pk_add_f32 v[28:29], v[24:25], v[6:7]
	v_add_u32_e32 v1, 0x400, v34
	v_pk_add_f32 v[14:15], v[14:15], v[12:13] neg_lo:[0,1] neg_hi:[0,1]
	v_pk_add_f32 v[30:31], v[24:25], v[6:7] neg_lo:[0,1] neg_hi:[0,1]
	v_pk_add_f32 v[12:13], v[26:27], v[28:29]
	v_pk_add_f32 v[6:7], v[26:27], v[28:29] neg_lo:[0,1] neg_hi:[0,1]
	v_add_u32_e32 v24, 0x800, v34
	v_add_u32_e32 v25, 0xc00, v34
	v_add_u32_e32 v26, 0x1000, v34
	v_add_u32_e32 v27, 0x1400, v34
	v_add_u32_e32 v28, 0x1800, v34
	v_add_u32_e32 v29, 0x1c00, v34
	v_add_u32_e32 v35, 0x2000, v34
	s_waitcnt vmcnt(0)
	v_mov_b32_e32 v1, v113
	s_nop 0
	v_mov_b32_e32 v36, v114
	v_mov_b32_e32 v37, v115
	v_mov_b32_e32 v38, v116
	v_mov_b32_e32 v39, v117
	v_mov_b32_e32 v40, v118
	v_mov_b32_e32 v41, v119
	v_mov_b32_e32 v42, v120
	v_add_u32_e32 v24, 0x2400, v34
	v_add_u32_e32 v25, 0x2800, v34
	v_add_u32_e32 v26, 0x2c00, v34
	v_add_u32_e32 v27, 0x3000, v34
	v_add_u32_e32 v28, 0x3400, v34
	v_add_u32_e32 v35, 0x3800, v34
	v_mov_b32_e32 v52, v112
	v_mov_b32_e32 v43, v126
	v_add_u32_e32 v29, 0x3c00, v34
	v_mov_b32_e32 v47, v121
	v_mov_b32_e32 v48, v122
	v_mov_b32_e32 v49, v123
	v_mov_b32_e32 v50, v124
	v_mov_b32_e32 v51, v125
	v_mov_b32_e32 v46, v127
	v_pk_add_f32 v[26:27], v[16:17], v[20:21] op_sel:[0,1] op_sel_hi:[1,0] neg_hi:[0,1]
	v_pk_add_f32 v[16:17], v[16:17], v[20:21] op_sel:[0,1] op_sel_hi:[1,0] neg_lo:[0,1]
	v_pk_add_f32 v[20:21], v[44:45], v[32:33]
	v_pk_add_f32 v[28:29], v[44:45], v[32:33] neg_lo:[0,1] neg_hi:[0,1]
	v_pk_add_f32 v[24:25], v[14:15], v[30:31] op_sel:[0,1] op_sel_hi:[1,0] neg_hi:[0,1]
	v_pk_add_f32 v[14:15], v[14:15], v[30:31] op_sel:[0,1] op_sel_hi:[1,0] neg_lo:[0,1]
	v_pk_add_f32 v[30:31], v[20:21], v[26:27]
	v_pk_add_f32 v[20:21], v[26:27], v[20:21] neg_lo:[0,1] neg_hi:[0,1]
	v_pk_add_f32 v[26:27], v[16:17], v[28:29] op_sel:[0,1] op_sel_hi:[1,0] neg_hi:[0,1]
	v_pk_add_f32 v[16:17], v[16:17], v[28:29] op_sel:[0,1] op_sel_hi:[1,0] neg_lo:[0,1]
	v_pk_add_f32 v[28:29], v[18:19], v[54:55]
	v_pk_add_f32 v[44:45], v[22:23], v[56:57]
	s_mov_b32 s2, 0xff61b1e6
	v_pk_add_f32 v[18:19], v[18:19], v[54:55] neg_lo:[0,1] neg_hi:[0,1]
	v_pk_add_f32 v[54:55], v[22:23], v[56:57] neg_lo:[0,1] neg_hi:[0,1]
	v_pk_add_f32 v[32:33], v[28:29], v[44:45]
	v_pk_add_f32 v[22:23], v[28:29], v[44:45] neg_lo:[0,1] neg_hi:[0,1]
	v_max3_f32 v44, v10, s2, v12
	v_max3_f32 v44, v44, v30, v32
	v_max3_f32 v44, v44, v8, v24
	v_pk_add_f32 v[28:29], v[18:19], v[54:55] op_sel:[0,1] op_sel_hi:[1,0] neg_hi:[0,1]
	v_pk_add_f32 v[18:19], v[18:19], v[54:55] op_sel:[0,1] op_sel_hi:[1,0] neg_lo:[0,1]
	v_max3_f32 v45, -v11, s2, -v13
	v_max3_f32 v44, v44, v26, v28
	v_max3_f32 v44, v44, v4, v6
	v_max3_f32 v44, v44, v20, v22
	v_max3_f32 v44, v44, v2, v14
	v_max3_f32 v44, v44, v16, v18
	v_max3_f32 v45, v45, -v31, -v33
	v_max3_f32 v45, v45, -v9, -v25
	v_mov_b32_dpp v53, v44 quad_perm:[1,0,3,2] row_mask:0xf bank_mask:0xf
	v_max_f32_e32 v53, v53, v53
	v_max_f32_e32 v44, v44, v53
	v_mov_b32_e32 v53, 0
	v_max3_f32 v45, v45, -v27, -v29
	v_max3_f32 v45, v45, -v5, -v7
	v_mov_b32_dpp v53, v44 quad_perm:[2,3,0,1] row_mask:0xf bank_mask:0xf
	v_max_f32_e32 v53, v53, v53
	v_max_f32_e32 v44, v44, v53
	v_mov_b32_e32 v53, 0
	v_max3_f32 v45, v45, -v21, -v23
	v_max3_f32 v45, v45, -v3, -v15
	v_mov_b32_dpp v53, v44 row_half_mirror row_mask:0xf bank_mask:0xf
	v_max_f32_e32 v53, v53, v53
	v_max_f32_e32 v44, v44, v53
	v_mov_b32_e32 v53, 0
	v_max3_f32 v45, v45, -v17, -v19
	s_nop 0
	v_mov_b32_dpp v53, v44 row_mirror row_mask:0xf bank_mask:0xf
	v_max_f32_e32 v53, v53, v53
	v_max_f32_e32 v44, v44, v53
	s_nop 0
	v_readlane_b32 s5, v44, 0
	v_readlane_b32 s6, v44, 16
	v_readlane_b32 s7, v44, 32
	v_readlane_b32 s8, v44, 48
	v_mov_b32_e32 v44, 0
	s_nop 1
	v_mov_b32_dpp v44, v45 quad_perm:[1,0,3,2] row_mask:0xf bank_mask:0xf
	v_max_f32_e32 v44, v44, v44
	v_max_f32_e32 v44, v45, v44
	v_mov_b32_e32 v45, 0
	s_nop 1
	v_mov_b32_dpp v45, v44 quad_perm:[2,3,0,1] row_mask:0xf bank_mask:0xf
	v_max_f32_e32 v45, v45, v45
	v_max_f32_e32 v44, v44, v45
	v_mov_b32_e32 v45, 0
	s_nop 1
	v_mov_b32_dpp v45, v44 row_half_mirror row_mask:0xf bank_mask:0xf
	v_max_f32_e32 v45, v45, v45
	v_max_f32_e32 v44, v44, v45
	v_mov_b32_e32 v45, 0
	s_nop 1
	v_mov_b32_dpp v45, v44 row_mirror row_mask:0xf bank_mask:0xf
	v_max_f32_e32 v45, v45, v45
	v_max_f32_e32 v44, v44, v45
	v_and_b32_e32 v45, 63, v0
	v_readlane_b32 s9, v44, 0
	v_readlane_b32 s10, v44, 16
	v_readlane_b32 s11, v44, 32
	v_readlane_b32 s12, v44, 48
	v_ashrrev_i32_e32 v44, 6, v0
	v_cmp_eq_u32_e32 vcc, 0, v45
	v_lshlrev_b32_e32 v61, 3, v44
	s_and_saveexec_b64 s[2:3], vcc
	s_cbranch_execz .LBB1_10
	v_max_f32_e64 v44, s12, s12
	v_max_f32_e64 v45, s11, s11
	v_max_f32_e32 v44, v45, v44
	v_mov_b32_e32 v45, s10
	v_max3_f32 v45, s9, v45, v44
	v_max_f32_e64 v44, s8, s8
	v_max_f32_e64 v53, s7, s7
	v_max_f32_e32 v44, v53, v44
	v_mov_b32_e32 v53, s6
	v_max3_f32 v44, s5, v53, v44
	ds_write_b64 v61, v[44:45] offset:36864

.LBB1_12:
	s_or_b64 exec, exec, s[8:9]
	s_waitcnt vmcnt(7)
	v_and_b32_e32 v23, 0xffff, v52
	v_and_b32_e32 v52, 0xffff, v1
	v_mov_b32_e32 v1, 0
	v_and_b32_e32 v61, 0xffff, v36
	v_and_b32_e32 v62, 0xffff, v37
	v_and_b32_e32 v63, 0xffff, v38
	v_and_b32_e32 v64, 0xffff, v39
	v_and_b32_e32 v65, 0xffff, v40
	v_and_b32_e32 v66, 0xffff, v41
	v_and_b32_e32 v67, 0xffff, v42
	s_waitcnt vmcnt(6)
	v_and_b32_e32 v14, 0xffff, v43
	s_waitcnt lgkmcnt(0)
	s_barrier
	ds_read_b128 v[36:39], v1 offset:36896
	ds_read_b128 v[40:43], v1 offset:36912
	s_mov_b32 s5, 0
	s_lshl_b64 s[2:3], s[4:5], 16
	s_add_u32 s0, s0, s2
	s_waitcnt lgkmcnt(1)
	v_add_f32_e32 v16, v36, v38
	s_waitcnt lgkmcnt(0)
	v_add_f32_e32 v18, v40, v42
	s_addc_u32 s1, s1, s3
	s_lshl_b32 s2, s16, 1
	v_add_f32_e32 v16, v16, v18
	s_mov_b32 s4, 0x45800000
	s_add_u32 s0, s0, s2
	v_div_scale_f32 v18, s[2:3], v16, v16, s4
	v_rcp_f32_e32 v36, v18
	v_add_f32_e32 v37, v37, v39
	v_add_f32_e32 v38, v41, v43
	v_add_f32_e32 v37, v37, v38
	v_fma_f32 v38, -v18, v36, 1.0
	v_fmac_f32_e32 v36, v38, v36
	v_div_scale_f32 v38, vcc, s4, v16, s4
	v_mul_f32_e32 v39, v38, v36
	v_fma_f32 v40, -v18, v39, v38
	v_fmac_f32_e32 v39, v40, v36
	v_fma_f32 v18, -v18, v39, v38
	v_div_scale_f32 v38, s[2:3], v37, v37, s4
	v_rcp_f32_e32 v40, v38
	v_div_fmas_f32 v18, v18, v36, v39
	v_div_fixup_f32 v16, v18, v16, s4
	s_addc_u32 s1, s1, 0
	v_fma_f32 v18, -v38, v40, 1.0
	v_fmac_f32_e32 v40, v18, v40
	v_div_scale_f32 v18, vcc, s4, v37, s4
	v_mul_f32_e32 v36, v18, v40
	v_fma_f32 v39, -v38, v36, v18
	v_fmac_f32_e32 v36, v39, v40
	v_fma_f32 v18, -v38, v36, v18
	v_div_fmas_f32 v18, v18, v40, v36
	v_cvt_f32_fp8_e32 v36, v23
	v_cvt_f32_fp8_sdwa v23, v23 src0_sel:BYTE_1
	v_div_fixup_f32 v18, v18, v37, s4
	v_mul_f32_e32 v37, v16, v59
	v_mul_f32_e32 v36, v37, v36
	v_mul_f32_e32 v37, v18, v60
	v_mul_f32_e32 v23, v37, v23
	v_mov_b32_e32 v38, 0
	v_cvt_pk_fp8_f32 v38, v36, v23
	v_cvt_f32_fp8_e32 v23, v52
	v_cvt_f32_fp8_sdwa v36, v52 src0_sel:BYTE_1
	v_mul_f32_e32 v37, v16, v57
	v_cvt_pk_fp8_f32 v38, 0, 0 op_sel:[0,0,1]
	v_mul_f32_e32 v23, v37, v23
	v_mul_f32_e32 v37, v18, v58
	v_lshlrev_b32_e32 v0, 3, v0
	v_mul_f32_e32 v36, v37, v36
	v_mov_b32_e32 v39, v1
	v_cvt_pk_fp8_f32 v39, v23, v36
	v_lshl_add_u64 v[36:37], v[0:1], 1, s[0:1]
	v_cvt_f32_fp8_e32 v23, v61
	global_store_short v[36:37], v38, off
	v_cvt_f32_fp8_sdwa v38, v61 src0_sel:BYTE_1
	v_mul_f32_e32 v40, v16, v55
	v_mul_f32_e32 v23, v40, v23
	v_mul_f32_e32 v40, v18, v56
	v_cvt_pk_fp8_f32 v39, 0, 0 op_sel:[0,0,1]
	v_mul_f32_e32 v38, v40, v38
	v_mov_b32_e32 v40, v1
	v_cvt_pk_fp8_f32 v40, v23, v38
	v_cvt_f32_fp8_e32 v23, v62
	v_add_u32_e32 v36, 0x800, v0
	v_mov_b32_e32 v37, v1
	v_cvt_f32_fp8_sdwa v38, v62 src0_sel:BYTE_1
	v_lshl_add_u64 v[36:37], v[36:37], 1, s[0:1]
	global_store_short v[36:37], v39, off
	v_mul_f32_e32 v39, v16, v53
	v_mul_f32_e32 v23, v39, v23
	v_mul_f32_e32 v39, v18, v54
	v_cvt_pk_fp8_f32 v40, 0, 0 op_sel:[0,0,1]
	v_mul_f32_e32 v38, v39, v38
	v_mov_b32_e32 v39, v1
	v_cvt_pk_fp8_f32 v39, v23, v38
	v_cvt_f32_fp8_e32 v23, v63
	v_add_u32_e32 v36, 0x1000, v0
	v_mov_b32_e32 v37, v1
	v_cvt_f32_fp8_sdwa v38, v63 src0_sel:BYTE_1
	v_lshl_add_u64 v[36:37], v[36:37], 1, s[0:1]
	global_store_short v[36:37], v40, off
	v_mul_f32_e32 v40, v16, v44
	v_mul_f32_e32 v23, v40, v23
	v_mul_f32_e32 v40, v18, v45
	v_mul_f32_e32 v38, v40, v38
	v_mov_b32_e32 v40, v1
	v_cvt_pk_fp8_f32 v40, v23, v38
	v_cvt_f32_fp8_e32 v23, v64
	v_cvt_f32_fp8_sdwa v38, v64 src0_sel:BYTE_1
	v_cvt_pk_fp8_f32 v39, 0, 0 op_sel:[0,0,1]
	v_mul_f32_e32 v32, v16, v32
	v_add_u32_e32 v36, 0x1800, v0
	v_mov_b32_e32 v37, v1
	v_mul_f32_e32 v23, v32, v23
	v_mul_f32_e32 v32, v18, v33
	v_lshl_add_u64 v[36:37], v[36:37], 1, s[0:1]
	v_mul_f32_e32 v32, v32, v38
	v_mov_b32_e32 v38, v1
	global_store_short v[36:37], v39, off
	v_add_u32_e32 v36, 0x2000, v0
	v_mov_b32_e32 v37, v1
	v_cvt_pk_fp8_f32 v38, v23, v32
	v_cvt_f32_fp8_e32 v23, v65
	v_lshl_add_u64 v[32:33], v[36:37], 1, s[0:1]
	v_cvt_f32_fp8_sdwa v36, v65 src0_sel:BYTE_1
	v_cvt_pk_fp8_f32 v40, 0, 0 op_sel:[0,0,1]
	v_mul_f32_e32 v30, v16, v30
	v_mul_f32_e32 v23, v30, v23
	v_mul_f32_e32 v30, v18, v31
	v_mul_f32_e32 v30, v30, v36
	v_mov_b32_e32 v36, v1
	global_store_short v[32:33], v40, off
	v_add_u32_e32 v32, 0x2800, v0
	v_mov_b32_e32 v33, v1
	v_cvt_pk_fp8_f32 v36, v23, v30
	v_cvt_f32_fp8_e32 v23, v66
	v_lshl_add_u64 v[30:31], v[32:33], 1, s[0:1]
	v_cvt_f32_fp8_sdwa v32, v66 src0_sel:BYTE_1
	v_cvt_pk_fp8_f32 v38, 0, 0 op_sel:[0,0,1]
	v_mul_f32_e32 v28, v16, v28
	v_mul_f32_e32 v23, v28, v23
	v_mul_f32_e32 v28, v18, v29
	v_mul_f32_e32 v28, v28, v32
	v_mov_b32_e32 v32, v1
	global_store_short v[30:31], v38, off
	v_add_u32_e32 v30, 0x3000, v0
	v_mov_b32_e32 v31, v1
	v_cvt_pk_fp8_f32 v32, v23, v28
	v_cvt_f32_fp8_e32 v23, v67
	v_lshl_add_u64 v[28:29], v[30:31], 1, s[0:1]
	v_cvt_f32_fp8_sdwa v30, v67 src0_sel:BYTE_1
	v_mul_f32_e32 v26, v16, v26
	v_mul_f32_e32 v23, v26, v23
	v_mul_f32_e32 v26, v18, v27
	s_waitcnt vmcnt(11)
	v_and_b32_e32 v22, 0xffff, v47
	v_mul_f32_e32 v26, v26, v30
	v_mov_b32_e32 v30, v1
	v_cvt_pk_fp8_f32 v30, v23, v26
	v_cvt_f32_fp8_e32 v23, v22
	s_waitcnt vmcnt(10)
	v_and_b32_e32 v21, 0xffff, v48
	v_mul_f32_e32 v24, v16, v24
	v_cvt_f32_fp8_sdwa v22, v22 src0_sel:BYTE_1
	v_mul_f32_e32 v23, v24, v23
	v_mul_f32_e32 v24, v18, v25
	v_cvt_f32_fp8_e32 v25, v21
	v_cvt_f32_fp8_sdwa v21, v21 src0_sel:BYTE_1
	v_mul_f32_e32 v13, v16, v13
	v_mul_f32_e32 v20, v18, v20
	s_waitcnt vmcnt(9)
	v_and_b32_e32 v19, 0xffff, v49
	v_cvt_pk_fp8_f32 v36, 0, 0 op_sel:[0,0,1]
	v_mul_f32_e32 v13, v13, v25
	v_mul_f32_e32 v20, v20, v21
	v_mov_b32_e32 v25, v1
	v_mul_f32_e32 v22, v24, v22
	v_mov_b32_e32 v24, v1
	v_cvt_pk_fp8_f32 v25, v13, v20
	v_cvt_f32_fp8_e32 v13, v19
	v_cvt_f32_fp8_sdwa v19, v19 src0_sel:BYTE_1
	v_cvt_pk_fp8_f32 v32, 0, 0 op_sel:[0,0,1]
	v_cvt_pk_fp8_f32 v24, v23, v22
	global_store_short v[28:29], v36, off
	v_add_u32_e32 v28, v35, v34
	v_mov_b32_e32 v29, v1
	v_cvt_pk_fp8_f32 v30, 0, 0 op_sel:[0,0,1]
	v_mul_f32_e32 v10, v16, v10
	v_mul_f32_e32 v11, v18, v11
	v_lshl_add_u64 v[26:27], v[28:29], 1, s[0:1]
	v_mul_f32_e32 v10, v10, v13
	v_mul_f32_e32 v11, v11, v19
	v_mov_b32_e32 v13, v1
	global_store_short v[26:27], v32, off
	v_add_u32_e32 v26, 0x4000, v0
	v_mov_b32_e32 v27, v1
	v_cvt_pk_fp8_f32 v24, 0, 0 op_sel:[0,0,1]
	v_cvt_pk_fp8_f32 v13, v10, v11
	v_lshl_add_u64 v[22:23], v[26:27], 1, s[0:1]
	s_waitcnt vmcnt(10)
	v_and_b32_e32 v17, 0xffff, v50
	global_store_short v[22:23], v30, off
	v_add_u32_e32 v22, 0x4800, v0
	v_mov_b32_e32 v23, v1
	v_cvt_pk_fp8_f32 v25, 0, 0 op_sel:[0,0,1]
	v_lshl_add_u64 v[20:21], v[22:23], 1, s[0:1]
	v_cvt_f32_fp8_e32 v19, v17
	v_cvt_f32_fp8_sdwa v17, v17 src0_sel:BYTE_1
	global_store_short v[20:21], v24, off
	v_add_u32_e32 v20, 0x5000, v0
	v_mov_b32_e32 v21, v1
	v_cvt_pk_fp8_f32 v13, 0, 0 op_sel:[0,0,1]
	v_lshl_add_u64 v[10:11], v[20:21], 1, s[0:1]
	global_store_short v[10:11], v25, off
	v_add_u32_e32 v10, 0x5800, v0
	v_mov_b32_e32 v11, v1
	v_mul_f32_e32 v8, v16, v8
	v_mul_f32_e32 v9, v18, v9
	s_waitcnt vmcnt(12)
	v_and_b32_e32 v15, 0xffff, v51
	v_lshl_add_u64 v[10:11], v[10:11], 1, s[0:1]
	v_mul_f32_e32 v8, v8, v19
	v_mul_f32_e32 v9, v9, v17
	v_mov_b32_e32 v17, v1
	v_cvt_pk_fp8_f32 v17, v8, v9
	global_store_short v[10:11], v13, off
	v_cvt_f32_fp8_e32 v9, v15
	v_cvt_f32_fp8_sdwa v10, v15 src0_sel:BYTE_1
	v_mul_f32_e32 v6, v16, v6
	v_mul_f32_e32 v7, v18, v7
	v_mul_f32_e32 v6, v6, v9
	v_mul_f32_e32 v7, v7, v10
	v_mov_b32_e32 v10, v1
	v_cvt_pk_fp8_f32 v10, v6, v7
	v_cvt_pk_fp8_f32 v17, 0, 0 op_sel:[0,0,1]
	v_add_u32_e32 v8, 0x6000, v0
	v_mov_b32_e32 v9, v1
	v_cvt_pk_fp8_f32 v10, 0, 0 op_sel:[0,0,1]
	v_lshl_add_u64 v[6:7], v[8:9], 1, s[0:1]
	global_store_short v[6:7], v17, off
	v_add_u32_e32 v6, 0x6800, v0
	v_mov_b32_e32 v7, v1
	v_lshl_add_u64 v[6:7], v[6:7], 1, s[0:1]
	global_store_short v[6:7], v10, off
	v_cvt_f32_fp8_e32 v7, v14
	v_cvt_f32_fp8_sdwa v8, v14 src0_sel:BYTE_1
	v_mul_f32_e32 v4, v16, v4
	v_mul_f32_e32 v5, v18, v5
	s_waitcnt vmcnt(14)
	v_and_b32_e32 v12, 0xffff, v46
	v_mul_f32_e32 v4, v4, v7
	v_mul_f32_e32 v5, v5, v8
	v_mov_b32_e32 v8, v1
	v_cvt_f32_fp8_e32 v7, v12
	v_cvt_pk_fp8_f32 v8, v4, v5
	v_cvt_f32_fp8_sdwa v4, v12 src0_sel:BYTE_1
	v_mul_f32_e32 v2, v16, v2
	v_mul_f32_e32 v3, v18, v3
	v_mul_f32_e32 v2, v2, v7
	v_mul_f32_e32 v3, v3, v4
	v_mov_b32_e32 v4, v1
	v_cvt_pk_fp8_f32 v4, v2, v3
	v_cvt_pk_fp8_f32 v8, 0, 0 op_sel:[0,0,1]
	v_add_u32_e32 v6, 0x7000, v0
	v_mov_b32_e32 v7, v1
	v_cvt_pk_fp8_f32 v4, 0, 0 op_sel:[0,0,1]
	v_add_u32_e32 v0, 0x7800, v0
	v_lshl_add_u64 v[2:3], v[6:7], 1, s[0:1]
	v_lshl_add_u64 v[0:1], v[0:1], 1, s[0:1]
	global_store_short v[2:3], v8, off
	global_store_short v[0:1], v4, off
	s_endpgm
	s_nop 0
	s_nop 0
	s_nop 0
	s_nop 0
	s_nop 0
	s_nop 0
	s_nop 0
	s_nop 0
	s_nop 0
	s_nop 0
	s_nop 0
	s_nop 0
	s_nop 0
	s_nop 0
	s_nop 0
	s_nop 0
	s_nop 0
	s_nop 0
	s_nop 0
	s_nop 0
	s_nop 0
	s_nop 0
	s_nop 0
	s_nop 0
	s_nop 0
	s_nop 0
	s_nop 0
	s_nop 0
	s_nop 0
	s_nop 0
	s_nop 0
	s_endpgm
